# v4
# speedup vs baseline: 1.0709x; 1.0246x over previous
.LBB1_9:
	s_waitcnt lgkmcnt(0)
	v_fma_f32 v2, s18, v1, v127
	v_fma_f32 v3, s22, v1, v128
	v_cndmask_b32_e64 v4, v3, v2, s[4:5]
	v_cndmask_b32_e64 v2, v3, v2, s[6:7]
	v_mul_f32_e32 v8, v2, v142
	v_mul_f32_e32 v2, v2, v143
	v_mul_f32_e32 v5, v4, v140
	v_mul_f32_e32 v4, v4, v141
	v_fract_f32_e32 v2, v2
	v_fract_f32_e32 v4, v4
	v_sin_f32_e32 v10, v2
	v_cos_f32_e32 v2, v2
	v_sin_f32_e32 v7, v4
	v_cos_f32_e32 v4, v4
	v_fma_f32 v1, s26, v1, v129
	v_fract_f32_e32 v5, v5
	v_sin_f32_e32 v6, v5
	v_cos_f32_e32 v5, v5
	v_cndmask_b32_e64 v1, v1, v3, s[2:3]
	v_cvt_pk_bf16_f32 v53, v10, v2
	v_mul_f32_e32 v2, v1, v144
	v_cvt_pk_bf16_f32 v51, v7, v4
	v_fract_f32_e32 v2, v2
	v_mul_f32_e32 v4, v1, v145
	v_sin_f32_e32 v3, v2
	v_cos_f32_e32 v2, v2
	v_fract_f32_e32 v4, v4
	v_cvt_pk_bf16_f32 v50, v6, v5
	v_sin_f32_e32 v5, v4
	v_cos_f32_e32 v4, v4
	v_mul_f32_e32 v6, v1, v146
	v_fract_f32_e32 v6, v6
	v_mul_f32_e32 v1, v1, v147
	v_cos_f32_e32 v7, v6
	v_cvt_pk_bf16_f32 v56, v3, v2
	v_sin_f32_e32 v2, v6
	v_fract_f32_e32 v1, v1
	v_cvt_pk_bf16_f32 v57, v5, v4
	v_cos_f32_e32 v4, v1
	v_sin_f32_e32 v1, v1
	v_cndmask_b32_e64 v3, v7, 0, s[0:1]
	v_cndmask_b32_e64 v2, v2, 1.0, s[0:1]
	v_fract_f32_e32 v8, v8
	v_cvt_pk_bf16_f32 v58, v2, v3
	v_cndmask_b32_e64 v2, v4, 0, s[0:1]
	v_cndmask_b32_e64 v1, v1, 0, s[0:1]
	v_sin_f32_e32 v9, v8
	v_cos_f32_e32 v8, v8
	v_cvt_pk_bf16_f32 v59, v1, v2
	v_fma_f32 v1, s18, v0, v127
	v_fma_f32 v2, s22, v0, v128
	v_cndmask_b32_e64 v3, v2, v1, s[4:5]
	v_cndmask_b32_e64 v1, v2, v1, s[6:7]
	v_mul_f32_e32 v7, v1, v142
	v_mul_f32_e32 v1, v1, v143
	v_mul_f32_e32 v4, v3, v140
	v_mul_f32_e32 v3, v3, v141
	v_fract_f32_e32 v1, v1
	v_cvt_pk_bf16_f32 v52, v9, v8
	v_fract_f32_e32 v3, v3
	v_sin_f32_e32 v9, v1
	v_cos_f32_e32 v1, v1
	v_sin_f32_e32 v6, v3
	v_cos_f32_e32 v3, v3
	v_fma_f32 v0, s26, v0, v129
	v_fract_f32_e32 v4, v4
	v_sin_f32_e32 v5, v4
	v_cos_f32_e32 v4, v4
	v_cndmask_b32_e64 v0, v0, v2, s[2:3]
	v_cvt_pk_bf16_f32 v63, v9, v1
	v_mul_f32_e32 v1, v0, v144
	v_cvt_pk_bf16_f32 v61, v6, v3
	v_fract_f32_e32 v1, v1
	v_mul_f32_e32 v3, v0, v145
	v_sin_f32_e32 v2, v1
	v_cos_f32_e32 v1, v1
	v_fract_f32_e32 v3, v3
	v_cvt_pk_bf16_f32 v60, v5, v4
	v_sin_f32_e32 v4, v3
	v_cos_f32_e32 v3, v3
	v_mul_f32_e32 v5, v0, v146
	v_fract_f32_e32 v5, v5
	v_mul_f32_e32 v0, v0, v147
	v_fract_f32_e32 v7, v7
	v_cos_f32_e32 v6, v5
	v_cvt_pk_bf16_f32 v72, v2, v1
	v_sin_f32_e32 v1, v5
	v_fract_f32_e32 v0, v0
	v_sin_f32_e32 v8, v7
	v_cos_f32_e32 v7, v7
	v_cvt_pk_bf16_f32 v73, v4, v3
	v_cos_f32_e32 v3, v0
	v_cndmask_b32_e64 v2, v6, 0, s[0:1]
	v_cndmask_b32_e64 v1, v1, 1.0, s[0:1]
	v_cvt_pk_bf16_f32 v62, v8, v7
	v_cvt_pk_bf16_f32 v74, v1, v2
	v_sin_f32_e32 v16, v0
	v_cndmask_b32_e64 v17, v3, 0, s[0:1]
	v_cndmask_b32_e64 v16, v16, 0, s[0:1]
	v_cvt_pk_bf16_f32 v75, v16, v17
	v_mov_b32_e32 v183, v131
	s_mov_b32 s50, 0x10000
	s_mov_b32 s52, 0
	s_waitcnt vmcnt(0) lgkmcnt(0)
	s_barrier
	ds_read_b128 v[224:227], v148 offset:0
	ds_read_b128 v[228:231], v148 offset:1024
	ds_read_b128 v[232:235], v148 offset:2048
	ds_read_b128 v[236:239], v148 offset:3072
	ds_read_b128 v[240:243], v148 offset:4096
	ds_read_b128 v[244:247], v148 offset:5120
	ds_read_b128 v[248:251], v148 offset:6144
	ds_read_b128 v[252:255], v148 offset:7168
	v_mov_b32_e32 v208, v50
	v_mov_b32_e32 v209, v51
	v_mov_b32_e32 v210, v52
	v_mov_b32_e32 v211, v53
	v_mov_b32_e32 v212, v60
	v_mov_b32_e32 v213, v61
	v_mov_b32_e32 v214, v62
	v_mov_b32_e32 v215, v63
	v_mov_b32_e32 v216, v56
	v_mov_b32_e32 v217, v57
	v_mov_b32_e32 v218, v58
	v_mov_b32_e32 v219, v59
	v_mov_b32_e32 v220, v72
	v_mov_b32_e32 v221, v73
	v_mov_b32_e32 v222, v74
	v_mov_b32_e32 v223, v75
	s_waitcnt lgkmcnt(7)
	v_mfma_f32_16x16x32_bf16 v[64:67], v[224:227], v[208:211], 0
	v_mfma_f32_16x16x32_bf16 v[56:59], v[224:227], v[212:215], 0
	ds_read_b128 v[224:227], v148 offset:8192
	s_waitcnt lgkmcnt(7)
	v_mfma_f32_16x16x32_bf16 v[68:71], v[228:231], v[208:211], 0
	v_mfma_f32_16x16x32_bf16 v[60:63], v[228:231], v[212:215], 0
	ds_read_b128 v[228:231], v148 offset:9216
	s_waitcnt lgkmcnt(7)
	v_mfma_f32_16x16x32_bf16 v[64:67], v[232:235], v[216:219], v[64:67]
	v_mfma_f32_16x16x32_bf16 v[56:59], v[232:235], v[220:223], v[56:59]
	ds_read_b128 v[232:235], v148 offset:10240
	s_waitcnt lgkmcnt(7)
	v_mfma_f32_16x16x32_bf16 v[68:71], v[236:239], v[216:219], v[68:71]
	v_mfma_f32_16x16x32_bf16 v[60:63], v[236:239], v[220:223], v[60:63]
	ds_read_b128 v[236:239], v148 offset:11264
	s_waitcnt lgkmcnt(7)
	v_mfma_f32_16x16x32_bf16 v[80:83], v[240:243], v[208:211], 0
	v_cvt_pk_bf16_f32 v0, v64, v65
	v_cvt_pk_bf16_f32 v1, v66, v67
	v_mfma_f32_16x16x32_bf16 v[84:87], v[240:243], v[212:215], 0
	v_cvt_pk_bf16_f32 v4, v56, v57
	v_cvt_pk_bf16_f32 v5, v58, v59
	ds_read_b128 v[240:243], v148 offset:12288
	s_waitcnt lgkmcnt(7)
	v_mfma_f32_16x16x32_bf16 v[76:79], v[244:247], v[208:211], 0
	v_cvt_pk_bf16_f32 v2, v68, v69
	v_cvt_pk_bf16_f32 v3, v70, v71
	s_mov_b32 m0, s28
	s_mov_b32 s51, 0x8000
	v_mfma_f32_16x16x32_bf16 v[72:75], v[244:247], v[212:215], 0
	v_cvt_pk_bf16_f32 v6, v60, v61
	v_cvt_pk_bf16_f32 v7, v62, v63
	buffer_load_dwordx4 v125, s[36:39], s51 offen lds
	ds_read_b128 v[244:247], v148 offset:13312
	s_waitcnt lgkmcnt(7)
	v_mfma_f32_16x16x32_bf16 v[80:83], v[248:251], v[216:219], v[80:83]
	v_pk_max_i16 v0, v0, 0
	v_pk_max_i16 v1, v1, 0
	v_mfma_f32_16x16x32_bf16 v[84:87], v[248:251], v[220:223], v[84:87]
	v_pk_max_i16 v2, v2, 0
	v_pk_max_i16 v3, v3, 0
	ds_read_b128 v[248:251], v148 offset:14336
	s_waitcnt lgkmcnt(7)
	v_mfma_f32_16x16x32_bf16 v[76:79], v[252:255], v[216:219], v[76:79]
	v_pk_max_i16 v4, v4, 0
	v_pk_max_i16 v5, v5, 0
	v_mfma_f32_16x16x32_bf16 v[72:75], v[252:255], v[220:223], v[72:75]
	v_pk_max_i16 v6, v6, 0
	v_pk_max_i16 v7, v7, 0
	ds_read_b128 v[252:255], v148 offset:15360
	s_waitcnt lgkmcnt(7)
	v_mfma_f32_16x16x32_bf16 v[64:67], v[224:227], v[208:211], 0
	v_cvt_pk_bf16_f32 v12, v80, v81
	v_cvt_pk_bf16_f32 v13, v82, v83
	v_mfma_f32_16x16x32_bf16 v[56:59], v[224:227], v[212:215], 0
	v_cvt_pk_bf16_f32 v8, v84, v85
	v_cvt_pk_bf16_f32 v9, v86, v87
	ds_read_b128 v[224:227], v148 offset:16384
	s_waitcnt lgkmcnt(7)
	v_mfma_f32_16x16x32_bf16 v[68:71], v[228:231], v[208:211], 0
	v_cvt_pk_bf16_f32 v14, v76, v77
	v_cvt_pk_bf16_f32 v15, v78, v79
	s_mov_b32 m0, s29
	s_mov_b32 s51, 0xa000
	v_mfma_f32_16x16x32_bf16 v[60:63], v[228:231], v[212:215], 0
	v_cvt_pk_bf16_f32 v10, v72, v73
	v_cvt_pk_bf16_f32 v11, v74, v75
	buffer_load_dwordx4 v125, s[36:39], s51 offen lds
	ds_read_b128 v[228:231], v148 offset:17408
	s_waitcnt lgkmcnt(7)
	v_mfma_f32_16x16x32_bf16 v[64:67], v[232:235], v[216:219], v[64:67]
	v_pk_max_i16 v12, v12, 0
	v_pk_max_i16 v13, v13, 0
	v_mfma_f32_16x16x32_bf16 v[56:59], v[232:235], v[220:223], v[56:59]
	v_pk_max_i16 v14, v14, 0
	v_pk_max_i16 v15, v15, 0
	ds_read_b128 v[232:235], v148 offset:18432
	s_waitcnt lgkmcnt(7)
	v_mfma_f32_16x16x32_bf16 v[68:71], v[236:239], v[216:219], v[68:71]
	v_pk_max_i16 v8, v8, 0
	v_pk_max_i16 v9, v9, 0
	v_mfma_f32_16x16x32_bf16 v[60:63], v[236:239], v[220:223], v[60:63]
	v_pk_max_i16 v10, v10, 0
	v_pk_max_i16 v11, v11, 0
	ds_read_b128 v[236:239], v148 offset:19456
	s_waitcnt lgkmcnt(7)
	v_mfma_f32_16x16x32_bf16 v[80:83], v[240:243], v[208:211], 0
	v_cvt_pk_bf16_f32 v16, v64, v65
	v_cvt_pk_bf16_f32 v17, v66, v67
	v_mfma_f32_16x16x32_bf16 v[84:87], v[240:243], v[212:215], 0
	v_cvt_pk_bf16_f32 v20, v56, v57
	v_cvt_pk_bf16_f32 v21, v58, v59
	ds_read_b128 v[240:243], v148 offset:20480
	s_waitcnt lgkmcnt(7)
	v_mfma_f32_16x16x32_bf16 v[76:79], v[244:247], v[208:211], 0
	v_cvt_pk_bf16_f32 v18, v68, v69
	v_cvt_pk_bf16_f32 v19, v70, v71
	s_mov_b32 m0, s33
	s_mov_b32 s51, 0xc000
	v_mfma_f32_16x16x32_bf16 v[72:75], v[244:247], v[212:215], 0
	v_cvt_pk_bf16_f32 v22, v60, v61
	v_cvt_pk_bf16_f32 v23, v62, v63
	buffer_load_dwordx4 v125, s[36:39], s51 offen lds
	ds_read_b128 v[244:247], v148 offset:21504
	s_waitcnt lgkmcnt(7)
	v_mfma_f32_16x16x32_bf16 v[80:83], v[248:251], v[216:219], v[80:83]
	v_pk_max_i16 v16, v16, 0
	v_pk_max_i16 v17, v17, 0
	v_mfma_f32_16x16x32_bf16 v[84:87], v[248:251], v[220:223], v[84:87]
	v_pk_max_i16 v18, v18, 0
	v_pk_max_i16 v19, v19, 0
	ds_read_b128 v[248:251], v148 offset:22528
	s_waitcnt lgkmcnt(7)
	v_mfma_f32_16x16x32_bf16 v[76:79], v[252:255], v[216:219], v[76:79]
	v_pk_max_i16 v20, v20, 0
	v_pk_max_i16 v21, v21, 0
	v_mfma_f32_16x16x32_bf16 v[72:75], v[252:255], v[220:223], v[72:75]
	v_pk_max_i16 v22, v22, 0
	v_pk_max_i16 v23, v23, 0
	ds_read_b128 v[252:255], v148 offset:23552
	s_waitcnt lgkmcnt(7)
	v_mfma_f32_16x16x32_bf16 v[64:67], v[224:227], v[208:211], 0
	v_cvt_pk_bf16_f32 v24, v80, v81
	v_cvt_pk_bf16_f32 v25, v82, v83
	v_mfma_f32_16x16x32_bf16 v[56:59], v[224:227], v[212:215], 0
	v_cvt_pk_bf16_f32 v28, v84, v85
	v_cvt_pk_bf16_f32 v29, v86, v87
	ds_read_b128 v[224:227], v148 offset:24576
	s_waitcnt lgkmcnt(7)
	v_mfma_f32_16x16x32_bf16 v[68:71], v[228:231], v[208:211], 0
	v_cvt_pk_bf16_f32 v26, v76, v77
	v_cvt_pk_bf16_f32 v27, v78, v79
	s_mov_b32 m0, s34
	s_mov_b32 s51, 0xe000
	v_mfma_f32_16x16x32_bf16 v[60:63], v[228:231], v[212:215], 0
	v_cvt_pk_bf16_f32 v30, v72, v73
	v_cvt_pk_bf16_f32 v31, v74, v75
	buffer_load_dwordx4 v125, s[36:39], s51 offen lds
	ds_read_b128 v[228:231], v148 offset:25600
	s_waitcnt lgkmcnt(7)
	v_mfma_f32_16x16x32_bf16 v[64:67], v[232:235], v[216:219], v[64:67]
	v_pk_max_i16 v24, v24, 0
	v_pk_max_i16 v25, v25, 0
	v_mfma_f32_16x16x32_bf16 v[56:59], v[232:235], v[220:223], v[56:59]
	v_pk_max_i16 v26, v26, 0
	v_pk_max_i16 v27, v27, 0
	ds_read_b128 v[232:235], v148 offset:26624
	s_waitcnt lgkmcnt(7)
	v_mfma_f32_16x16x32_bf16 v[68:71], v[236:239], v[216:219], v[68:71]
	v_pk_max_i16 v28, v28, 0
	v_pk_max_i16 v29, v29, 0
	v_mfma_f32_16x16x32_bf16 v[60:63], v[236:239], v[220:223], v[60:63]
	v_pk_max_i16 v30, v30, 0
	v_pk_max_i16 v31, v31, 0
	ds_read_b128 v[236:239], v148 offset:27648
	s_waitcnt lgkmcnt(7)
	v_mfma_f32_16x16x32_bf16 v[80:83], v[240:243], v[208:211], 0
	v_cvt_pk_bf16_f32 v32, v64, v65
	v_cvt_pk_bf16_f32 v33, v66, v67
	v_mfma_f32_16x16x32_bf16 v[84:87], v[240:243], v[212:215], 0
	v_cvt_pk_bf16_f32 v36, v56, v57
	v_cvt_pk_bf16_f32 v37, v58, v59
	ds_read_b128 v[240:243], v148 offset:28672
	s_waitcnt lgkmcnt(7)
	v_mfma_f32_16x16x32_bf16 v[76:79], v[244:247], v[208:211], 0
	v_cvt_pk_bf16_f32 v34, v68, v69
	v_cvt_pk_bf16_f32 v35, v70, v71
	v_mfma_f32_16x16x32_bf16 v[72:75], v[244:247], v[212:215], 0
	v_cvt_pk_bf16_f32 v38, v60, v61
	v_cvt_pk_bf16_f32 v39, v62, v63
	ds_read_b128 v[244:247], v148 offset:29696
	s_waitcnt lgkmcnt(7)
	v_mfma_f32_16x16x32_bf16 v[80:83], v[248:251], v[216:219], v[80:83]
	v_pk_max_i16 v32, v32, 0
	v_pk_max_i16 v33, v33, 0
	v_mfma_f32_16x16x32_bf16 v[84:87], v[248:251], v[220:223], v[84:87]
	v_pk_max_i16 v34, v34, 0
	v_pk_max_i16 v35, v35, 0
	ds_read_b128 v[248:251], v148 offset:30720
	s_waitcnt lgkmcnt(7)
	v_mfma_f32_16x16x32_bf16 v[76:79], v[252:255], v[216:219], v[76:79]
	v_pk_max_i16 v36, v36, 0
	v_pk_max_i16 v37, v37, 0
	v_mfma_f32_16x16x32_bf16 v[72:75], v[252:255], v[220:223], v[72:75]
	v_pk_max_i16 v38, v38, 0
	v_pk_max_i16 v39, v39, 0
	ds_read_b128 v[252:255], v148 offset:31744
	s_waitcnt lgkmcnt(7)
	v_mfma_f32_16x16x32_bf16 v[64:67], v[224:227], v[208:211], 0
	v_cvt_pk_bf16_f32 v40, v80, v81
	v_cvt_pk_bf16_f32 v41, v82, v83
	v_mfma_f32_16x16x32_bf16 v[56:59], v[224:227], v[212:215], 0
	v_cvt_pk_bf16_f32 v44, v84, v85
	v_cvt_pk_bf16_f32 v45, v86, v87
	s_waitcnt lgkmcnt(6)
	v_mfma_f32_16x16x32_bf16 v[68:71], v[228:231], v[208:211], 0
	v_cvt_pk_bf16_f32 v42, v76, v77
	v_cvt_pk_bf16_f32 v43, v78, v79
	v_mfma_f32_16x16x32_bf16 v[60:63], v[228:231], v[212:215], 0
	v_cvt_pk_bf16_f32 v46, v72, v73
	v_cvt_pk_bf16_f32 v47, v74, v75
	s_waitcnt lgkmcnt(5)
	v_mfma_f32_16x16x32_bf16 v[64:67], v[232:235], v[216:219], v[64:67]
	v_pk_max_i16 v40, v40, 0
	v_pk_max_i16 v41, v41, 0
	v_mfma_f32_16x16x32_bf16 v[56:59], v[232:235], v[220:223], v[56:59]
	v_pk_max_i16 v42, v42, 0
	v_pk_max_i16 v43, v43, 0
	s_waitcnt lgkmcnt(4)
	v_mfma_f32_16x16x32_bf16 v[68:71], v[236:239], v[216:219], v[68:71]
	v_pk_max_i16 v44, v44, 0
	v_pk_max_i16 v45, v45, 0
	v_mfma_f32_16x16x32_bf16 v[60:63], v[236:239], v[220:223], v[60:63]
	v_pk_max_i16 v46, v46, 0
	v_pk_max_i16 v47, v47, 0
	s_waitcnt lgkmcnt(3)
	v_mfma_f32_16x16x32_bf16 v[80:83], v[240:243], v[208:211], 0
	v_cvt_pk_bf16_f32 v48, v64, v65
	v_cvt_pk_bf16_f32 v49, v66, v67
	v_mfma_f32_16x16x32_bf16 v[84:87], v[240:243], v[212:215], 0
	v_cvt_pk_bf16_f32 v52, v56, v57
	v_cvt_pk_bf16_f32 v53, v58, v59
	s_waitcnt lgkmcnt(2)
	v_mfma_f32_16x16x32_bf16 v[76:79], v[244:247], v[208:211], 0
	v_cvt_pk_bf16_f32 v50, v68, v69
	v_cvt_pk_bf16_f32 v51, v70, v71
	v_mfma_f32_16x16x32_bf16 v[72:75], v[244:247], v[212:215], 0
	v_cvt_pk_bf16_f32 v54, v60, v61
	v_cvt_pk_bf16_f32 v55, v62, v63
	s_waitcnt lgkmcnt(1)
	v_mfma_f32_16x16x32_bf16 v[80:83], v[248:251], v[216:219], v[80:83]
	v_pk_max_i16 v48, v48, 0
	v_pk_max_i16 v49, v49, 0
	v_mfma_f32_16x16x32_bf16 v[84:87], v[248:251], v[220:223], v[84:87]
	v_pk_max_i16 v50, v50, 0
	v_pk_max_i16 v51, v51, 0
	s_waitcnt lgkmcnt(0)
	v_mfma_f32_16x16x32_bf16 v[76:79], v[252:255], v[216:219], v[76:79]
	v_pk_max_i16 v52, v52, 0
	v_pk_max_i16 v53, v53, 0
	v_mfma_f32_16x16x32_bf16 v[72:75], v[252:255], v[220:223], v[72:75]
	v_pk_max_i16 v54, v54, 0
	v_pk_max_i16 v55, v55, 0
	s_cmp_lt_u32 s31, 2
	s_cbranch_scc0 .Lnerf_hid_b_first
	s_waitcnt vmcnt(0) lgkmcnt(0)
	s_barrier
	ds_read_b128 v[224:227], v121 offset:40960
	ds_read_b128 v[228:231], v121 offset:41984
	ds_read_b128 v[152:155], v183 offset:0
	ds_read_b128 v[156:159], v183 offset:64
	ds_read_b128 v[232:235], v121 offset:43008
	ds_read_b128 v[236:239], v121 offset:44032
	ds_read_b128 v[240:243], v121 offset:45056
	ds_read_b128 v[244:247], v121 offset:46080
	ds_read_b128 v[248:251], v121 offset:47104
	ds_read_b128 v[252:255], v121 offset:48128
	s_setprio 3
	s_waitcnt lgkmcnt(6)
	v_mfma_f32_16x16x32_bf16 v[64:67], v[224:227], v[0:3], v[152:155]
	v_cvt_pk_bf16_f32 v112, v80, v81
	v_mfma_f32_16x16x32_bf16 v[68:71], v[228:231], v[0:3], v[156:159]
	v_cvt_pk_bf16_f32 v113, v82, v83
	v_mfma_f32_16x16x32_bf16 v[60:63], v[228:231], v[4:7], v[156:159]
	v_cvt_pk_bf16_f32 v114, v76, v77
	v_mfma_f32_16x16x32_bf16 v[56:59], v[224:227], v[4:7], v[152:155]
	v_cvt_pk_bf16_f32 v115, v78, v79
	ds_read_b128 v[224:227], v121 offset:49152
	ds_read_b128 v[228:231], v121 offset:50176
	s_waitcnt lgkmcnt(6)
	ds_read_b128 v[160:163], v183 offset:128
	ds_read_b128 v[164:167], v183 offset:192
	v_mfma_f32_16x16x32_bf16 v[64:67], v[232:235], v[12:15], v[64:67]
	v_cvt_pk_bf16_f32 v116, v84, v85
	v_mfma_f32_16x16x32_bf16 v[68:71], v[236:239], v[12:15], v[68:71]
	s_mov_b32 m0, s35
	s_add_i32 s51, s50, 0x0
	v_cvt_pk_bf16_f32 v117, v86, v87
	v_mfma_f32_16x16x32_bf16 v[60:63], v[236:239], v[8:11], v[60:63]
	buffer_load_dwordx4 v125, s[36:39], s51 offen lds
	v_cvt_pk_bf16_f32 v118, v72, v73
	v_mfma_f32_16x16x32_bf16 v[56:59], v[232:235], v[8:11], v[56:59]
	v_cvt_pk_bf16_f32 v119, v74, v75
	ds_read_b128 v[232:235], v121 offset:51200
	ds_read_b128 v[236:239], v121 offset:52224
	s_waitcnt lgkmcnt(8)
	v_mfma_f32_16x16x32_bf16 v[64:67], v[240:243], v[16:19], v[64:67]
	v_pk_max_i16 v112, v112, 0
	v_mfma_f32_16x16x32_bf16 v[68:71], v[244:247], v[16:19], v[68:71]
	s_mov_b32 m0, s42
	s_add_i32 s51, s50, 0x2000
	v_pk_max_i16 v113, v113, 0
	v_mfma_f32_16x16x32_bf16 v[60:63], v[244:247], v[20:23], v[60:63]
	buffer_load_dwordx4 v125, s[36:39], s51 offen lds
	v_pk_max_i16 v114, v114, 0
	v_mfma_f32_16x16x32_bf16 v[56:59], v[240:243], v[20:23], v[56:59]
	v_pk_max_i16 v115, v115, 0
	ds_read_b128 v[240:243], v121 offset:53248
	ds_read_b128 v[244:247], v121 offset:54272
	s_waitcnt lgkmcnt(8)
	v_mfma_f32_16x16x32_bf16 v[64:67], v[248:251], v[24:27], v[64:67]
	v_pk_max_i16 v116, v116, 0
	v_mfma_f32_16x16x32_bf16 v[68:71], v[252:255], v[24:27], v[68:71]
	s_mov_b32 m0, s41
	s_add_i32 s51, s50, 0x4000
	v_pk_max_i16 v117, v117, 0
	v_mfma_f32_16x16x32_bf16 v[60:63], v[252:255], v[28:31], v[60:63]
	buffer_load_dwordx4 v125, s[36:39], s51 offen lds
	v_pk_max_i16 v118, v118, 0
	v_mfma_f32_16x16x32_bf16 v[56:59], v[248:251], v[28:31], v[56:59]
	v_pk_max_i16 v119, v119, 0
	ds_read_b128 v[248:251], v121 offset:55296
	ds_read_b128 v[252:255], v121 offset:56320
	s_setprio 2
	s_waitcnt lgkmcnt(8)
	v_mfma_f32_16x16x32_bf16 v[64:67], v[224:227], v[32:35], v[64:67]
	v_mfma_f32_16x16x32_bf16 v[68:71], v[228:231], v[32:35], v[68:71]
	s_mov_b32 m0, s40
	s_add_i32 s51, s50, 0x6000
	v_mfma_f32_16x16x32_bf16 v[60:63], v[228:231], v[36:39], v[60:63]
	buffer_load_dwordx4 v125, s[36:39], s51 offen lds
	v_mfma_f32_16x16x32_bf16 v[56:59], v[224:227], v[36:39], v[56:59]
	ds_read_b128 v[224:227], v121 offset:57344
	ds_read_b128 v[228:231], v121 offset:58368
	s_waitcnt lgkmcnt(6)
	v_mfma_f32_16x16x32_bf16 v[64:67], v[232:235], v[40:43], v[64:67]
	v_mfma_f32_16x16x32_bf16 v[68:71], v[236:239], v[40:43], v[68:71]
	v_mfma_f32_16x16x32_bf16 v[60:63], v[236:239], v[44:47], v[60:63]
	v_mfma_f32_16x16x32_bf16 v[56:59], v[232:235], v[44:47], v[56:59]
	ds_read_b128 v[232:235], v121 offset:59392
	ds_read_b128 v[236:239], v121 offset:60416
	s_waitcnt lgkmcnt(6)
	ds_read_b128 v[152:155], v183 offset:256
	ds_read_b128 v[156:159], v183 offset:320
	v_mfma_f32_16x16x32_bf16 v[64:67], v[240:243], v[48:51], v[64:67]
	v_mfma_f32_16x16x32_bf16 v[68:71], v[244:247], v[48:51], v[68:71]
	v_mfma_f32_16x16x32_bf16 v[60:63], v[244:247], v[52:55], v[60:63]
	v_mfma_f32_16x16x32_bf16 v[56:59], v[240:243], v[52:55], v[56:59]
	ds_read_b128 v[240:243], v121 offset:61440
	ds_read_b128 v[244:247], v121 offset:62464
	s_waitcnt lgkmcnt(8)
	v_mfma_f32_16x16x32_bf16 v[64:67], v[248:251], v[112:115], v[64:67]
	v_mfma_f32_16x16x32_bf16 v[68:71], v[252:255], v[112:115], v[68:71]
	v_mfma_f32_16x16x32_bf16 v[60:63], v[252:255], v[116:119], v[60:63]
	v_mfma_f32_16x16x32_bf16 v[56:59], v[248:251], v[116:119], v[56:59]
	ds_read_b128 v[248:251], v121 offset:63488
	ds_read_b128 v[252:255], v121 offset:64512
	s_setprio 1
	s_waitcnt lgkmcnt(8)
	v_mfma_f32_16x16x32_bf16 v[80:83], v[224:227], v[0:3], v[160:163]
	v_mfma_f32_16x16x32_bf16 v[76:79], v[228:231], v[0:3], v[164:167]
	v_mfma_f32_16x16x32_bf16 v[72:75], v[228:231], v[4:7], v[164:167]
	v_mfma_f32_16x16x32_bf16 v[84:87], v[224:227], v[4:7], v[160:163]
	ds_read_b128 v[224:227], v126 offset:57344
	ds_read_b128 v[228:231], v126 offset:58368
	s_waitcnt lgkmcnt(8)
	v_mfma_f32_16x16x32_bf16 v[80:83], v[232:235], v[12:15], v[80:83]
	v_cvt_pk_bf16_f32 v88, v64, v65
	v_mfma_f32_16x16x32_bf16 v[76:79], v[236:239], v[12:15], v[76:79]
	v_cvt_pk_bf16_f32 v89, v66, v67
	v_mfma_f32_16x16x32_bf16 v[72:75], v[236:239], v[8:11], v[72:75]
	v_cvt_pk_bf16_f32 v90, v68, v69
	v_mfma_f32_16x16x32_bf16 v[84:87], v[232:235], v[8:11], v[84:87]
	v_cvt_pk_bf16_f32 v91, v70, v71
	ds_read_b128 v[232:235], v126 offset:59392
	ds_read_b128 v[236:239], v126 offset:60416
	s_waitcnt lgkmcnt(6)
	v_mfma_f32_16x16x32_bf16 v[80:83], v[240:243], v[16:19], v[80:83]
	v_cvt_pk_bf16_f32 v92, v56, v57
	v_mfma_f32_16x16x32_bf16 v[76:79], v[244:247], v[16:19], v[76:79]
	v_cvt_pk_bf16_f32 v93, v58, v59
	v_mfma_f32_16x16x32_bf16 v[72:75], v[244:247], v[20:23], v[72:75]
	v_cvt_pk_bf16_f32 v94, v60, v61
	v_mfma_f32_16x16x32_bf16 v[84:87], v[240:243], v[20:23], v[84:87]
	v_cvt_pk_bf16_f32 v95, v62, v63
	ds_read_b128 v[240:243], v126 offset:61440
	ds_read_b128 v[244:247], v126 offset:62464
	s_waitcnt lgkmcnt(6)
	v_mfma_f32_16x16x32_bf16 v[80:83], v[248:251], v[24:27], v[80:83]
	v_pk_max_i16 v88, v88, 0
	v_mfma_f32_16x16x32_bf16 v[76:79], v[252:255], v[24:27], v[76:79]
	v_pk_max_i16 v89, v89, 0
	v_mfma_f32_16x16x32_bf16 v[72:75], v[252:255], v[28:31], v[72:75]
	v_pk_max_i16 v90, v90, 0
	v_mfma_f32_16x16x32_bf16 v[84:87], v[248:251], v[28:31], v[84:87]
	v_pk_max_i16 v91, v91, 0
	ds_read_b128 v[248:251], v126 offset:63488
	ds_read_b128 v[252:255], v126 offset:64512
	s_setprio 0
	s_waitcnt lgkmcnt(6)
	v_mfma_f32_16x16x32_bf16 v[80:83], v[224:227], v[32:35], v[80:83]
	v_pk_max_i16 v92, v92, 0
	v_mfma_f32_16x16x32_bf16 v[76:79], v[228:231], v[32:35], v[76:79]
	v_pk_max_i16 v93, v93, 0
	v_mfma_f32_16x16x32_bf16 v[72:75], v[228:231], v[36:39], v[72:75]
	v_pk_max_i16 v94, v94, 0
	v_mfma_f32_16x16x32_bf16 v[84:87], v[224:227], v[36:39], v[84:87]
	v_pk_max_i16 v95, v95, 0
	s_waitcnt lgkmcnt(4)
	v_mfma_f32_16x16x32_bf16 v[80:83], v[232:235], v[40:43], v[80:83]
	v_mfma_f32_16x16x32_bf16 v[76:79], v[236:239], v[40:43], v[76:79]
	v_mfma_f32_16x16x32_bf16 v[72:75], v[236:239], v[44:47], v[72:75]
	v_mfma_f32_16x16x32_bf16 v[84:87], v[232:235], v[44:47], v[84:87]
	s_branch .Lnerf_hid_a1
.Lnerf_hid_a0:
	s_waitcnt vmcnt(0) lgkmcnt(0)
	s_barrier
	ds_read_b128 v[224:227], v121 offset:40960
	ds_read_b128 v[228:231], v121 offset:41984
	v_mfma_f32_16x16x32_bf16 v[80:83], v[240:243], v[208:211], v[80:83]
	ds_read_b128 v[232:235], v121 offset:43008
	v_mfma_f32_16x16x32_bf16 v[76:79], v[244:247], v[208:211], v[76:79]
	ds_read_b128 v[236:239], v121 offset:44032
	v_mfma_f32_16x16x32_bf16 v[72:75], v[244:247], v[212:215], v[72:75]
	v_mfma_f32_16x16x32_bf16 v[84:87], v[240:243], v[212:215], v[84:87]
	ds_read_b128 v[240:243], v121 offset:45056
	ds_read_b128 v[244:247], v121 offset:46080
	v_mfma_f32_16x16x32_bf16 v[80:83], v[248:251], v[216:219], v[80:83]
	v_mfma_f32_16x16x32_bf16 v[76:79], v[252:255], v[216:219], v[76:79]
	v_mfma_f32_16x16x32_bf16 v[72:75], v[252:255], v[220:223], v[72:75]
	v_mfma_f32_16x16x32_bf16 v[84:87], v[248:251], v[220:223], v[84:87]
	ds_read_b128 v[248:251], v121 offset:47104
	ds_read_b128 v[252:255], v121 offset:48128
	s_setprio 3
	s_waitcnt lgkmcnt(6)
	v_mfma_f32_16x16x32_bf16 v[64:67], v[224:227], v[0:3], v[152:155]
	v_mfma_f32_16x16x32_bf16 v[68:71], v[228:231], v[0:3], v[156:159]
	v_mfma_f32_16x16x32_bf16 v[60:63], v[228:231], v[4:7], v[156:159]
	v_mfma_f32_16x16x32_bf16 v[56:59], v[224:227], v[4:7], v[152:155]
	ds_read_b128 v[224:227], v121 offset:49152
	ds_read_b128 v[228:231], v121 offset:50176
	s_waitcnt lgkmcnt(6)
	ds_read_b128 v[160:163], v183 offset:128
	ds_read_b128 v[164:167], v183 offset:192
	v_mfma_f32_16x16x32_bf16 v[64:67], v[232:235], v[12:15], v[64:67]
	v_cvt_pk_bf16_f32 v112, v80, v81
	v_mfma_f32_16x16x32_bf16 v[68:71], v[236:239], v[12:15], v[68:71]
	s_mov_b32 m0, s35
	s_add_i32 s51, s50, 0x0
	v_cvt_pk_bf16_f32 v113, v82, v83
	v_mfma_f32_16x16x32_bf16 v[60:63], v[236:239], v[8:11], v[60:63]
	buffer_load_dwordx4 v125, s[36:39], s51 offen lds
	v_cvt_pk_bf16_f32 v114, v76, v77
	v_mfma_f32_16x16x32_bf16 v[56:59], v[232:235], v[8:11], v[56:59]
	v_cvt_pk_bf16_f32 v115, v78, v79
	ds_read_b128 v[232:235], v121 offset:51200
	ds_read_b128 v[236:239], v121 offset:52224
	s_waitcnt lgkmcnt(8)
	v_mfma_f32_16x16x32_bf16 v[64:67], v[240:243], v[16:19], v[64:67]
	v_cvt_pk_bf16_f32 v116, v84, v85
	v_mfma_f32_16x16x32_bf16 v[68:71], v[244:247], v[16:19], v[68:71]
	s_mov_b32 m0, s42
	s_add_i32 s51, s50, 0x2000
	v_cvt_pk_bf16_f32 v117, v86, v87
	v_mfma_f32_16x16x32_bf16 v[60:63], v[244:247], v[20:23], v[60:63]
	buffer_load_dwordx4 v125, s[36:39], s51 offen lds
	v_cvt_pk_bf16_f32 v118, v72, v73
	v_mfma_f32_16x16x32_bf16 v[56:59], v[240:243], v[20:23], v[56:59]
	v_cvt_pk_bf16_f32 v119, v74, v75
	ds_read_b128 v[240:243], v121 offset:53248
	ds_read_b128 v[244:247], v121 offset:54272
	s_waitcnt lgkmcnt(8)
	v_mfma_f32_16x16x32_bf16 v[64:67], v[248:251], v[24:27], v[64:67]
	v_pk_max_i16 v112, v112, 0
	v_mfma_f32_16x16x32_bf16 v[68:71], v[252:255], v[24:27], v[68:71]
	s_mov_b32 m0, s41
	s_add_i32 s51, s50, 0x4000
	v_pk_max_i16 v113, v113, 0
	v_mfma_f32_16x16x32_bf16 v[60:63], v[252:255], v[28:31], v[60:63]
	buffer_load_dwordx4 v125, s[36:39], s51 offen lds
	v_pk_max_i16 v114, v114, 0
	v_mfma_f32_16x16x32_bf16 v[56:59], v[248:251], v[28:31], v[56:59]
	v_pk_max_i16 v115, v115, 0
	ds_read_b128 v[248:251], v121 offset:55296
	ds_read_b128 v[252:255], v121 offset:56320
	s_setprio 2
	s_waitcnt lgkmcnt(8)
	v_mfma_f32_16x16x32_bf16 v[64:67], v[224:227], v[32:35], v[64:67]
	v_pk_max_i16 v116, v116, 0
	v_mfma_f32_16x16x32_bf16 v[68:71], v[228:231], v[32:35], v[68:71]
	s_mov_b32 m0, s40
	s_add_i32 s51, s50, 0x6000
	v_pk_max_i16 v117, v117, 0
	v_mfma_f32_16x16x32_bf16 v[60:63], v[228:231], v[36:39], v[60:63]
	buffer_load_dwordx4 v125, s[36:39], s51 offen lds
	v_pk_max_i16 v118, v118, 0
	v_mfma_f32_16x16x32_bf16 v[56:59], v[224:227], v[36:39], v[56:59]
	v_pk_max_i16 v119, v119, 0
	ds_read_b128 v[224:227], v121 offset:57344
	ds_read_b128 v[228:231], v121 offset:58368
	s_waitcnt lgkmcnt(6)
	v_mfma_f32_16x16x32_bf16 v[64:67], v[232:235], v[40:43], v[64:67]
	v_mfma_f32_16x16x32_bf16 v[68:71], v[236:239], v[40:43], v[68:71]
	v_mfma_f32_16x16x32_bf16 v[60:63], v[236:239], v[44:47], v[60:63]
	v_mfma_f32_16x16x32_bf16 v[56:59], v[232:235], v[44:47], v[56:59]
	ds_read_b128 v[232:235], v121 offset:59392
	ds_read_b128 v[236:239], v121 offset:60416
	s_waitcnt lgkmcnt(6)
	ds_read_b128 v[152:155], v183 offset:256
	ds_read_b128 v[156:159], v183 offset:320
	v_mfma_f32_16x16x32_bf16 v[64:67], v[240:243], v[48:51], v[64:67]
	v_mfma_f32_16x16x32_bf16 v[68:71], v[244:247], v[48:51], v[68:71]
	v_mfma_f32_16x16x32_bf16 v[60:63], v[244:247], v[52:55], v[60:63]
	v_mfma_f32_16x16x32_bf16 v[56:59], v[240:243], v[52:55], v[56:59]
	ds_read_b128 v[240:243], v121 offset:61440
	ds_read_b128 v[244:247], v121 offset:62464
	s_waitcnt lgkmcnt(8)
	v_mfma_f32_16x16x32_bf16 v[64:67], v[248:251], v[112:115], v[64:67]
	v_mfma_f32_16x16x32_bf16 v[68:71], v[252:255], v[112:115], v[68:71]
	v_mfma_f32_16x16x32_bf16 v[60:63], v[252:255], v[116:119], v[60:63]
	v_mfma_f32_16x16x32_bf16 v[56:59], v[248:251], v[116:119], v[56:59]
	ds_read_b128 v[248:251], v121 offset:63488
	ds_read_b128 v[252:255], v121 offset:64512
	s_setprio 1
	s_waitcnt lgkmcnt(8)
	v_mfma_f32_16x16x32_bf16 v[80:83], v[224:227], v[0:3], v[160:163]
	v_mfma_f32_16x16x32_bf16 v[76:79], v[228:231], v[0:3], v[164:167]
	v_mfma_f32_16x16x32_bf16 v[72:75], v[228:231], v[4:7], v[164:167]
	v_mfma_f32_16x16x32_bf16 v[84:87], v[224:227], v[4:7], v[160:163]
	ds_read_b128 v[224:227], v126 offset:57344
	ds_read_b128 v[228:231], v126 offset:58368
	s_waitcnt lgkmcnt(8)
	v_mfma_f32_16x16x32_bf16 v[80:83], v[232:235], v[12:15], v[80:83]
	v_cvt_pk_bf16_f32 v88, v64, v65
	v_mfma_f32_16x16x32_bf16 v[76:79], v[236:239], v[12:15], v[76:79]
	v_cvt_pk_bf16_f32 v89, v66, v67
	v_mfma_f32_16x16x32_bf16 v[72:75], v[236:239], v[8:11], v[72:75]
	v_cvt_pk_bf16_f32 v90, v68, v69
	v_mfma_f32_16x16x32_bf16 v[84:87], v[232:235], v[8:11], v[84:87]
	v_cvt_pk_bf16_f32 v91, v70, v71
	ds_read_b128 v[232:235], v126 offset:59392
	ds_read_b128 v[236:239], v126 offset:60416
	s_waitcnt lgkmcnt(6)
	v_mfma_f32_16x16x32_bf16 v[80:83], v[240:243], v[16:19], v[80:83]
	v_cvt_pk_bf16_f32 v92, v56, v57
	v_mfma_f32_16x16x32_bf16 v[76:79], v[244:247], v[16:19], v[76:79]
	v_cvt_pk_bf16_f32 v93, v58, v59
	v_mfma_f32_16x16x32_bf16 v[72:75], v[244:247], v[20:23], v[72:75]
	v_cvt_pk_bf16_f32 v94, v60, v61
	v_mfma_f32_16x16x32_bf16 v[84:87], v[240:243], v[20:23], v[84:87]
	v_cvt_pk_bf16_f32 v95, v62, v63
	ds_read_b128 v[240:243], v126 offset:61440
	ds_read_b128 v[244:247], v126 offset:62464
	s_waitcnt lgkmcnt(6)
	v_mfma_f32_16x16x32_bf16 v[80:83], v[248:251], v[24:27], v[80:83]
	v_pk_max_i16 v88, v88, 0
	v_mfma_f32_16x16x32_bf16 v[76:79], v[252:255], v[24:27], v[76:79]
	v_pk_max_i16 v89, v89, 0
	v_mfma_f32_16x16x32_bf16 v[72:75], v[252:255], v[28:31], v[72:75]
	v_pk_max_i16 v90, v90, 0
	v_mfma_f32_16x16x32_bf16 v[84:87], v[248:251], v[28:31], v[84:87]
	v_pk_max_i16 v91, v91, 0
	ds_read_b128 v[248:251], v126 offset:63488
	ds_read_b128 v[252:255], v126 offset:64512
	s_setprio 0
	s_waitcnt lgkmcnt(6)
	v_mfma_f32_16x16x32_bf16 v[80:83], v[224:227], v[32:35], v[80:83]
	v_pk_max_i16 v92, v92, 0
	v_mfma_f32_16x16x32_bf16 v[76:79], v[228:231], v[32:35], v[76:79]
	v_pk_max_i16 v93, v93, 0
	v_mfma_f32_16x16x32_bf16 v[72:75], v[228:231], v[36:39], v[72:75]
	v_pk_max_i16 v94, v94, 0
	v_mfma_f32_16x16x32_bf16 v[84:87], v[224:227], v[36:39], v[84:87]
	v_pk_max_i16 v95, v95, 0
	s_waitcnt lgkmcnt(4)
	v_mfma_f32_16x16x32_bf16 v[80:83], v[232:235], v[40:43], v[80:83]
	v_mfma_f32_16x16x32_bf16 v[76:79], v[236:239], v[40:43], v[76:79]
	v_mfma_f32_16x16x32_bf16 v[72:75], v[236:239], v[44:47], v[72:75]
	v_mfma_f32_16x16x32_bf16 v[84:87], v[232:235], v[44:47], v[84:87]
.Lnerf_hid_a1:
	s_waitcnt vmcnt(0) lgkmcnt(0)
	s_barrier
	ds_read_b128 v[224:227], v121 offset:8192
	ds_read_b128 v[228:231], v121 offset:9216
	v_mfma_f32_16x16x32_bf16 v[80:83], v[240:243], v[48:51], v[80:83]
	ds_read_b128 v[232:235], v121 offset:10240
	v_mfma_f32_16x16x32_bf16 v[76:79], v[244:247], v[48:51], v[76:79]
	ds_read_b128 v[236:239], v121 offset:11264
	v_mfma_f32_16x16x32_bf16 v[72:75], v[244:247], v[52:55], v[72:75]
	v_mfma_f32_16x16x32_bf16 v[84:87], v[240:243], v[52:55], v[84:87]
	ds_read_b128 v[240:243], v121 offset:12288
	ds_read_b128 v[244:247], v121 offset:13312
	v_mfma_f32_16x16x32_bf16 v[80:83], v[248:251], v[112:115], v[80:83]
	v_mfma_f32_16x16x32_bf16 v[76:79], v[252:255], v[112:115], v[76:79]
	v_mfma_f32_16x16x32_bf16 v[72:75], v[252:255], v[116:119], v[72:75]
	v_mfma_f32_16x16x32_bf16 v[84:87], v[248:251], v[116:119], v[84:87]
	ds_read_b128 v[248:251], v121 offset:14336
	ds_read_b128 v[252:255], v121 offset:15360
	s_setprio 3
	s_waitcnt lgkmcnt(6)
	v_mfma_f32_16x16x32_bf16 v[64:67], v[224:227], v[0:3], v[152:155]
	v_mfma_f32_16x16x32_bf16 v[68:71], v[228:231], v[0:3], v[156:159]
	v_mfma_f32_16x16x32_bf16 v[60:63], v[228:231], v[4:7], v[156:159]
	v_mfma_f32_16x16x32_bf16 v[56:59], v[224:227], v[4:7], v[152:155]
	ds_read_b128 v[224:227], v121 offset:16384
	ds_read_b128 v[228:231], v121 offset:17408
	s_waitcnt lgkmcnt(6)
	ds_read_b128 v[160:163], v183 offset:384
	ds_read_b128 v[164:167], v183 offset:448
	v_mfma_f32_16x16x32_bf16 v[64:67], v[232:235], v[12:15], v[64:67]
	v_cvt_pk_bf16_f32 v96, v80, v81
	v_mfma_f32_16x16x32_bf16 v[68:71], v[236:239], v[12:15], v[68:71]
	s_mov_b32 m0, s28
	s_add_i32 s51, s50, 0x8000
	v_cvt_pk_bf16_f32 v97, v82, v83
	v_mfma_f32_16x16x32_bf16 v[60:63], v[236:239], v[8:11], v[60:63]
	buffer_load_dwordx4 v125, s[36:39], s51 offen lds
	v_cvt_pk_bf16_f32 v98, v76, v77
	v_mfma_f32_16x16x32_bf16 v[56:59], v[232:235], v[8:11], v[56:59]
	v_cvt_pk_bf16_f32 v99, v78, v79
	ds_read_b128 v[232:235], v121 offset:18432
	ds_read_b128 v[236:239], v121 offset:19456
	s_waitcnt lgkmcnt(8)
	v_mfma_f32_16x16x32_bf16 v[64:67], v[240:243], v[16:19], v[64:67]
	v_cvt_pk_bf16_f32 v100, v84, v85
	v_mfma_f32_16x16x32_bf16 v[68:71], v[244:247], v[16:19], v[68:71]
	s_mov_b32 m0, s29
	s_add_i32 s51, s50, 0xa000
	v_cvt_pk_bf16_f32 v101, v86, v87
	v_mfma_f32_16x16x32_bf16 v[60:63], v[244:247], v[20:23], v[60:63]
	buffer_load_dwordx4 v125, s[36:39], s51 offen lds
	v_cvt_pk_bf16_f32 v102, v72, v73
	v_mfma_f32_16x16x32_bf16 v[56:59], v[240:243], v[20:23], v[56:59]
	v_cvt_pk_bf16_f32 v103, v74, v75
	ds_read_b128 v[240:243], v121 offset:20480
	ds_read_b128 v[244:247], v121 offset:21504
	s_waitcnt lgkmcnt(8)
	v_mfma_f32_16x16x32_bf16 v[64:67], v[248:251], v[24:27], v[64:67]
	v_pk_max_i16 v96, v96, 0
	v_mfma_f32_16x16x32_bf16 v[68:71], v[252:255], v[24:27], v[68:71]
	s_mov_b32 m0, s33
	s_add_i32 s51, s50, 0xc000
	v_pk_max_i16 v97, v97, 0
	v_mfma_f32_16x16x32_bf16 v[60:63], v[252:255], v[28:31], v[60:63]
	buffer_load_dwordx4 v125, s[36:39], s51 offen lds
	v_pk_max_i16 v98, v98, 0
	v_mfma_f32_16x16x32_bf16 v[56:59], v[248:251], v[28:31], v[56:59]
	v_pk_max_i16 v99, v99, 0
	ds_read_b128 v[248:251], v121 offset:22528
	ds_read_b128 v[252:255], v121 offset:23552
	s_setprio 2
	s_waitcnt lgkmcnt(8)
	v_mfma_f32_16x16x32_bf16 v[64:67], v[224:227], v[32:35], v[64:67]
	v_pk_max_i16 v100, v100, 0
	v_mfma_f32_16x16x32_bf16 v[68:71], v[228:231], v[32:35], v[68:71]
	s_mov_b32 m0, s34
	s_add_i32 s51, s50, 0xe000
	v_pk_max_i16 v101, v101, 0
	v_mfma_f32_16x16x32_bf16 v[60:63], v[228:231], v[36:39], v[60:63]
	buffer_load_dwordx4 v125, s[36:39], s51 offen lds
	v_pk_max_i16 v102, v102, 0
	v_mfma_f32_16x16x32_bf16 v[56:59], v[224:227], v[36:39], v[56:59]
	v_pk_max_i16 v103, v103, 0
	ds_read_b128 v[224:227], v121 offset:24576
	ds_read_b128 v[228:231], v121 offset:25600
	s_waitcnt lgkmcnt(6)
	v_mfma_f32_16x16x32_bf16 v[64:67], v[232:235], v[40:43], v[64:67]
	v_mfma_f32_16x16x32_bf16 v[68:71], v[236:239], v[40:43], v[68:71]
	v_mfma_f32_16x16x32_bf16 v[60:63], v[236:239], v[44:47], v[60:63]
	v_mfma_f32_16x16x32_bf16 v[56:59], v[232:235], v[44:47], v[56:59]
	ds_read_b128 v[232:235], v121 offset:26624
	ds_read_b128 v[236:239], v121 offset:27648
	s_waitcnt lgkmcnt(6)
	ds_read_b128 v[152:155], v183 offset:512
	ds_read_b128 v[156:159], v183 offset:576
	v_mfma_f32_16x16x32_bf16 v[64:67], v[240:243], v[48:51], v[64:67]
	v_mfma_f32_16x16x32_bf16 v[68:71], v[244:247], v[48:51], v[68:71]
	v_mfma_f32_16x16x32_bf16 v[60:63], v[244:247], v[52:55], v[60:63]
	v_mfma_f32_16x16x32_bf16 v[56:59], v[240:243], v[52:55], v[56:59]
	ds_read_b128 v[240:243], v121 offset:28672
	ds_read_b128 v[244:247], v121 offset:29696
	s_waitcnt lgkmcnt(8)
	v_mfma_f32_16x16x32_bf16 v[64:67], v[248:251], v[112:115], v[64:67]
	v_mfma_f32_16x16x32_bf16 v[68:71], v[252:255], v[112:115], v[68:71]
	v_mfma_f32_16x16x32_bf16 v[60:63], v[252:255], v[116:119], v[60:63]
	v_mfma_f32_16x16x32_bf16 v[56:59], v[248:251], v[116:119], v[56:59]
	ds_read_b128 v[248:251], v121 offset:30720
	ds_read_b128 v[252:255], v121 offset:31744
	s_setprio 1
	s_waitcnt lgkmcnt(8)
	v_mfma_f32_16x16x32_bf16 v[80:83], v[224:227], v[0:3], v[160:163]
	v_mfma_f32_16x16x32_bf16 v[76:79], v[228:231], v[0:3], v[164:167]
	v_mfma_f32_16x16x32_bf16 v[72:75], v[228:231], v[4:7], v[164:167]
	v_mfma_f32_16x16x32_bf16 v[84:87], v[224:227], v[4:7], v[160:163]
	ds_read_b128 v[224:227], v121 offset:32768
	ds_read_b128 v[228:231], v121 offset:33792
	s_waitcnt lgkmcnt(8)
	v_mfma_f32_16x16x32_bf16 v[80:83], v[232:235], v[12:15], v[80:83]
	v_cvt_pk_bf16_f32 v104, v64, v65
	v_mfma_f32_16x16x32_bf16 v[76:79], v[236:239], v[12:15], v[76:79]
	v_cvt_pk_bf16_f32 v105, v66, v67
	v_mfma_f32_16x16x32_bf16 v[72:75], v[236:239], v[8:11], v[72:75]
	v_cvt_pk_bf16_f32 v106, v68, v69
	v_mfma_f32_16x16x32_bf16 v[84:87], v[232:235], v[8:11], v[84:87]
	v_cvt_pk_bf16_f32 v107, v70, v71
	ds_read_b128 v[232:235], v121 offset:34816
	ds_read_b128 v[236:239], v121 offset:35840
	s_waitcnt lgkmcnt(6)
	v_mfma_f32_16x16x32_bf16 v[80:83], v[240:243], v[16:19], v[80:83]
	v_cvt_pk_bf16_f32 v108, v56, v57
	v_mfma_f32_16x16x32_bf16 v[76:79], v[244:247], v[16:19], v[76:79]
	v_cvt_pk_bf16_f32 v109, v58, v59
	v_mfma_f32_16x16x32_bf16 v[72:75], v[244:247], v[20:23], v[72:75]
	v_cvt_pk_bf16_f32 v110, v60, v61
	v_mfma_f32_16x16x32_bf16 v[84:87], v[240:243], v[20:23], v[84:87]
	v_cvt_pk_bf16_f32 v111, v62, v63
	ds_read_b128 v[240:243], v121 offset:36864
	ds_read_b128 v[244:247], v121 offset:37888
	s_waitcnt lgkmcnt(6)
	v_mfma_f32_16x16x32_bf16 v[80:83], v[248:251], v[24:27], v[80:83]
	v_pk_max_i16 v104, v104, 0
	v_mfma_f32_16x16x32_bf16 v[76:79], v[252:255], v[24:27], v[76:79]
	v_pk_max_i16 v105, v105, 0
	v_mfma_f32_16x16x32_bf16 v[72:75], v[252:255], v[28:31], v[72:75]
	v_pk_max_i16 v106, v106, 0
	v_mfma_f32_16x16x32_bf16 v[84:87], v[248:251], v[28:31], v[84:87]
	v_pk_max_i16 v107, v107, 0
	ds_read_b128 v[248:251], v121 offset:38912
	ds_read_b128 v[252:255], v121 offset:39936
	s_setprio 0
	s_waitcnt lgkmcnt(6)
	v_mfma_f32_16x16x32_bf16 v[80:83], v[224:227], v[32:35], v[80:83]
	v_pk_max_i16 v108, v108, 0
	v_mfma_f32_16x16x32_bf16 v[76:79], v[228:231], v[32:35], v[76:79]
	v_pk_max_i16 v109, v109, 0
	v_mfma_f32_16x16x32_bf16 v[72:75], v[228:231], v[36:39], v[72:75]
	v_pk_max_i16 v110, v110, 0
	v_mfma_f32_16x16x32_bf16 v[84:87], v[224:227], v[36:39], v[84:87]
	v_pk_max_i16 v111, v111, 0
	s_waitcnt lgkmcnt(4)
	v_mfma_f32_16x16x32_bf16 v[80:83], v[232:235], v[40:43], v[80:83]
	v_mfma_f32_16x16x32_bf16 v[76:79], v[236:239], v[40:43], v[76:79]
	v_mfma_f32_16x16x32_bf16 v[72:75], v[236:239], v[44:47], v[72:75]
	v_mfma_f32_16x16x32_bf16 v[84:87], v[232:235], v[44:47], v[84:87]
.Lnerf_hid_a2:
	s_waitcnt vmcnt(0) lgkmcnt(0)
	s_barrier
	ds_read_b128 v[224:227], v121 offset:40960
	ds_read_b128 v[228:231], v121 offset:41984
	v_mfma_f32_16x16x32_bf16 v[80:83], v[240:243], v[48:51], v[80:83]
	ds_read_b128 v[232:235], v121 offset:43008
	v_mfma_f32_16x16x32_bf16 v[76:79], v[244:247], v[48:51], v[76:79]
	ds_read_b128 v[236:239], v121 offset:44032
	v_mfma_f32_16x16x32_bf16 v[72:75], v[244:247], v[52:55], v[72:75]
	v_mfma_f32_16x16x32_bf16 v[84:87], v[240:243], v[52:55], v[84:87]
	ds_read_b128 v[240:243], v121 offset:45056
	ds_read_b128 v[244:247], v121 offset:46080
	v_mfma_f32_16x16x32_bf16 v[80:83], v[248:251], v[112:115], v[80:83]
	v_mfma_f32_16x16x32_bf16 v[76:79], v[252:255], v[112:115], v[76:79]
	v_mfma_f32_16x16x32_bf16 v[72:75], v[252:255], v[116:119], v[72:75]
	v_mfma_f32_16x16x32_bf16 v[84:87], v[248:251], v[116:119], v[84:87]
	ds_read_b128 v[248:251], v121 offset:47104
	ds_read_b128 v[252:255], v121 offset:48128
	s_setprio 3
	s_waitcnt lgkmcnt(6)
	v_mfma_f32_16x16x32_bf16 v[64:67], v[224:227], v[0:3], v[152:155]
	v_mfma_f32_16x16x32_bf16 v[68:71], v[228:231], v[0:3], v[156:159]
	v_mfma_f32_16x16x32_bf16 v[60:63], v[228:231], v[4:7], v[156:159]
	v_mfma_f32_16x16x32_bf16 v[56:59], v[224:227], v[4:7], v[152:155]
	ds_read_b128 v[224:227], v121 offset:49152
	ds_read_b128 v[228:231], v121 offset:50176
	s_waitcnt lgkmcnt(6)
	ds_read_b128 v[160:163], v183 offset:640
	ds_read_b128 v[164:167], v183 offset:704
	v_mfma_f32_16x16x32_bf16 v[64:67], v[232:235], v[12:15], v[64:67]
	v_cvt_pk_bf16_f32 v184, v80, v81
	v_mfma_f32_16x16x32_bf16 v[68:71], v[236:239], v[12:15], v[68:71]
	s_mov_b32 m0, s35
	s_add_i32 s51, s50, 0x10000
	v_cvt_pk_bf16_f32 v185, v82, v83
	v_mfma_f32_16x16x32_bf16 v[60:63], v[236:239], v[8:11], v[60:63]
	buffer_load_dwordx4 v125, s[36:39], s51 offen lds
	v_cvt_pk_bf16_f32 v186, v76, v77
	v_mfma_f32_16x16x32_bf16 v[56:59], v[232:235], v[8:11], v[56:59]
	v_cvt_pk_bf16_f32 v187, v78, v79
	ds_read_b128 v[232:235], v121 offset:51200
	ds_read_b128 v[236:239], v121 offset:52224
	s_waitcnt lgkmcnt(8)
	v_mfma_f32_16x16x32_bf16 v[64:67], v[240:243], v[16:19], v[64:67]
	v_cvt_pk_bf16_f32 v188, v84, v85
	v_mfma_f32_16x16x32_bf16 v[68:71], v[244:247], v[16:19], v[68:71]
	s_mov_b32 m0, s42
	s_add_i32 s51, s50, 0x12000
	v_cvt_pk_bf16_f32 v189, v86, v87
	v_mfma_f32_16x16x32_bf16 v[60:63], v[244:247], v[20:23], v[60:63]
	buffer_load_dwordx4 v125, s[36:39], s51 offen lds
	v_cvt_pk_bf16_f32 v190, v72, v73
	v_mfma_f32_16x16x32_bf16 v[56:59], v[240:243], v[20:23], v[56:59]
	v_cvt_pk_bf16_f32 v191, v74, v75
	ds_read_b128 v[240:243], v121 offset:53248
	ds_read_b128 v[244:247], v121 offset:54272
	s_waitcnt lgkmcnt(8)
	v_mfma_f32_16x16x32_bf16 v[64:67], v[248:251], v[24:27], v[64:67]
	v_pk_max_i16 v184, v184, 0
	v_mfma_f32_16x16x32_bf16 v[68:71], v[252:255], v[24:27], v[68:71]
	s_mov_b32 m0, s41
	s_add_i32 s51, s50, 0x14000
	v_pk_max_i16 v185, v185, 0
	v_mfma_f32_16x16x32_bf16 v[60:63], v[252:255], v[28:31], v[60:63]
	buffer_load_dwordx4 v125, s[36:39], s51 offen lds
	v_pk_max_i16 v186, v186, 0
	v_mfma_f32_16x16x32_bf16 v[56:59], v[248:251], v[28:31], v[56:59]
	v_pk_max_i16 v187, v187, 0
	ds_read_b128 v[248:251], v121 offset:55296
	ds_read_b128 v[252:255], v121 offset:56320
	s_setprio 2
	s_waitcnt lgkmcnt(8)
	v_mfma_f32_16x16x32_bf16 v[64:67], v[224:227], v[32:35], v[64:67]
	v_pk_max_i16 v188, v188, 0
	v_mfma_f32_16x16x32_bf16 v[68:71], v[228:231], v[32:35], v[68:71]
	s_mov_b32 m0, s40
	s_add_i32 s51, s50, 0x16000
	v_pk_max_i16 v189, v189, 0
	v_mfma_f32_16x16x32_bf16 v[60:63], v[228:231], v[36:39], v[60:63]
	buffer_load_dwordx4 v125, s[36:39], s51 offen lds
	v_pk_max_i16 v190, v190, 0
	v_mfma_f32_16x16x32_bf16 v[56:59], v[224:227], v[36:39], v[56:59]
	v_pk_max_i16 v191, v191, 0
	ds_read_b128 v[224:227], v121 offset:57344
	ds_read_b128 v[228:231], v121 offset:58368
	s_waitcnt lgkmcnt(6)
	v_mfma_f32_16x16x32_bf16 v[64:67], v[232:235], v[40:43], v[64:67]
	v_mfma_f32_16x16x32_bf16 v[68:71], v[236:239], v[40:43], v[68:71]
	v_mfma_f32_16x16x32_bf16 v[60:63], v[236:239], v[44:47], v[60:63]
	v_mfma_f32_16x16x32_bf16 v[56:59], v[232:235], v[44:47], v[56:59]
	ds_read_b128 v[232:235], v121 offset:59392
	ds_read_b128 v[236:239], v121 offset:60416
	s_waitcnt lgkmcnt(6)
	ds_read_b128 v[152:155], v183 offset:768
	ds_read_b128 v[156:159], v183 offset:832
	v_mfma_f32_16x16x32_bf16 v[64:67], v[240:243], v[48:51], v[64:67]
	v_mfma_f32_16x16x32_bf16 v[68:71], v[244:247], v[48:51], v[68:71]
	v_mfma_f32_16x16x32_bf16 v[60:63], v[244:247], v[52:55], v[60:63]
	v_mfma_f32_16x16x32_bf16 v[56:59], v[240:243], v[52:55], v[56:59]
	ds_read_b128 v[240:243], v121 offset:61440
	ds_read_b128 v[244:247], v121 offset:62464
	s_waitcnt lgkmcnt(8)
	v_mfma_f32_16x16x32_bf16 v[64:67], v[248:251], v[112:115], v[64:67]
	v_mfma_f32_16x16x32_bf16 v[68:71], v[252:255], v[112:115], v[68:71]
	v_mfma_f32_16x16x32_bf16 v[60:63], v[252:255], v[116:119], v[60:63]
	v_mfma_f32_16x16x32_bf16 v[56:59], v[248:251], v[116:119], v[56:59]
	ds_read_b128 v[248:251], v121 offset:63488
	ds_read_b128 v[252:255], v121 offset:64512
	s_setprio 1
	s_waitcnt lgkmcnt(8)
	v_mfma_f32_16x16x32_bf16 v[80:83], v[224:227], v[0:3], v[160:163]
	v_mfma_f32_16x16x32_bf16 v[76:79], v[228:231], v[0:3], v[164:167]
	v_mfma_f32_16x16x32_bf16 v[72:75], v[228:231], v[4:7], v[164:167]
	v_mfma_f32_16x16x32_bf16 v[84:87], v[224:227], v[4:7], v[160:163]
	ds_read_b128 v[224:227], v126 offset:57344
	ds_read_b128 v[228:231], v126 offset:58368
	s_waitcnt lgkmcnt(8)
	v_mfma_f32_16x16x32_bf16 v[80:83], v[232:235], v[12:15], v[80:83]
	v_cvt_pk_bf16_f32 v192, v64, v65
	v_mfma_f32_16x16x32_bf16 v[76:79], v[236:239], v[12:15], v[76:79]
	v_cvt_pk_bf16_f32 v193, v66, v67
	v_mfma_f32_16x16x32_bf16 v[72:75], v[236:239], v[8:11], v[72:75]
	v_cvt_pk_bf16_f32 v194, v68, v69
	v_mfma_f32_16x16x32_bf16 v[84:87], v[232:235], v[8:11], v[84:87]
	v_cvt_pk_bf16_f32 v195, v70, v71
	ds_read_b128 v[232:235], v126 offset:59392
	ds_read_b128 v[236:239], v126 offset:60416
	s_waitcnt lgkmcnt(6)
	v_mfma_f32_16x16x32_bf16 v[80:83], v[240:243], v[16:19], v[80:83]
	v_cvt_pk_bf16_f32 v196, v56, v57
	v_mfma_f32_16x16x32_bf16 v[76:79], v[244:247], v[16:19], v[76:79]
	v_cvt_pk_bf16_f32 v197, v58, v59
	v_mfma_f32_16x16x32_bf16 v[72:75], v[244:247], v[20:23], v[72:75]
	v_cvt_pk_bf16_f32 v198, v60, v61
	v_mfma_f32_16x16x32_bf16 v[84:87], v[240:243], v[20:23], v[84:87]
	v_cvt_pk_bf16_f32 v199, v62, v63
	ds_read_b128 v[240:243], v126 offset:61440
	ds_read_b128 v[244:247], v126 offset:62464
	s_waitcnt lgkmcnt(6)
	v_mfma_f32_16x16x32_bf16 v[80:83], v[248:251], v[24:27], v[80:83]
	v_pk_max_i16 v192, v192, 0
	v_mfma_f32_16x16x32_bf16 v[76:79], v[252:255], v[24:27], v[76:79]
	v_pk_max_i16 v193, v193, 0
	v_mfma_f32_16x16x32_bf16 v[72:75], v[252:255], v[28:31], v[72:75]
	v_pk_max_i16 v194, v194, 0
	v_mfma_f32_16x16x32_bf16 v[84:87], v[248:251], v[28:31], v[84:87]
	v_pk_max_i16 v195, v195, 0
	ds_read_b128 v[248:251], v126 offset:63488
	ds_read_b128 v[252:255], v126 offset:64512
	s_setprio 0
	s_waitcnt lgkmcnt(6)
	v_mfma_f32_16x16x32_bf16 v[80:83], v[224:227], v[32:35], v[80:83]
	v_pk_max_i16 v196, v196, 0
	v_mfma_f32_16x16x32_bf16 v[76:79], v[228:231], v[32:35], v[76:79]
	v_pk_max_i16 v197, v197, 0
	v_mfma_f32_16x16x32_bf16 v[72:75], v[228:231], v[36:39], v[72:75]
	v_pk_max_i16 v198, v198, 0
	v_mfma_f32_16x16x32_bf16 v[84:87], v[224:227], v[36:39], v[84:87]
	v_pk_max_i16 v199, v199, 0
	s_waitcnt lgkmcnt(4)
	v_mfma_f32_16x16x32_bf16 v[80:83], v[232:235], v[40:43], v[80:83]
	v_mfma_f32_16x16x32_bf16 v[76:79], v[236:239], v[40:43], v[76:79]
	v_mfma_f32_16x16x32_bf16 v[72:75], v[236:239], v[44:47], v[72:75]
	v_mfma_f32_16x16x32_bf16 v[84:87], v[232:235], v[44:47], v[84:87]
.Lnerf_hid_a3:
	s_waitcnt vmcnt(0) lgkmcnt(0)
	s_barrier
	ds_read_b128 v[224:227], v121 offset:8192
	ds_read_b128 v[228:231], v121 offset:9216
	v_mfma_f32_16x16x32_bf16 v[80:83], v[240:243], v[48:51], v[80:83]
	ds_read_b128 v[232:235], v121 offset:10240
	v_mfma_f32_16x16x32_bf16 v[76:79], v[244:247], v[48:51], v[76:79]
	ds_read_b128 v[236:239], v121 offset:11264
	v_mfma_f32_16x16x32_bf16 v[72:75], v[244:247], v[52:55], v[72:75]
	v_mfma_f32_16x16x32_bf16 v[84:87], v[240:243], v[52:55], v[84:87]
	ds_read_b128 v[240:243], v121 offset:12288
	ds_read_b128 v[244:247], v121 offset:13312
	v_mfma_f32_16x16x32_bf16 v[80:83], v[248:251], v[112:115], v[80:83]
	v_mfma_f32_16x16x32_bf16 v[76:79], v[252:255], v[112:115], v[76:79]
	v_mfma_f32_16x16x32_bf16 v[72:75], v[252:255], v[116:119], v[72:75]
	v_mfma_f32_16x16x32_bf16 v[84:87], v[248:251], v[116:119], v[84:87]
	ds_read_b128 v[248:251], v121 offset:14336
	ds_read_b128 v[252:255], v121 offset:15360
	s_setprio 3
	s_waitcnt lgkmcnt(6)
	v_mfma_f32_16x16x32_bf16 v[64:67], v[224:227], v[0:3], v[152:155]
	v_mfma_f32_16x16x32_bf16 v[68:71], v[228:231], v[0:3], v[156:159]
	v_mfma_f32_16x16x32_bf16 v[60:63], v[228:231], v[4:7], v[156:159]
	v_mfma_f32_16x16x32_bf16 v[56:59], v[224:227], v[4:7], v[152:155]
	ds_read_b128 v[224:227], v121 offset:16384
	ds_read_b128 v[228:231], v121 offset:17408
	s_waitcnt lgkmcnt(6)
	ds_read_b128 v[160:163], v183 offset:896
	ds_read_b128 v[164:167], v183 offset:960
	v_mfma_f32_16x16x32_bf16 v[64:67], v[232:235], v[12:15], v[64:67]
	v_cvt_pk_bf16_f32 v200, v80, v81
	v_mfma_f32_16x16x32_bf16 v[68:71], v[236:239], v[12:15], v[68:71]
	s_mov_b32 m0, s28
	s_add_i32 s51, s50, 0x18000
	v_cvt_pk_bf16_f32 v201, v82, v83
	v_mfma_f32_16x16x32_bf16 v[60:63], v[236:239], v[8:11], v[60:63]
	buffer_load_dwordx4 v125, s[36:39], s51 offen lds
	v_cvt_pk_bf16_f32 v202, v76, v77
	v_mfma_f32_16x16x32_bf16 v[56:59], v[232:235], v[8:11], v[56:59]
	v_cvt_pk_bf16_f32 v203, v78, v79
	ds_read_b128 v[232:235], v121 offset:18432
	ds_read_b128 v[236:239], v121 offset:19456
	s_waitcnt lgkmcnt(8)
	v_mfma_f32_16x16x32_bf16 v[64:67], v[240:243], v[16:19], v[64:67]
	v_cvt_pk_bf16_f32 v204, v84, v85
	v_mfma_f32_16x16x32_bf16 v[68:71], v[244:247], v[16:19], v[68:71]
	s_mov_b32 m0, s29
	s_add_i32 s51, s50, 0x1a000
	v_cvt_pk_bf16_f32 v205, v86, v87
	v_mfma_f32_16x16x32_bf16 v[60:63], v[244:247], v[20:23], v[60:63]
	buffer_load_dwordx4 v125, s[36:39], s51 offen lds
	v_cvt_pk_bf16_f32 v206, v72, v73
	v_mfma_f32_16x16x32_bf16 v[56:59], v[240:243], v[20:23], v[56:59]
	v_cvt_pk_bf16_f32 v207, v74, v75
	ds_read_b128 v[240:243], v121 offset:20480
	ds_read_b128 v[244:247], v121 offset:21504
	s_waitcnt lgkmcnt(8)
	v_mfma_f32_16x16x32_bf16 v[64:67], v[248:251], v[24:27], v[64:67]
	v_pk_max_i16 v200, v200, 0
	v_mfma_f32_16x16x32_bf16 v[68:71], v[252:255], v[24:27], v[68:71]
	s_mov_b32 m0, s33
	s_add_i32 s51, s50, 0x1c000
	v_pk_max_i16 v201, v201, 0
	v_mfma_f32_16x16x32_bf16 v[60:63], v[252:255], v[28:31], v[60:63]
	buffer_load_dwordx4 v125, s[36:39], s51 offen lds
	v_pk_max_i16 v202, v202, 0
	v_mfma_f32_16x16x32_bf16 v[56:59], v[248:251], v[28:31], v[56:59]
	v_pk_max_i16 v203, v203, 0
	ds_read_b128 v[248:251], v121 offset:22528
	ds_read_b128 v[252:255], v121 offset:23552
	s_setprio 2
	s_waitcnt lgkmcnt(8)
	v_mfma_f32_16x16x32_bf16 v[64:67], v[224:227], v[32:35], v[64:67]
	v_pk_max_i16 v204, v204, 0
	v_mfma_f32_16x16x32_bf16 v[68:71], v[228:231], v[32:35], v[68:71]
	s_mov_b32 m0, s34
	s_add_i32 s51, s50, 0x1e000
	v_pk_max_i16 v205, v205, 0
	v_mfma_f32_16x16x32_bf16 v[60:63], v[228:231], v[36:39], v[60:63]
	buffer_load_dwordx4 v125, s[36:39], s51 offen lds
	v_pk_max_i16 v206, v206, 0
	v_mfma_f32_16x16x32_bf16 v[56:59], v[224:227], v[36:39], v[56:59]
	v_pk_max_i16 v207, v207, 0
	ds_read_b128 v[224:227], v121 offset:24576
	ds_read_b128 v[228:231], v121 offset:25600
	s_waitcnt lgkmcnt(6)
	v_mfma_f32_16x16x32_bf16 v[64:67], v[232:235], v[40:43], v[64:67]
	v_mfma_f32_16x16x32_bf16 v[68:71], v[236:239], v[40:43], v[68:71]
	v_mfma_f32_16x16x32_bf16 v[60:63], v[236:239], v[44:47], v[60:63]
	v_mfma_f32_16x16x32_bf16 v[56:59], v[232:235], v[44:47], v[56:59]
	ds_read_b128 v[232:235], v121 offset:26624
	ds_read_b128 v[236:239], v121 offset:27648
	s_waitcnt lgkmcnt(6)
	ds_read_b128 v[152:155], v183 offset:1024
	ds_read_b128 v[156:159], v183 offset:1088
	v_mfma_f32_16x16x32_bf16 v[64:67], v[240:243], v[48:51], v[64:67]
	v_mfma_f32_16x16x32_bf16 v[68:71], v[244:247], v[48:51], v[68:71]
	v_mfma_f32_16x16x32_bf16 v[60:63], v[244:247], v[52:55], v[60:63]
	v_mfma_f32_16x16x32_bf16 v[56:59], v[240:243], v[52:55], v[56:59]
	ds_read_b128 v[240:243], v121 offset:28672
	ds_read_b128 v[244:247], v121 offset:29696
	s_waitcnt lgkmcnt(8)
	v_mfma_f32_16x16x32_bf16 v[64:67], v[248:251], v[112:115], v[64:67]
	v_mfma_f32_16x16x32_bf16 v[68:71], v[252:255], v[112:115], v[68:71]
	v_mfma_f32_16x16x32_bf16 v[60:63], v[252:255], v[116:119], v[60:63]
	v_mfma_f32_16x16x32_bf16 v[56:59], v[248:251], v[116:119], v[56:59]
	ds_read_b128 v[248:251], v121 offset:30720
	ds_read_b128 v[252:255], v121 offset:31744
	s_setprio 1
	s_waitcnt lgkmcnt(8)
	v_mfma_f32_16x16x32_bf16 v[80:83], v[224:227], v[0:3], v[160:163]
	v_mfma_f32_16x16x32_bf16 v[76:79], v[228:231], v[0:3], v[164:167]
	v_mfma_f32_16x16x32_bf16 v[72:75], v[228:231], v[4:7], v[164:167]
	v_mfma_f32_16x16x32_bf16 v[84:87], v[224:227], v[4:7], v[160:163]
	ds_read_b128 v[224:227], v121 offset:32768
	ds_read_b128 v[228:231], v121 offset:33792
	s_waitcnt lgkmcnt(8)
	v_mfma_f32_16x16x32_bf16 v[80:83], v[232:235], v[12:15], v[80:83]
	v_cvt_pk_bf16_f32 v208, v64, v65
	v_mfma_f32_16x16x32_bf16 v[76:79], v[236:239], v[12:15], v[76:79]
	v_cvt_pk_bf16_f32 v209, v66, v67
	v_mfma_f32_16x16x32_bf16 v[72:75], v[236:239], v[8:11], v[72:75]
	v_cvt_pk_bf16_f32 v210, v68, v69
	v_mfma_f32_16x16x32_bf16 v[84:87], v[232:235], v[8:11], v[84:87]
	v_cvt_pk_bf16_f32 v211, v70, v71
	ds_read_b128 v[232:235], v121 offset:34816
	ds_read_b128 v[236:239], v121 offset:35840
	s_waitcnt lgkmcnt(6)
	v_mfma_f32_16x16x32_bf16 v[80:83], v[240:243], v[16:19], v[80:83]
	v_cvt_pk_bf16_f32 v212, v56, v57
	v_mfma_f32_16x16x32_bf16 v[76:79], v[244:247], v[16:19], v[76:79]
	v_cvt_pk_bf16_f32 v213, v58, v59
	v_mfma_f32_16x16x32_bf16 v[72:75], v[244:247], v[20:23], v[72:75]
	v_cvt_pk_bf16_f32 v214, v60, v61
	v_mfma_f32_16x16x32_bf16 v[84:87], v[240:243], v[20:23], v[84:87]
	v_cvt_pk_bf16_f32 v215, v62, v63
	ds_read_b128 v[240:243], v121 offset:36864
	ds_read_b128 v[244:247], v121 offset:37888
	s_waitcnt lgkmcnt(6)
	v_mfma_f32_16x16x32_bf16 v[80:83], v[248:251], v[24:27], v[80:83]
	v_pk_max_i16 v208, v208, 0
	v_mfma_f32_16x16x32_bf16 v[76:79], v[252:255], v[24:27], v[76:79]
	v_pk_max_i16 v209, v209, 0
	v_mfma_f32_16x16x32_bf16 v[72:75], v[252:255], v[28:31], v[72:75]
	v_pk_max_i16 v210, v210, 0
	v_mfma_f32_16x16x32_bf16 v[84:87], v[248:251], v[28:31], v[84:87]
	v_pk_max_i16 v211, v211, 0
	ds_read_b128 v[248:251], v121 offset:38912
	ds_read_b128 v[252:255], v121 offset:39936
	s_setprio 0
	s_waitcnt lgkmcnt(6)
	v_mfma_f32_16x16x32_bf16 v[80:83], v[224:227], v[32:35], v[80:83]
	v_pk_max_i16 v212, v212, 0
	v_mfma_f32_16x16x32_bf16 v[76:79], v[228:231], v[32:35], v[76:79]
	v_pk_max_i16 v213, v213, 0
	v_mfma_f32_16x16x32_bf16 v[72:75], v[228:231], v[36:39], v[72:75]
	v_pk_max_i16 v214, v214, 0
	v_mfma_f32_16x16x32_bf16 v[84:87], v[224:227], v[36:39], v[84:87]
	v_pk_max_i16 v215, v215, 0
	s_waitcnt lgkmcnt(4)
	v_mfma_f32_16x16x32_bf16 v[80:83], v[232:235], v[40:43], v[80:83]
	v_mfma_f32_16x16x32_bf16 v[76:79], v[236:239], v[40:43], v[76:79]
	v_mfma_f32_16x16x32_bf16 v[72:75], v[236:239], v[44:47], v[72:75]
	v_mfma_f32_16x16x32_bf16 v[84:87], v[232:235], v[44:47], v[84:87]
	s_cmp_eq_u32 s52, 3
	s_cbranch_scc1 .Lnerf_head
.Lnerf_hid_a4:
	s_waitcnt vmcnt(0) lgkmcnt(0)
	s_barrier
	ds_read_b128 v[224:227], v121 offset:40960
	ds_read_b128 v[228:231], v121 offset:41984
	v_mfma_f32_16x16x32_bf16 v[80:83], v[240:243], v[48:51], v[80:83]
	ds_read_b128 v[232:235], v121 offset:43008
	v_mfma_f32_16x16x32_bf16 v[76:79], v[244:247], v[48:51], v[76:79]
	ds_read_b128 v[236:239], v121 offset:44032
	v_mfma_f32_16x16x32_bf16 v[72:75], v[244:247], v[52:55], v[72:75]
	v_mfma_f32_16x16x32_bf16 v[84:87], v[240:243], v[52:55], v[84:87]
	ds_read_b128 v[240:243], v121 offset:45056
	ds_read_b128 v[244:247], v121 offset:46080
	v_mfma_f32_16x16x32_bf16 v[80:83], v[248:251], v[112:115], v[80:83]
	v_mfma_f32_16x16x32_bf16 v[76:79], v[252:255], v[112:115], v[76:79]
	v_mfma_f32_16x16x32_bf16 v[72:75], v[252:255], v[116:119], v[72:75]
	v_mfma_f32_16x16x32_bf16 v[84:87], v[248:251], v[116:119], v[84:87]
	ds_read_b128 v[248:251], v121 offset:47104
	ds_read_b128 v[252:255], v121 offset:48128
	s_setprio 3
	s_waitcnt lgkmcnt(6)
	v_mfma_f32_16x16x32_bf16 v[64:67], v[224:227], v[88:91], v[152:155]
	v_mfma_f32_16x16x32_bf16 v[68:71], v[228:231], v[88:91], v[156:159]
	v_mfma_f32_16x16x32_bf16 v[60:63], v[228:231], v[92:95], v[156:159]
	v_mfma_f32_16x16x32_bf16 v[56:59], v[224:227], v[92:95], v[152:155]
	ds_read_b128 v[224:227], v121 offset:49152
	ds_read_b128 v[228:231], v121 offset:50176
	s_waitcnt lgkmcnt(6)
	ds_read_b128 v[160:163], v183 offset:1152
	ds_read_b128 v[164:167], v183 offset:1216
	v_mfma_f32_16x16x32_bf16 v[64:67], v[232:235], v[96:99], v[64:67]
	v_cvt_pk_bf16_f32 v216, v80, v81
	v_mfma_f32_16x16x32_bf16 v[68:71], v[236:239], v[96:99], v[68:71]
	s_mov_b32 m0, s35
	s_add_i32 s51, s50, 0x20000
	v_cvt_pk_bf16_f32 v217, v82, v83
	v_mfma_f32_16x16x32_bf16 v[60:63], v[236:239], v[100:103], v[60:63]
	buffer_load_dwordx4 v125, s[36:39], s51 offen lds
	v_cvt_pk_bf16_f32 v218, v76, v77
	v_mfma_f32_16x16x32_bf16 v[56:59], v[232:235], v[100:103], v[56:59]
	v_cvt_pk_bf16_f32 v219, v78, v79
	ds_read_b128 v[232:235], v121 offset:51200
	ds_read_b128 v[236:239], v121 offset:52224
	s_waitcnt lgkmcnt(8)
	v_mfma_f32_16x16x32_bf16 v[64:67], v[240:243], v[104:107], v[64:67]
	v_cvt_pk_bf16_f32 v220, v84, v85
	v_mfma_f32_16x16x32_bf16 v[68:71], v[244:247], v[104:107], v[68:71]
	s_mov_b32 m0, s42
	s_add_i32 s51, s50, 0x22000
	v_cvt_pk_bf16_f32 v221, v86, v87
	v_mfma_f32_16x16x32_bf16 v[60:63], v[244:247], v[108:111], v[60:63]
	buffer_load_dwordx4 v125, s[36:39], s51 offen lds
	v_cvt_pk_bf16_f32 v222, v72, v73
	v_mfma_f32_16x16x32_bf16 v[56:59], v[240:243], v[108:111], v[56:59]
	v_cvt_pk_bf16_f32 v223, v74, v75
	ds_read_b128 v[240:243], v121 offset:53248
	ds_read_b128 v[244:247], v121 offset:54272
	s_waitcnt lgkmcnt(8)
	v_mfma_f32_16x16x32_bf16 v[64:67], v[248:251], v[184:187], v[64:67]
	v_pk_max_i16 v216, v216, 0
	v_mfma_f32_16x16x32_bf16 v[68:71], v[252:255], v[184:187], v[68:71]
	s_mov_b32 m0, s41
	s_add_i32 s51, s50, 0x24000
	v_pk_max_i16 v217, v217, 0
	v_mfma_f32_16x16x32_bf16 v[60:63], v[252:255], v[188:191], v[60:63]
	buffer_load_dwordx4 v125, s[36:39], s51 offen lds
	v_pk_max_i16 v218, v218, 0
	v_mfma_f32_16x16x32_bf16 v[56:59], v[248:251], v[188:191], v[56:59]
	v_pk_max_i16 v219, v219, 0
	ds_read_b128 v[248:251], v121 offset:55296
	ds_read_b128 v[252:255], v121 offset:56320
	s_setprio 2
	s_waitcnt lgkmcnt(8)
	v_mfma_f32_16x16x32_bf16 v[64:67], v[224:227], v[192:195], v[64:67]
	v_pk_max_i16 v220, v220, 0
	v_mfma_f32_16x16x32_bf16 v[68:71], v[228:231], v[192:195], v[68:71]
	s_mov_b32 m0, s40
	s_add_i32 s51, s50, 0x26000
	v_pk_max_i16 v221, v221, 0
	v_mfma_f32_16x16x32_bf16 v[60:63], v[228:231], v[196:199], v[60:63]
	buffer_load_dwordx4 v125, s[36:39], s51 offen lds
	v_pk_max_i16 v222, v222, 0
	v_mfma_f32_16x16x32_bf16 v[56:59], v[224:227], v[196:199], v[56:59]
	v_pk_max_i16 v223, v223, 0
	ds_read_b128 v[224:227], v121 offset:57344
	ds_read_b128 v[228:231], v121 offset:58368
	s_waitcnt lgkmcnt(6)
	v_mfma_f32_16x16x32_bf16 v[64:67], v[232:235], v[200:203], v[64:67]
	v_mfma_f32_16x16x32_bf16 v[68:71], v[236:239], v[200:203], v[68:71]
	v_mfma_f32_16x16x32_bf16 v[60:63], v[236:239], v[204:207], v[60:63]
	v_mfma_f32_16x16x32_bf16 v[56:59], v[232:235], v[204:207], v[56:59]
	ds_read_b128 v[232:235], v121 offset:59392
	ds_read_b128 v[236:239], v121 offset:60416
	s_waitcnt lgkmcnt(6)
	ds_read_b128 v[152:155], v183 offset:1280
	ds_read_b128 v[156:159], v183 offset:1344
	v_mfma_f32_16x16x32_bf16 v[64:67], v[240:243], v[208:211], v[64:67]
	v_mfma_f32_16x16x32_bf16 v[68:71], v[244:247], v[208:211], v[68:71]
	v_mfma_f32_16x16x32_bf16 v[60:63], v[244:247], v[212:215], v[60:63]
	v_mfma_f32_16x16x32_bf16 v[56:59], v[240:243], v[212:215], v[56:59]
	ds_read_b128 v[240:243], v121 offset:61440
	ds_read_b128 v[244:247], v121 offset:62464
	s_waitcnt lgkmcnt(8)
	v_mfma_f32_16x16x32_bf16 v[64:67], v[248:251], v[216:219], v[64:67]
	v_mfma_f32_16x16x32_bf16 v[68:71], v[252:255], v[216:219], v[68:71]
	v_mfma_f32_16x16x32_bf16 v[60:63], v[252:255], v[220:223], v[60:63]
	v_mfma_f32_16x16x32_bf16 v[56:59], v[248:251], v[220:223], v[56:59]
	ds_read_b128 v[248:251], v121 offset:63488
	ds_read_b128 v[252:255], v121 offset:64512
	s_setprio 1
	s_waitcnt lgkmcnt(8)
	v_mfma_f32_16x16x32_bf16 v[80:83], v[224:227], v[88:91], v[160:163]
	v_mfma_f32_16x16x32_bf16 v[76:79], v[228:231], v[88:91], v[164:167]
	v_mfma_f32_16x16x32_bf16 v[72:75], v[228:231], v[92:95], v[164:167]
	v_mfma_f32_16x16x32_bf16 v[84:87], v[224:227], v[92:95], v[160:163]
	ds_read_b128 v[224:227], v126 offset:57344
	ds_read_b128 v[228:231], v126 offset:58368
	s_waitcnt lgkmcnt(8)
	v_mfma_f32_16x16x32_bf16 v[80:83], v[232:235], v[96:99], v[80:83]
	v_cvt_pk_bf16_f32 v0, v64, v65
	v_mfma_f32_16x16x32_bf16 v[76:79], v[236:239], v[96:99], v[76:79]
	v_cvt_pk_bf16_f32 v1, v66, v67
	v_mfma_f32_16x16x32_bf16 v[72:75], v[236:239], v[100:103], v[72:75]
	v_cvt_pk_bf16_f32 v2, v68, v69
	v_mfma_f32_16x16x32_bf16 v[84:87], v[232:235], v[100:103], v[84:87]
	v_cvt_pk_bf16_f32 v3, v70, v71
	ds_read_b128 v[232:235], v126 offset:59392
	ds_read_b128 v[236:239], v126 offset:60416
	s_waitcnt lgkmcnt(6)
	v_mfma_f32_16x16x32_bf16 v[80:83], v[240:243], v[104:107], v[80:83]
	v_cvt_pk_bf16_f32 v4, v56, v57
	v_mfma_f32_16x16x32_bf16 v[76:79], v[244:247], v[104:107], v[76:79]
	v_cvt_pk_bf16_f32 v5, v58, v59
	v_mfma_f32_16x16x32_bf16 v[72:75], v[244:247], v[108:111], v[72:75]
	v_cvt_pk_bf16_f32 v6, v60, v61
	v_mfma_f32_16x16x32_bf16 v[84:87], v[240:243], v[108:111], v[84:87]
	v_cvt_pk_bf16_f32 v7, v62, v63
	ds_read_b128 v[240:243], v126 offset:61440
	ds_read_b128 v[244:247], v126 offset:62464
	s_waitcnt lgkmcnt(6)
	v_mfma_f32_16x16x32_bf16 v[80:83], v[248:251], v[184:187], v[80:83]
	v_pk_max_i16 v0, v0, 0
	v_mfma_f32_16x16x32_bf16 v[76:79], v[252:255], v[184:187], v[76:79]
	v_pk_max_i16 v1, v1, 0
	v_mfma_f32_16x16x32_bf16 v[72:75], v[252:255], v[188:191], v[72:75]
	v_pk_max_i16 v2, v2, 0
	v_mfma_f32_16x16x32_bf16 v[84:87], v[248:251], v[188:191], v[84:87]
	v_pk_max_i16 v3, v3, 0
	ds_read_b128 v[248:251], v126 offset:63488
	ds_read_b128 v[252:255], v126 offset:64512
	s_setprio 0
	s_waitcnt lgkmcnt(6)
	v_mfma_f32_16x16x32_bf16 v[80:83], v[224:227], v[192:195], v[80:83]
	v_pk_max_i16 v4, v4, 0
	v_mfma_f32_16x16x32_bf16 v[76:79], v[228:231], v[192:195], v[76:79]
	v_pk_max_i16 v5, v5, 0
	v_mfma_f32_16x16x32_bf16 v[72:75], v[228:231], v[196:199], v[72:75]
	v_pk_max_i16 v6, v6, 0
	v_mfma_f32_16x16x32_bf16 v[84:87], v[224:227], v[196:199], v[84:87]
	v_pk_max_i16 v7, v7, 0
	s_waitcnt lgkmcnt(4)
	v_mfma_f32_16x16x32_bf16 v[80:83], v[232:235], v[200:203], v[80:83]
	v_mfma_f32_16x16x32_bf16 v[76:79], v[236:239], v[200:203], v[76:79]
	v_mfma_f32_16x16x32_bf16 v[72:75], v[236:239], v[204:207], v[72:75]
	v_mfma_f32_16x16x32_bf16 v[84:87], v[232:235], v[204:207], v[84:87]
.Lnerf_hid_a5:
	s_waitcnt vmcnt(0) lgkmcnt(0)
	s_barrier
	ds_read_b128 v[224:227], v121 offset:8192
	ds_read_b128 v[228:231], v121 offset:9216
	v_mfma_f32_16x16x32_bf16 v[80:83], v[240:243], v[208:211], v[80:83]
	ds_read_b128 v[232:235], v121 offset:10240
	v_mfma_f32_16x16x32_bf16 v[76:79], v[244:247], v[208:211], v[76:79]
	ds_read_b128 v[236:239], v121 offset:11264
	v_mfma_f32_16x16x32_bf16 v[72:75], v[244:247], v[212:215], v[72:75]
	v_mfma_f32_16x16x32_bf16 v[84:87], v[240:243], v[212:215], v[84:87]
	ds_read_b128 v[240:243], v121 offset:12288
	ds_read_b128 v[244:247], v121 offset:13312
	v_mfma_f32_16x16x32_bf16 v[80:83], v[248:251], v[216:219], v[80:83]
	v_mfma_f32_16x16x32_bf16 v[76:79], v[252:255], v[216:219], v[76:79]
	v_mfma_f32_16x16x32_bf16 v[72:75], v[252:255], v[220:223], v[72:75]
	v_mfma_f32_16x16x32_bf16 v[84:87], v[248:251], v[220:223], v[84:87]
	ds_read_b128 v[248:251], v121 offset:14336
	ds_read_b128 v[252:255], v121 offset:15360
	s_setprio 3
	s_waitcnt lgkmcnt(6)
	v_mfma_f32_16x16x32_bf16 v[64:67], v[224:227], v[88:91], v[152:155]
	v_mfma_f32_16x16x32_bf16 v[68:71], v[228:231], v[88:91], v[156:159]
	v_mfma_f32_16x16x32_bf16 v[60:63], v[228:231], v[92:95], v[156:159]
	v_mfma_f32_16x16x32_bf16 v[56:59], v[224:227], v[92:95], v[152:155]
	ds_read_b128 v[224:227], v121 offset:16384
	ds_read_b128 v[228:231], v121 offset:17408
	s_waitcnt lgkmcnt(6)
	ds_read_b128 v[160:163], v183 offset:1408
	ds_read_b128 v[164:167], v183 offset:1472
	v_mfma_f32_16x16x32_bf16 v[64:67], v[232:235], v[96:99], v[64:67]
	v_cvt_pk_bf16_f32 v12, v80, v81
	v_mfma_f32_16x16x32_bf16 v[68:71], v[236:239], v[96:99], v[68:71]
	s_mov_b32 m0, s28
	s_add_i32 s51, s50, 0x28000
	v_cvt_pk_bf16_f32 v13, v82, v83
	v_mfma_f32_16x16x32_bf16 v[60:63], v[236:239], v[100:103], v[60:63]
	buffer_load_dwordx4 v125, s[36:39], s51 offen lds
	v_cvt_pk_bf16_f32 v14, v76, v77
	v_mfma_f32_16x16x32_bf16 v[56:59], v[232:235], v[100:103], v[56:59]
	v_cvt_pk_bf16_f32 v15, v78, v79
	ds_read_b128 v[232:235], v121 offset:18432
	ds_read_b128 v[236:239], v121 offset:19456
	s_waitcnt lgkmcnt(8)
	v_mfma_f32_16x16x32_bf16 v[64:67], v[240:243], v[104:107], v[64:67]
	v_cvt_pk_bf16_f32 v8, v84, v85
	v_mfma_f32_16x16x32_bf16 v[68:71], v[244:247], v[104:107], v[68:71]
	s_mov_b32 m0, s29
	s_add_i32 s51, s50, 0x2a000
	v_cvt_pk_bf16_f32 v9, v86, v87
	v_mfma_f32_16x16x32_bf16 v[60:63], v[244:247], v[108:111], v[60:63]
	buffer_load_dwordx4 v125, s[36:39], s51 offen lds
	v_cvt_pk_bf16_f32 v10, v72, v73
	v_mfma_f32_16x16x32_bf16 v[56:59], v[240:243], v[108:111], v[56:59]
	v_cvt_pk_bf16_f32 v11, v74, v75
	ds_read_b128 v[240:243], v121 offset:20480
	ds_read_b128 v[244:247], v121 offset:21504
	s_waitcnt lgkmcnt(8)
	v_mfma_f32_16x16x32_bf16 v[64:67], v[248:251], v[184:187], v[64:67]
	v_pk_max_i16 v12, v12, 0
	v_mfma_f32_16x16x32_bf16 v[68:71], v[252:255], v[184:187], v[68:71]
	s_mov_b32 m0, s33
	s_add_i32 s51, s50, 0x2c000
	v_pk_max_i16 v13, v13, 0
	v_mfma_f32_16x16x32_bf16 v[60:63], v[252:255], v[188:191], v[60:63]
	buffer_load_dwordx4 v125, s[36:39], s51 offen lds
	v_pk_max_i16 v14, v14, 0
	v_mfma_f32_16x16x32_bf16 v[56:59], v[248:251], v[188:191], v[56:59]
	v_pk_max_i16 v15, v15, 0
	ds_read_b128 v[248:251], v121 offset:22528
	ds_read_b128 v[252:255], v121 offset:23552
	s_setprio 2
	s_waitcnt lgkmcnt(8)
	v_mfma_f32_16x16x32_bf16 v[64:67], v[224:227], v[192:195], v[64:67]
	v_pk_max_i16 v8, v8, 0
	v_mfma_f32_16x16x32_bf16 v[68:71], v[228:231], v[192:195], v[68:71]
	s_mov_b32 m0, s34
	s_add_i32 s51, s50, 0x2e000
	v_pk_max_i16 v9, v9, 0
	v_mfma_f32_16x16x32_bf16 v[60:63], v[228:231], v[196:199], v[60:63]
	buffer_load_dwordx4 v125, s[36:39], s51 offen lds
	v_pk_max_i16 v10, v10, 0
	v_mfma_f32_16x16x32_bf16 v[56:59], v[224:227], v[196:199], v[56:59]
	v_pk_max_i16 v11, v11, 0
	ds_read_b128 v[224:227], v121 offset:24576
	ds_read_b128 v[228:231], v121 offset:25600
	s_waitcnt lgkmcnt(6)
	v_mfma_f32_16x16x32_bf16 v[64:67], v[232:235], v[200:203], v[64:67]
	v_mfma_f32_16x16x32_bf16 v[68:71], v[236:239], v[200:203], v[68:71]
	v_mfma_f32_16x16x32_bf16 v[60:63], v[236:239], v[204:207], v[60:63]
	v_mfma_f32_16x16x32_bf16 v[56:59], v[232:235], v[204:207], v[56:59]
	ds_read_b128 v[232:235], v121 offset:26624
	ds_read_b128 v[236:239], v121 offset:27648
	s_waitcnt lgkmcnt(6)
	ds_read_b128 v[152:155], v183 offset:1536
	ds_read_b128 v[156:159], v183 offset:1600
	v_mfma_f32_16x16x32_bf16 v[64:67], v[240:243], v[208:211], v[64:67]
	v_mfma_f32_16x16x32_bf16 v[68:71], v[244:247], v[208:211], v[68:71]
	v_mfma_f32_16x16x32_bf16 v[60:63], v[244:247], v[212:215], v[60:63]
	v_mfma_f32_16x16x32_bf16 v[56:59], v[240:243], v[212:215], v[56:59]
	ds_read_b128 v[240:243], v121 offset:28672
	ds_read_b128 v[244:247], v121 offset:29696
	s_waitcnt lgkmcnt(8)
	v_mfma_f32_16x16x32_bf16 v[64:67], v[248:251], v[216:219], v[64:67]
	v_mfma_f32_16x16x32_bf16 v[68:71], v[252:255], v[216:219], v[68:71]
	v_mfma_f32_16x16x32_bf16 v[60:63], v[252:255], v[220:223], v[60:63]
	v_mfma_f32_16x16x32_bf16 v[56:59], v[248:251], v[220:223], v[56:59]
	ds_read_b128 v[248:251], v121 offset:30720
	ds_read_b128 v[252:255], v121 offset:31744
	s_setprio 1
	s_waitcnt lgkmcnt(8)
	v_mfma_f32_16x16x32_bf16 v[80:83], v[224:227], v[88:91], v[160:163]
	v_mfma_f32_16x16x32_bf16 v[76:79], v[228:231], v[88:91], v[164:167]
	v_mfma_f32_16x16x32_bf16 v[72:75], v[228:231], v[92:95], v[164:167]
	v_mfma_f32_16x16x32_bf16 v[84:87], v[224:227], v[92:95], v[160:163]
	ds_read_b128 v[224:227], v121 offset:32768
	ds_read_b128 v[228:231], v121 offset:33792
	s_waitcnt lgkmcnt(8)
	v_mfma_f32_16x16x32_bf16 v[80:83], v[232:235], v[96:99], v[80:83]
	v_cvt_pk_bf16_f32 v16, v64, v65
	v_mfma_f32_16x16x32_bf16 v[76:79], v[236:239], v[96:99], v[76:79]
	v_cvt_pk_bf16_f32 v17, v66, v67
	v_mfma_f32_16x16x32_bf16 v[72:75], v[236:239], v[100:103], v[72:75]
	v_cvt_pk_bf16_f32 v18, v68, v69
	v_mfma_f32_16x16x32_bf16 v[84:87], v[232:235], v[100:103], v[84:87]
	v_cvt_pk_bf16_f32 v19, v70, v71
	ds_read_b128 v[232:235], v121 offset:34816
	ds_read_b128 v[236:239], v121 offset:35840
	s_waitcnt lgkmcnt(6)
	v_mfma_f32_16x16x32_bf16 v[80:83], v[240:243], v[104:107], v[80:83]
	v_cvt_pk_bf16_f32 v20, v56, v57
	v_mfma_f32_16x16x32_bf16 v[76:79], v[244:247], v[104:107], v[76:79]
	v_cvt_pk_bf16_f32 v21, v58, v59
	v_mfma_f32_16x16x32_bf16 v[72:75], v[244:247], v[108:111], v[72:75]
	v_cvt_pk_bf16_f32 v22, v60, v61
	v_mfma_f32_16x16x32_bf16 v[84:87], v[240:243], v[108:111], v[84:87]
	v_cvt_pk_bf16_f32 v23, v62, v63
	ds_read_b128 v[240:243], v121 offset:36864
	ds_read_b128 v[244:247], v121 offset:37888
	s_waitcnt lgkmcnt(6)
	v_mfma_f32_16x16x32_bf16 v[80:83], v[248:251], v[184:187], v[80:83]
	v_pk_max_i16 v16, v16, 0
	v_mfma_f32_16x16x32_bf16 v[76:79], v[252:255], v[184:187], v[76:79]
	v_pk_max_i16 v17, v17, 0
	v_mfma_f32_16x16x32_bf16 v[72:75], v[252:255], v[188:191], v[72:75]
	v_pk_max_i16 v18, v18, 0
	v_mfma_f32_16x16x32_bf16 v[84:87], v[248:251], v[188:191], v[84:87]
	v_pk_max_i16 v19, v19, 0
	ds_read_b128 v[248:251], v121 offset:38912
	ds_read_b128 v[252:255], v121 offset:39936
	s_setprio 0
	s_waitcnt lgkmcnt(6)
	v_mfma_f32_16x16x32_bf16 v[80:83], v[224:227], v[192:195], v[80:83]
	v_pk_max_i16 v20, v20, 0
	v_mfma_f32_16x16x32_bf16 v[76:79], v[228:231], v[192:195], v[76:79]
	v_pk_max_i16 v21, v21, 0
	v_mfma_f32_16x16x32_bf16 v[72:75], v[228:231], v[196:199], v[72:75]
	v_pk_max_i16 v22, v22, 0
	v_mfma_f32_16x16x32_bf16 v[84:87], v[224:227], v[196:199], v[84:87]
	v_pk_max_i16 v23, v23, 0
	s_waitcnt lgkmcnt(4)
	v_mfma_f32_16x16x32_bf16 v[80:83], v[232:235], v[200:203], v[80:83]
	v_mfma_f32_16x16x32_bf16 v[76:79], v[236:239], v[200:203], v[76:79]
	v_mfma_f32_16x16x32_bf16 v[72:75], v[236:239], v[204:207], v[72:75]
	v_mfma_f32_16x16x32_bf16 v[84:87], v[232:235], v[204:207], v[84:87]
.Lnerf_hid_a6:
	s_waitcnt vmcnt(0) lgkmcnt(0)
	s_barrier
	ds_read_b128 v[224:227], v121 offset:40960
	ds_read_b128 v[228:231], v121 offset:41984
	v_mfma_f32_16x16x32_bf16 v[80:83], v[240:243], v[208:211], v[80:83]
	ds_read_b128 v[232:235], v121 offset:43008
	v_mfma_f32_16x16x32_bf16 v[76:79], v[244:247], v[208:211], v[76:79]
	ds_read_b128 v[236:239], v121 offset:44032
	v_mfma_f32_16x16x32_bf16 v[72:75], v[244:247], v[212:215], v[72:75]
	v_mfma_f32_16x16x32_bf16 v[84:87], v[240:243], v[212:215], v[84:87]
	ds_read_b128 v[240:243], v121 offset:45056
	ds_read_b128 v[244:247], v121 offset:46080
	v_mfma_f32_16x16x32_bf16 v[80:83], v[248:251], v[216:219], v[80:83]
	v_mfma_f32_16x16x32_bf16 v[76:79], v[252:255], v[216:219], v[76:79]
	v_mfma_f32_16x16x32_bf16 v[72:75], v[252:255], v[220:223], v[72:75]
	v_mfma_f32_16x16x32_bf16 v[84:87], v[248:251], v[220:223], v[84:87]
	ds_read_b128 v[248:251], v121 offset:47104
	ds_read_b128 v[252:255], v121 offset:48128
	s_setprio 3
	s_waitcnt lgkmcnt(6)
	v_mfma_f32_16x16x32_bf16 v[64:67], v[224:227], v[88:91], v[152:155]
	v_mfma_f32_16x16x32_bf16 v[68:71], v[228:231], v[88:91], v[156:159]
	v_mfma_f32_16x16x32_bf16 v[60:63], v[228:231], v[92:95], v[156:159]
	v_mfma_f32_16x16x32_bf16 v[56:59], v[224:227], v[92:95], v[152:155]
	ds_read_b128 v[224:227], v121 offset:49152
	ds_read_b128 v[228:231], v121 offset:50176
	s_waitcnt lgkmcnt(6)
	ds_read_b128 v[160:163], v183 offset:1664
	ds_read_b128 v[164:167], v183 offset:1728
	v_mfma_f32_16x16x32_bf16 v[64:67], v[232:235], v[96:99], v[64:67]
	v_cvt_pk_bf16_f32 v24, v80, v81
	v_mfma_f32_16x16x32_bf16 v[68:71], v[236:239], v[96:99], v[68:71]
	s_mov_b32 m0, s35
	s_add_i32 s51, s50, 0x30000
	v_cvt_pk_bf16_f32 v25, v82, v83
	v_mfma_f32_16x16x32_bf16 v[60:63], v[236:239], v[100:103], v[60:63]
	buffer_load_dwordx4 v125, s[36:39], s51 offen lds
	v_cvt_pk_bf16_f32 v26, v76, v77
	v_mfma_f32_16x16x32_bf16 v[56:59], v[232:235], v[100:103], v[56:59]
	v_cvt_pk_bf16_f32 v27, v78, v79
	ds_read_b128 v[232:235], v121 offset:51200
	ds_read_b128 v[236:239], v121 offset:52224
	s_waitcnt lgkmcnt(8)
	v_mfma_f32_16x16x32_bf16 v[64:67], v[240:243], v[104:107], v[64:67]
	v_cvt_pk_bf16_f32 v28, v84, v85
	v_mfma_f32_16x16x32_bf16 v[68:71], v[244:247], v[104:107], v[68:71]
	s_mov_b32 m0, s42
	s_add_i32 s51, s50, 0x32000
	v_cvt_pk_bf16_f32 v29, v86, v87
	v_mfma_f32_16x16x32_bf16 v[60:63], v[244:247], v[108:111], v[60:63]
	buffer_load_dwordx4 v125, s[36:39], s51 offen lds
	v_cvt_pk_bf16_f32 v30, v72, v73
	v_mfma_f32_16x16x32_bf16 v[56:59], v[240:243], v[108:111], v[56:59]
	v_cvt_pk_bf16_f32 v31, v74, v75
	ds_read_b128 v[240:243], v121 offset:53248
	ds_read_b128 v[244:247], v121 offset:54272
	s_waitcnt lgkmcnt(8)
	v_mfma_f32_16x16x32_bf16 v[64:67], v[248:251], v[184:187], v[64:67]
	v_pk_max_i16 v24, v24, 0
	v_mfma_f32_16x16x32_bf16 v[68:71], v[252:255], v[184:187], v[68:71]
	s_mov_b32 m0, s41
	s_add_i32 s51, s50, 0x34000
	v_pk_max_i16 v25, v25, 0
	v_mfma_f32_16x16x32_bf16 v[60:63], v[252:255], v[188:191], v[60:63]
	buffer_load_dwordx4 v125, s[36:39], s51 offen lds
	v_pk_max_i16 v26, v26, 0
	v_mfma_f32_16x16x32_bf16 v[56:59], v[248:251], v[188:191], v[56:59]
	v_pk_max_i16 v27, v27, 0
	ds_read_b128 v[248:251], v121 offset:55296
	ds_read_b128 v[252:255], v121 offset:56320
	s_setprio 2
	s_waitcnt lgkmcnt(8)
	v_mfma_f32_16x16x32_bf16 v[64:67], v[224:227], v[192:195], v[64:67]
	v_pk_max_i16 v28, v28, 0
	v_mfma_f32_16x16x32_bf16 v[68:71], v[228:231], v[192:195], v[68:71]
	s_mov_b32 m0, s40
	s_add_i32 s51, s50, 0x36000
	v_pk_max_i16 v29, v29, 0
	v_mfma_f32_16x16x32_bf16 v[60:63], v[228:231], v[196:199], v[60:63]
	buffer_load_dwordx4 v125, s[36:39], s51 offen lds
	v_pk_max_i16 v30, v30, 0
	v_mfma_f32_16x16x32_bf16 v[56:59], v[224:227], v[196:199], v[56:59]
	v_pk_max_i16 v31, v31, 0
	ds_read_b128 v[224:227], v121 offset:57344
	ds_read_b128 v[228:231], v121 offset:58368
	s_waitcnt lgkmcnt(6)
	v_mfma_f32_16x16x32_bf16 v[64:67], v[232:235], v[200:203], v[64:67]
	v_mfma_f32_16x16x32_bf16 v[68:71], v[236:239], v[200:203], v[68:71]
	v_mfma_f32_16x16x32_bf16 v[60:63], v[236:239], v[204:207], v[60:63]
	v_mfma_f32_16x16x32_bf16 v[56:59], v[232:235], v[204:207], v[56:59]
	ds_read_b128 v[232:235], v121 offset:59392
	ds_read_b128 v[236:239], v121 offset:60416
	s_waitcnt lgkmcnt(6)
	ds_read_b128 v[152:155], v183 offset:1792
	ds_read_b128 v[156:159], v183 offset:1856
	v_mfma_f32_16x16x32_bf16 v[64:67], v[240:243], v[208:211], v[64:67]
	v_mfma_f32_16x16x32_bf16 v[68:71], v[244:247], v[208:211], v[68:71]
	v_mfma_f32_16x16x32_bf16 v[60:63], v[244:247], v[212:215], v[60:63]
	v_mfma_f32_16x16x32_bf16 v[56:59], v[240:243], v[212:215], v[56:59]
	ds_read_b128 v[240:243], v121 offset:61440
	ds_read_b128 v[244:247], v121 offset:62464
	s_waitcnt lgkmcnt(8)
	v_mfma_f32_16x16x32_bf16 v[64:67], v[248:251], v[216:219], v[64:67]
	v_mfma_f32_16x16x32_bf16 v[68:71], v[252:255], v[216:219], v[68:71]
	v_mfma_f32_16x16x32_bf16 v[60:63], v[252:255], v[220:223], v[60:63]
	v_mfma_f32_16x16x32_bf16 v[56:59], v[248:251], v[220:223], v[56:59]
	ds_read_b128 v[248:251], v121 offset:63488
	ds_read_b128 v[252:255], v121 offset:64512
	s_setprio 1
	s_waitcnt lgkmcnt(8)
	v_mfma_f32_16x16x32_bf16 v[80:83], v[224:227], v[88:91], v[160:163]
	v_mfma_f32_16x16x32_bf16 v[76:79], v[228:231], v[88:91], v[164:167]
	v_mfma_f32_16x16x32_bf16 v[72:75], v[228:231], v[92:95], v[164:167]
	v_mfma_f32_16x16x32_bf16 v[84:87], v[224:227], v[92:95], v[160:163]
	ds_read_b128 v[224:227], v126 offset:57344
	ds_read_b128 v[228:231], v126 offset:58368
	s_waitcnt lgkmcnt(8)
	v_mfma_f32_16x16x32_bf16 v[80:83], v[232:235], v[96:99], v[80:83]
	v_cvt_pk_bf16_f32 v32, v64, v65
	v_mfma_f32_16x16x32_bf16 v[76:79], v[236:239], v[96:99], v[76:79]
	v_cvt_pk_bf16_f32 v33, v66, v67
	v_mfma_f32_16x16x32_bf16 v[72:75], v[236:239], v[100:103], v[72:75]
	v_cvt_pk_bf16_f32 v34, v68, v69
	v_mfma_f32_16x16x32_bf16 v[84:87], v[232:235], v[100:103], v[84:87]
	v_cvt_pk_bf16_f32 v35, v70, v71
	ds_read_b128 v[232:235], v126 offset:59392
	ds_read_b128 v[236:239], v126 offset:60416
	s_waitcnt lgkmcnt(6)
	v_mfma_f32_16x16x32_bf16 v[80:83], v[240:243], v[104:107], v[80:83]
	v_cvt_pk_bf16_f32 v36, v56, v57
	v_mfma_f32_16x16x32_bf16 v[76:79], v[244:247], v[104:107], v[76:79]
	v_cvt_pk_bf16_f32 v37, v58, v59
	v_mfma_f32_16x16x32_bf16 v[72:75], v[244:247], v[108:111], v[72:75]
	v_cvt_pk_bf16_f32 v38, v60, v61
	v_mfma_f32_16x16x32_bf16 v[84:87], v[240:243], v[108:111], v[84:87]
	v_cvt_pk_bf16_f32 v39, v62, v63
	ds_read_b128 v[240:243], v126 offset:61440
	ds_read_b128 v[244:247], v126 offset:62464
	s_waitcnt lgkmcnt(6)
	v_mfma_f32_16x16x32_bf16 v[80:83], v[248:251], v[184:187], v[80:83]
	v_pk_max_i16 v32, v32, 0
	v_mfma_f32_16x16x32_bf16 v[76:79], v[252:255], v[184:187], v[76:79]
	v_pk_max_i16 v33, v33, 0
	v_mfma_f32_16x16x32_bf16 v[72:75], v[252:255], v[188:191], v[72:75]
	v_pk_max_i16 v34, v34, 0
	v_mfma_f32_16x16x32_bf16 v[84:87], v[248:251], v[188:191], v[84:87]
	v_pk_max_i16 v35, v35, 0
	ds_read_b128 v[248:251], v126 offset:63488
	ds_read_b128 v[252:255], v126 offset:64512
	s_setprio 0
	s_waitcnt lgkmcnt(6)
	v_mfma_f32_16x16x32_bf16 v[80:83], v[224:227], v[192:195], v[80:83]
	v_pk_max_i16 v36, v36, 0
	v_mfma_f32_16x16x32_bf16 v[76:79], v[228:231], v[192:195], v[76:79]
	v_pk_max_i16 v37, v37, 0
	v_mfma_f32_16x16x32_bf16 v[72:75], v[228:231], v[196:199], v[72:75]
	v_pk_max_i16 v38, v38, 0
	v_mfma_f32_16x16x32_bf16 v[84:87], v[224:227], v[196:199], v[84:87]
	v_pk_max_i16 v39, v39, 0
	s_waitcnt lgkmcnt(4)
	v_mfma_f32_16x16x32_bf16 v[80:83], v[232:235], v[200:203], v[80:83]
	v_mfma_f32_16x16x32_bf16 v[76:79], v[236:239], v[200:203], v[76:79]
	v_mfma_f32_16x16x32_bf16 v[72:75], v[236:239], v[204:207], v[72:75]
	v_mfma_f32_16x16x32_bf16 v[84:87], v[232:235], v[204:207], v[84:87]
.Lnerf_hid_a7:
	s_waitcnt vmcnt(0) lgkmcnt(0)
	s_barrier
	ds_read_b128 v[224:227], v121 offset:8192
	ds_read_b128 v[228:231], v121 offset:9216
	v_mfma_f32_16x16x32_bf16 v[80:83], v[240:243], v[208:211], v[80:83]
	ds_read_b128 v[232:235], v121 offset:10240
	v_mfma_f32_16x16x32_bf16 v[76:79], v[244:247], v[208:211], v[76:79]
	ds_read_b128 v[236:239], v121 offset:11264
	v_mfma_f32_16x16x32_bf16 v[72:75], v[244:247], v[212:215], v[72:75]
	v_mfma_f32_16x16x32_bf16 v[84:87], v[240:243], v[212:215], v[84:87]
	ds_read_b128 v[240:243], v121 offset:12288
	ds_read_b128 v[244:247], v121 offset:13312
	v_mfma_f32_16x16x32_bf16 v[80:83], v[248:251], v[216:219], v[80:83]
	v_mfma_f32_16x16x32_bf16 v[76:79], v[252:255], v[216:219], v[76:79]
	v_mfma_f32_16x16x32_bf16 v[72:75], v[252:255], v[220:223], v[72:75]
	v_mfma_f32_16x16x32_bf16 v[84:87], v[248:251], v[220:223], v[84:87]
	ds_read_b128 v[248:251], v121 offset:14336
	ds_read_b128 v[252:255], v121 offset:15360
	s_setprio 3
	s_waitcnt lgkmcnt(6)
	v_mfma_f32_16x16x32_bf16 v[64:67], v[224:227], v[88:91], v[152:155]
	v_mfma_f32_16x16x32_bf16 v[68:71], v[228:231], v[88:91], v[156:159]
	v_mfma_f32_16x16x32_bf16 v[60:63], v[228:231], v[92:95], v[156:159]
	v_mfma_f32_16x16x32_bf16 v[56:59], v[224:227], v[92:95], v[152:155]
	ds_read_b128 v[224:227], v121 offset:16384
	ds_read_b128 v[228:231], v121 offset:17408
	s_waitcnt lgkmcnt(6)
	ds_read_b128 v[160:163], v183 offset:1920
	ds_read_b128 v[164:167], v183 offset:1984
	v_mfma_f32_16x16x32_bf16 v[64:67], v[232:235], v[96:99], v[64:67]
	v_cvt_pk_bf16_f32 v40, v80, v81
	v_mfma_f32_16x16x32_bf16 v[68:71], v[236:239], v[96:99], v[68:71]
	s_mov_b32 m0, s28
	s_add_i32 s51, s50, 0x38000
	v_cvt_pk_bf16_f32 v41, v82, v83
	v_mfma_f32_16x16x32_bf16 v[60:63], v[236:239], v[100:103], v[60:63]
	buffer_load_dwordx4 v125, s[36:39], s51 offen lds
	v_cvt_pk_bf16_f32 v42, v76, v77
	v_mfma_f32_16x16x32_bf16 v[56:59], v[232:235], v[100:103], v[56:59]
	v_cvt_pk_bf16_f32 v43, v78, v79
	ds_read_b128 v[232:235], v121 offset:18432
	ds_read_b128 v[236:239], v121 offset:19456
	s_waitcnt lgkmcnt(8)
	v_mfma_f32_16x16x32_bf16 v[64:67], v[240:243], v[104:107], v[64:67]
	v_cvt_pk_bf16_f32 v44, v84, v85
	v_mfma_f32_16x16x32_bf16 v[68:71], v[244:247], v[104:107], v[68:71]
	s_mov_b32 m0, s29
	s_add_i32 s51, s50, 0x3a000
	v_cvt_pk_bf16_f32 v45, v86, v87
	v_mfma_f32_16x16x32_bf16 v[60:63], v[244:247], v[108:111], v[60:63]
	buffer_load_dwordx4 v125, s[36:39], s51 offen lds
	v_cvt_pk_bf16_f32 v46, v72, v73
	v_mfma_f32_16x16x32_bf16 v[56:59], v[240:243], v[108:111], v[56:59]
	v_cvt_pk_bf16_f32 v47, v74, v75
	ds_read_b128 v[240:243], v121 offset:20480
	ds_read_b128 v[244:247], v121 offset:21504
	s_waitcnt lgkmcnt(8)
	v_mfma_f32_16x16x32_bf16 v[64:67], v[248:251], v[184:187], v[64:67]
	v_pk_max_i16 v40, v40, 0
	v_mfma_f32_16x16x32_bf16 v[68:71], v[252:255], v[184:187], v[68:71]
	s_mov_b32 m0, s33
	s_add_i32 s51, s50, 0x3c000
	v_pk_max_i16 v41, v41, 0
	v_mfma_f32_16x16x32_bf16 v[60:63], v[252:255], v[188:191], v[60:63]
	buffer_load_dwordx4 v125, s[36:39], s51 offen lds
	v_pk_max_i16 v42, v42, 0
	v_mfma_f32_16x16x32_bf16 v[56:59], v[248:251], v[188:191], v[56:59]
	v_pk_max_i16 v43, v43, 0
	ds_read_b128 v[248:251], v121 offset:22528
	ds_read_b128 v[252:255], v121 offset:23552
	s_setprio 2
	s_waitcnt lgkmcnt(8)
	v_mfma_f32_16x16x32_bf16 v[64:67], v[224:227], v[192:195], v[64:67]
	v_pk_max_i16 v44, v44, 0
	v_mfma_f32_16x16x32_bf16 v[68:71], v[228:231], v[192:195], v[68:71]
	s_mov_b32 m0, s34
	s_add_i32 s51, s50, 0x3e000
	v_pk_max_i16 v45, v45, 0
	v_mfma_f32_16x16x32_bf16 v[60:63], v[228:231], v[196:199], v[60:63]
	buffer_load_dwordx4 v125, s[36:39], s51 offen lds
	v_pk_max_i16 v46, v46, 0
	v_mfma_f32_16x16x32_bf16 v[56:59], v[224:227], v[196:199], v[56:59]
	v_pk_max_i16 v47, v47, 0
	ds_read_b128 v[224:227], v121 offset:24576
	ds_read_b128 v[228:231], v121 offset:25600
	s_waitcnt lgkmcnt(6)
	v_mfma_f32_16x16x32_bf16 v[64:67], v[232:235], v[200:203], v[64:67]
	v_mfma_f32_16x16x32_bf16 v[68:71], v[236:239], v[200:203], v[68:71]
	v_mfma_f32_16x16x32_bf16 v[60:63], v[236:239], v[204:207], v[60:63]
	v_mfma_f32_16x16x32_bf16 v[56:59], v[232:235], v[204:207], v[56:59]
	ds_read_b128 v[232:235], v121 offset:26624
	ds_read_b128 v[236:239], v121 offset:27648
	s_waitcnt lgkmcnt(6)
	ds_read_b128 v[152:155], v183 offset:2048
	ds_read_b128 v[156:159], v183 offset:2112
	v_mfma_f32_16x16x32_bf16 v[64:67], v[240:243], v[208:211], v[64:67]
	v_mfma_f32_16x16x32_bf16 v[68:71], v[244:247], v[208:211], v[68:71]
	v_mfma_f32_16x16x32_bf16 v[60:63], v[244:247], v[212:215], v[60:63]
	v_mfma_f32_16x16x32_bf16 v[56:59], v[240:243], v[212:215], v[56:59]
	ds_read_b128 v[240:243], v121 offset:28672
	ds_read_b128 v[244:247], v121 offset:29696
	s_waitcnt lgkmcnt(8)
	v_mfma_f32_16x16x32_bf16 v[64:67], v[248:251], v[216:219], v[64:67]
	v_mfma_f32_16x16x32_bf16 v[68:71], v[252:255], v[216:219], v[68:71]
	v_mfma_f32_16x16x32_bf16 v[60:63], v[252:255], v[220:223], v[60:63]
	v_mfma_f32_16x16x32_bf16 v[56:59], v[248:251], v[220:223], v[56:59]
	ds_read_b128 v[248:251], v121 offset:30720
	ds_read_b128 v[252:255], v121 offset:31744
	s_setprio 1
	s_waitcnt lgkmcnt(8)
	v_mfma_f32_16x16x32_bf16 v[80:83], v[224:227], v[88:91], v[160:163]
	v_mfma_f32_16x16x32_bf16 v[76:79], v[228:231], v[88:91], v[164:167]
	v_mfma_f32_16x16x32_bf16 v[72:75], v[228:231], v[92:95], v[164:167]
	v_mfma_f32_16x16x32_bf16 v[84:87], v[224:227], v[92:95], v[160:163]
	ds_read_b128 v[224:227], v121 offset:32768
	ds_read_b128 v[228:231], v121 offset:33792
	s_waitcnt lgkmcnt(8)
	v_mfma_f32_16x16x32_bf16 v[80:83], v[232:235], v[96:99], v[80:83]
	v_cvt_pk_bf16_f32 v48, v64, v65
	v_mfma_f32_16x16x32_bf16 v[76:79], v[236:239], v[96:99], v[76:79]
	v_cvt_pk_bf16_f32 v49, v66, v67
	v_mfma_f32_16x16x32_bf16 v[72:75], v[236:239], v[100:103], v[72:75]
	v_cvt_pk_bf16_f32 v50, v68, v69
	v_mfma_f32_16x16x32_bf16 v[84:87], v[232:235], v[100:103], v[84:87]
	v_cvt_pk_bf16_f32 v51, v70, v71
	ds_read_b128 v[232:235], v121 offset:34816
	ds_read_b128 v[236:239], v121 offset:35840
	s_waitcnt lgkmcnt(6)
	v_mfma_f32_16x16x32_bf16 v[80:83], v[240:243], v[104:107], v[80:83]
	v_cvt_pk_bf16_f32 v52, v56, v57
	v_mfma_f32_16x16x32_bf16 v[76:79], v[244:247], v[104:107], v[76:79]
	v_cvt_pk_bf16_f32 v53, v58, v59
	v_mfma_f32_16x16x32_bf16 v[72:75], v[244:247], v[108:111], v[72:75]
	v_cvt_pk_bf16_f32 v54, v60, v61
	v_mfma_f32_16x16x32_bf16 v[84:87], v[240:243], v[108:111], v[84:87]
	v_cvt_pk_bf16_f32 v55, v62, v63
	ds_read_b128 v[240:243], v121 offset:36864
	ds_read_b128 v[244:247], v121 offset:37888
	s_waitcnt lgkmcnt(6)
	v_mfma_f32_16x16x32_bf16 v[80:83], v[248:251], v[184:187], v[80:83]
	v_pk_max_i16 v48, v48, 0
	v_mfma_f32_16x16x32_bf16 v[76:79], v[252:255], v[184:187], v[76:79]
	v_pk_max_i16 v49, v49, 0
	v_mfma_f32_16x16x32_bf16 v[72:75], v[252:255], v[188:191], v[72:75]
	v_pk_max_i16 v50, v50, 0
	v_mfma_f32_16x16x32_bf16 v[84:87], v[248:251], v[188:191], v[84:87]
	v_pk_max_i16 v51, v51, 0
	ds_read_b128 v[248:251], v121 offset:38912
	ds_read_b128 v[252:255], v121 offset:39936
	s_setprio 0
	s_waitcnt lgkmcnt(6)
	v_mfma_f32_16x16x32_bf16 v[80:83], v[224:227], v[192:195], v[80:83]
	v_pk_max_i16 v52, v52, 0
	v_mfma_f32_16x16x32_bf16 v[76:79], v[228:231], v[192:195], v[76:79]
	v_pk_max_i16 v53, v53, 0
	v_mfma_f32_16x16x32_bf16 v[72:75], v[228:231], v[196:199], v[72:75]
	v_pk_max_i16 v54, v54, 0
	v_mfma_f32_16x16x32_bf16 v[84:87], v[224:227], v[196:199], v[84:87]
	v_pk_max_i16 v55, v55, 0
	s_waitcnt lgkmcnt(4)
	v_mfma_f32_16x16x32_bf16 v[80:83], v[232:235], v[200:203], v[80:83]
	v_mfma_f32_16x16x32_bf16 v[76:79], v[236:239], v[200:203], v[76:79]
	v_mfma_f32_16x16x32_bf16 v[72:75], v[236:239], v[204:207], v[72:75]
	v_mfma_f32_16x16x32_bf16 v[84:87], v[232:235], v[204:207], v[84:87]
	s_add_i32 s50, s50, 0x40000
	v_add_u32_e32 v183, 0x800, v183
	s_add_i32 s52, s52, 1
	s_branch .Lnerf_hid_a0
.Lnerf_hid_b_first:
	s_waitcnt vmcnt(0) lgkmcnt(0)
	s_barrier
	ds_read_b128 v[224:227], v121 offset:40960
	ds_read_b128 v[228:231], v121 offset:41984
	ds_read_b128 v[152:155], v183 offset:0
	ds_read_b128 v[156:159], v183 offset:64
	ds_read_b128 v[232:235], v121 offset:43008
	ds_read_b128 v[236:239], v121 offset:44032
	ds_read_b128 v[240:243], v121 offset:45056
	ds_read_b128 v[244:247], v121 offset:46080
	ds_read_b128 v[248:251], v121 offset:47104
	ds_read_b128 v[252:255], v121 offset:48128
	s_setprio 3
	s_waitcnt lgkmcnt(6)
	v_mfma_f32_16x16x32_bf16 v[64:67], v[224:227], v[0:3], v[152:155]
	v_cvt_pk_bf16_f32 v112, v80, v81
	v_mfma_f32_16x16x32_bf16 v[68:71], v[228:231], v[0:3], v[156:159]
	v_cvt_pk_bf16_f32 v113, v82, v83
	v_mfma_f32_16x16x32_bf16 v[60:63], v[228:231], v[4:7], v[156:159]
	v_cvt_pk_bf16_f32 v114, v76, v77
	v_mfma_f32_16x16x32_bf16 v[56:59], v[224:227], v[4:7], v[152:155]
	v_cvt_pk_bf16_f32 v115, v78, v79
	ds_read_b128 v[224:227], v121 offset:49152
	ds_read_b128 v[228:231], v121 offset:50176
	s_waitcnt lgkmcnt(6)
	ds_read_b128 v[160:163], v183 offset:128
	ds_read_b128 v[164:167], v183 offset:192
	v_mfma_f32_16x16x32_bf16 v[64:67], v[232:235], v[12:15], v[64:67]
	v_cvt_pk_bf16_f32 v116, v84, v85
	v_mfma_f32_16x16x32_bf16 v[68:71], v[236:239], v[12:15], v[68:71]
	v_cvt_pk_bf16_f32 v117, v86, v87
	v_mfma_f32_16x16x32_bf16 v[60:63], v[236:239], v[8:11], v[60:63]
	v_cvt_pk_bf16_f32 v118, v72, v73
	v_mfma_f32_16x16x32_bf16 v[56:59], v[232:235], v[8:11], v[56:59]
	v_cvt_pk_bf16_f32 v119, v74, v75
	ds_read_b128 v[232:235], v121 offset:51200
	ds_read_b128 v[236:239], v121 offset:52224
	s_waitcnt lgkmcnt(8)
	v_mfma_f32_16x16x32_bf16 v[64:67], v[240:243], v[16:19], v[64:67]
	v_pk_max_i16 v112, v112, 0
	v_mfma_f32_16x16x32_bf16 v[68:71], v[244:247], v[16:19], v[68:71]
	v_pk_max_i16 v113, v113, 0
	v_mfma_f32_16x16x32_bf16 v[60:63], v[244:247], v[20:23], v[60:63]
	v_pk_max_i16 v114, v114, 0
	v_mfma_f32_16x16x32_bf16 v[56:59], v[240:243], v[20:23], v[56:59]
	v_pk_max_i16 v115, v115, 0
	ds_read_b128 v[240:243], v121 offset:53248
	ds_read_b128 v[244:247], v121 offset:54272
	s_waitcnt lgkmcnt(8)
	v_mfma_f32_16x16x32_bf16 v[64:67], v[248:251], v[24:27], v[64:67]
	v_pk_max_i16 v116, v116, 0
	v_mfma_f32_16x16x32_bf16 v[68:71], v[252:255], v[24:27], v[68:71]
	v_pk_max_i16 v117, v117, 0
	v_mfma_f32_16x16x32_bf16 v[60:63], v[252:255], v[28:31], v[60:63]
	v_pk_max_i16 v118, v118, 0
	v_mfma_f32_16x16x32_bf16 v[56:59], v[248:251], v[28:31], v[56:59]
	v_pk_max_i16 v119, v119, 0
	ds_read_b128 v[248:251], v121 offset:55296
	ds_read_b128 v[252:255], v121 offset:56320
	s_setprio 2
	s_waitcnt lgkmcnt(8)
	v_mfma_f32_16x16x32_bf16 v[64:67], v[224:227], v[32:35], v[64:67]
	v_mfma_f32_16x16x32_bf16 v[68:71], v[228:231], v[32:35], v[68:71]
	v_mfma_f32_16x16x32_bf16 v[60:63], v[228:231], v[36:39], v[60:63]
	v_mfma_f32_16x16x32_bf16 v[56:59], v[224:227], v[36:39], v[56:59]
	ds_read_b128 v[224:227], v121 offset:57344
	ds_read_b128 v[228:231], v121 offset:58368
	s_waitcnt lgkmcnt(6)
	v_mfma_f32_16x16x32_bf16 v[64:67], v[232:235], v[40:43], v[64:67]
	v_mfma_f32_16x16x32_bf16 v[68:71], v[236:239], v[40:43], v[68:71]
	s_mov_b32 m0, s35
	s_add_i32 s51, s50, 0x0
	v_mfma_f32_16x16x32_bf16 v[60:63], v[236:239], v[44:47], v[60:63]
	buffer_load_dwordx4 v125, s[36:39], s51 offen lds
	v_mfma_f32_16x16x32_bf16 v[56:59], v[232:235], v[44:47], v[56:59]
	ds_read_b128 v[232:235], v121 offset:59392
	ds_read_b128 v[236:239], v121 offset:60416
	s_waitcnt lgkmcnt(6)
	ds_read_b128 v[152:155], v183 offset:256
	ds_read_b128 v[156:159], v183 offset:320
	v_mfma_f32_16x16x32_bf16 v[64:67], v[240:243], v[48:51], v[64:67]
	v_mfma_f32_16x16x32_bf16 v[68:71], v[244:247], v[48:51], v[68:71]
	s_mov_b32 m0, s42
	s_add_i32 s51, s50, 0x2000
	v_mfma_f32_16x16x32_bf16 v[60:63], v[244:247], v[52:55], v[60:63]
	buffer_load_dwordx4 v125, s[36:39], s51 offen lds
	v_mfma_f32_16x16x32_bf16 v[56:59], v[240:243], v[52:55], v[56:59]
	ds_read_b128 v[240:243], v121 offset:61440
	ds_read_b128 v[244:247], v121 offset:62464
	s_waitcnt lgkmcnt(8)
	v_mfma_f32_16x16x32_bf16 v[64:67], v[248:251], v[112:115], v[64:67]
	v_mfma_f32_16x16x32_bf16 v[68:71], v[252:255], v[112:115], v[68:71]
	s_mov_b32 m0, s41
	s_add_i32 s51, s50, 0x4000
	v_mfma_f32_16x16x32_bf16 v[60:63], v[252:255], v[116:119], v[60:63]
	buffer_load_dwordx4 v125, s[36:39], s51 offen lds
	v_mfma_f32_16x16x32_bf16 v[56:59], v[248:251], v[116:119], v[56:59]
	ds_read_b128 v[248:251], v121 offset:63488
	ds_read_b128 v[252:255], v121 offset:64512
	s_setprio 1
	s_waitcnt lgkmcnt(8)
	v_mfma_f32_16x16x32_bf16 v[80:83], v[224:227], v[0:3], v[160:163]
	v_mfma_f32_16x16x32_bf16 v[76:79], v[228:231], v[0:3], v[164:167]
	s_mov_b32 m0, s40
	s_add_i32 s51, s50, 0x6000
	v_mfma_f32_16x16x32_bf16 v[72:75], v[228:231], v[4:7], v[164:167]
	buffer_load_dwordx4 v125, s[36:39], s51 offen lds
	v_mfma_f32_16x16x32_bf16 v[84:87], v[224:227], v[4:7], v[160:163]
	ds_read_b128 v[224:227], v126 offset:57344
	ds_read_b128 v[228:231], v126 offset:58368
	s_waitcnt lgkmcnt(8)
	v_mfma_f32_16x16x32_bf16 v[80:83], v[232:235], v[12:15], v[80:83]
	v_cvt_pk_bf16_f32 v88, v64, v65
	v_mfma_f32_16x16x32_bf16 v[76:79], v[236:239], v[12:15], v[76:79]
	v_cvt_pk_bf16_f32 v89, v66, v67
	v_mfma_f32_16x16x32_bf16 v[72:75], v[236:239], v[8:11], v[72:75]
	v_cvt_pk_bf16_f32 v90, v68, v69
	v_mfma_f32_16x16x32_bf16 v[84:87], v[232:235], v[8:11], v[84:87]
	v_cvt_pk_bf16_f32 v91, v70, v71
	ds_read_b128 v[232:235], v126 offset:59392
	ds_read_b128 v[236:239], v126 offset:60416
	s_waitcnt lgkmcnt(6)
	v_mfma_f32_16x16x32_bf16 v[80:83], v[240:243], v[16:19], v[80:83]
	v_cvt_pk_bf16_f32 v92, v56, v57
	v_mfma_f32_16x16x32_bf16 v[76:79], v[244:247], v[16:19], v[76:79]
	v_cvt_pk_bf16_f32 v93, v58, v59
	v_mfma_f32_16x16x32_bf16 v[72:75], v[244:247], v[20:23], v[72:75]
	v_cvt_pk_bf16_f32 v94, v60, v61
	v_mfma_f32_16x16x32_bf16 v[84:87], v[240:243], v[20:23], v[84:87]
	v_cvt_pk_bf16_f32 v95, v62, v63
	ds_read_b128 v[240:243], v126 offset:61440
	ds_read_b128 v[244:247], v126 offset:62464
	s_waitcnt lgkmcnt(6)
	v_mfma_f32_16x16x32_bf16 v[80:83], v[248:251], v[24:27], v[80:83]
	v_pk_max_i16 v88, v88, 0
	v_mfma_f32_16x16x32_bf16 v[76:79], v[252:255], v[24:27], v[76:79]
	v_pk_max_i16 v89, v89, 0
	v_mfma_f32_16x16x32_bf16 v[72:75], v[252:255], v[28:31], v[72:75]
	v_pk_max_i16 v90, v90, 0
	v_mfma_f32_16x16x32_bf16 v[84:87], v[248:251], v[28:31], v[84:87]
	v_pk_max_i16 v91, v91, 0
	ds_read_b128 v[248:251], v126 offset:63488
	ds_read_b128 v[252:255], v126 offset:64512
	s_setprio 0
	s_waitcnt lgkmcnt(6)
	v_mfma_f32_16x16x32_bf16 v[80:83], v[224:227], v[32:35], v[80:83]
	v_pk_max_i16 v92, v92, 0
	v_mfma_f32_16x16x32_bf16 v[76:79], v[228:231], v[32:35], v[76:79]
	v_pk_max_i16 v93, v93, 0
	v_mfma_f32_16x16x32_bf16 v[72:75], v[228:231], v[36:39], v[72:75]
	v_pk_max_i16 v94, v94, 0
	v_mfma_f32_16x16x32_bf16 v[84:87], v[224:227], v[36:39], v[84:87]
	v_pk_max_i16 v95, v95, 0
	s_waitcnt lgkmcnt(4)
	v_mfma_f32_16x16x32_bf16 v[80:83], v[232:235], v[40:43], v[80:83]
	v_mfma_f32_16x16x32_bf16 v[76:79], v[236:239], v[40:43], v[76:79]
	v_mfma_f32_16x16x32_bf16 v[72:75], v[236:239], v[44:47], v[72:75]
	v_mfma_f32_16x16x32_bf16 v[84:87], v[232:235], v[44:47], v[84:87]
	s_branch .Lnerf_hid_b1
.Lnerf_hid_b0:
	s_waitcnt vmcnt(0) lgkmcnt(0)
	s_barrier
	ds_read_b128 v[224:227], v121 offset:40960
	ds_read_b128 v[228:231], v121 offset:41984
	v_mfma_f32_16x16x32_bf16 v[80:83], v[240:243], v[208:211], v[80:83]
	ds_read_b128 v[232:235], v121 offset:43008
	v_mfma_f32_16x16x32_bf16 v[76:79], v[244:247], v[208:211], v[76:79]
	ds_read_b128 v[236:239], v121 offset:44032
	v_mfma_f32_16x16x32_bf16 v[72:75], v[244:247], v[212:215], v[72:75]
	v_mfma_f32_16x16x32_bf16 v[84:87], v[240:243], v[212:215], v[84:87]
	ds_read_b128 v[240:243], v121 offset:45056
	ds_read_b128 v[244:247], v121 offset:46080
	v_mfma_f32_16x16x32_bf16 v[80:83], v[248:251], v[216:219], v[80:83]
	v_mfma_f32_16x16x32_bf16 v[76:79], v[252:255], v[216:219], v[76:79]
	v_mfma_f32_16x16x32_bf16 v[72:75], v[252:255], v[220:223], v[72:75]
	v_mfma_f32_16x16x32_bf16 v[84:87], v[248:251], v[220:223], v[84:87]
	ds_read_b128 v[248:251], v121 offset:47104
	ds_read_b128 v[252:255], v121 offset:48128
	s_setprio 3
	s_waitcnt lgkmcnt(6)
	v_mfma_f32_16x16x32_bf16 v[64:67], v[224:227], v[0:3], v[152:155]
	v_mfma_f32_16x16x32_bf16 v[68:71], v[228:231], v[0:3], v[156:159]
	v_mfma_f32_16x16x32_bf16 v[60:63], v[228:231], v[4:7], v[156:159]
	v_mfma_f32_16x16x32_bf16 v[56:59], v[224:227], v[4:7], v[152:155]
	ds_read_b128 v[224:227], v121 offset:49152
	ds_read_b128 v[228:231], v121 offset:50176
	s_waitcnt lgkmcnt(6)
	ds_read_b128 v[160:163], v183 offset:128
	ds_read_b128 v[164:167], v183 offset:192
	v_mfma_f32_16x16x32_bf16 v[64:67], v[232:235], v[12:15], v[64:67]
	v_cvt_pk_bf16_f32 v112, v80, v81
	v_mfma_f32_16x16x32_bf16 v[68:71], v[236:239], v[12:15], v[68:71]
	v_cvt_pk_bf16_f32 v113, v82, v83
	v_mfma_f32_16x16x32_bf16 v[60:63], v[236:239], v[8:11], v[60:63]
	v_cvt_pk_bf16_f32 v114, v76, v77
	v_mfma_f32_16x16x32_bf16 v[56:59], v[232:235], v[8:11], v[56:59]
	v_cvt_pk_bf16_f32 v115, v78, v79
	ds_read_b128 v[232:235], v121 offset:51200
	ds_read_b128 v[236:239], v121 offset:52224
	s_waitcnt lgkmcnt(8)
	v_mfma_f32_16x16x32_bf16 v[64:67], v[240:243], v[16:19], v[64:67]
	v_cvt_pk_bf16_f32 v116, v84, v85
	v_mfma_f32_16x16x32_bf16 v[68:71], v[244:247], v[16:19], v[68:71]
	v_cvt_pk_bf16_f32 v117, v86, v87
	v_mfma_f32_16x16x32_bf16 v[60:63], v[244:247], v[20:23], v[60:63]
	v_cvt_pk_bf16_f32 v118, v72, v73
	v_mfma_f32_16x16x32_bf16 v[56:59], v[240:243], v[20:23], v[56:59]
	v_cvt_pk_bf16_f32 v119, v74, v75
	ds_read_b128 v[240:243], v121 offset:53248
	ds_read_b128 v[244:247], v121 offset:54272
	s_waitcnt lgkmcnt(8)
	v_mfma_f32_16x16x32_bf16 v[64:67], v[248:251], v[24:27], v[64:67]
	v_pk_max_i16 v112, v112, 0
	v_mfma_f32_16x16x32_bf16 v[68:71], v[252:255], v[24:27], v[68:71]
	v_pk_max_i16 v113, v113, 0
	v_mfma_f32_16x16x32_bf16 v[60:63], v[252:255], v[28:31], v[60:63]
	v_pk_max_i16 v114, v114, 0
	v_mfma_f32_16x16x32_bf16 v[56:59], v[248:251], v[28:31], v[56:59]
	v_pk_max_i16 v115, v115, 0
	ds_read_b128 v[248:251], v121 offset:55296
	ds_read_b128 v[252:255], v121 offset:56320
	s_setprio 2
	s_waitcnt lgkmcnt(8)
	v_mfma_f32_16x16x32_bf16 v[64:67], v[224:227], v[32:35], v[64:67]
	v_pk_max_i16 v116, v116, 0
	v_mfma_f32_16x16x32_bf16 v[68:71], v[228:231], v[32:35], v[68:71]
	v_pk_max_i16 v117, v117, 0
	v_mfma_f32_16x16x32_bf16 v[60:63], v[228:231], v[36:39], v[60:63]
	v_pk_max_i16 v118, v118, 0
	v_mfma_f32_16x16x32_bf16 v[56:59], v[224:227], v[36:39], v[56:59]
	v_pk_max_i16 v119, v119, 0
	ds_read_b128 v[224:227], v121 offset:57344
	ds_read_b128 v[228:231], v121 offset:58368
	s_waitcnt lgkmcnt(6)
	v_mfma_f32_16x16x32_bf16 v[64:67], v[232:235], v[40:43], v[64:67]
	v_mfma_f32_16x16x32_bf16 v[68:71], v[236:239], v[40:43], v[68:71]
	s_mov_b32 m0, s35
	s_add_i32 s51, s50, 0x0
	v_mfma_f32_16x16x32_bf16 v[60:63], v[236:239], v[44:47], v[60:63]
	buffer_load_dwordx4 v125, s[36:39], s51 offen lds
	v_mfma_f32_16x16x32_bf16 v[56:59], v[232:235], v[44:47], v[56:59]
	ds_read_b128 v[232:235], v121 offset:59392
	ds_read_b128 v[236:239], v121 offset:60416
	s_waitcnt lgkmcnt(6)
	ds_read_b128 v[152:155], v183 offset:256
	ds_read_b128 v[156:159], v183 offset:320
	v_mfma_f32_16x16x32_bf16 v[64:67], v[240:243], v[48:51], v[64:67]
	v_mfma_f32_16x16x32_bf16 v[68:71], v[244:247], v[48:51], v[68:71]
	s_mov_b32 m0, s42
	s_add_i32 s51, s50, 0x2000
	v_mfma_f32_16x16x32_bf16 v[60:63], v[244:247], v[52:55], v[60:63]
	buffer_load_dwordx4 v125, s[36:39], s51 offen lds
	v_mfma_f32_16x16x32_bf16 v[56:59], v[240:243], v[52:55], v[56:59]
	ds_read_b128 v[240:243], v121 offset:61440
	ds_read_b128 v[244:247], v121 offset:62464
	s_waitcnt lgkmcnt(8)
	v_mfma_f32_16x16x32_bf16 v[64:67], v[248:251], v[112:115], v[64:67]
	v_mfma_f32_16x16x32_bf16 v[68:71], v[252:255], v[112:115], v[68:71]
	s_mov_b32 m0, s41
	s_add_i32 s51, s50, 0x4000
	v_mfma_f32_16x16x32_bf16 v[60:63], v[252:255], v[116:119], v[60:63]
	buffer_load_dwordx4 v125, s[36:39], s51 offen lds
	v_mfma_f32_16x16x32_bf16 v[56:59], v[248:251], v[116:119], v[56:59]
	ds_read_b128 v[248:251], v121 offset:63488
	ds_read_b128 v[252:255], v121 offset:64512
	s_setprio 1
	s_waitcnt lgkmcnt(8)
	v_mfma_f32_16x16x32_bf16 v[80:83], v[224:227], v[0:3], v[160:163]
	v_mfma_f32_16x16x32_bf16 v[76:79], v[228:231], v[0:3], v[164:167]
	s_mov_b32 m0, s40
	s_add_i32 s51, s50, 0x6000
	v_mfma_f32_16x16x32_bf16 v[72:75], v[228:231], v[4:7], v[164:167]
	buffer_load_dwordx4 v125, s[36:39], s51 offen lds
	v_mfma_f32_16x16x32_bf16 v[84:87], v[224:227], v[4:7], v[160:163]
	ds_read_b128 v[224:227], v126 offset:57344
	ds_read_b128 v[228:231], v126 offset:58368
	s_waitcnt lgkmcnt(8)
	v_mfma_f32_16x16x32_bf16 v[80:83], v[232:235], v[12:15], v[80:83]
	v_cvt_pk_bf16_f32 v88, v64, v65
	v_mfma_f32_16x16x32_bf16 v[76:79], v[236:239], v[12:15], v[76:79]
	v_cvt_pk_bf16_f32 v89, v66, v67
	v_mfma_f32_16x16x32_bf16 v[72:75], v[236:239], v[8:11], v[72:75]
	v_cvt_pk_bf16_f32 v90, v68, v69
	v_mfma_f32_16x16x32_bf16 v[84:87], v[232:235], v[8:11], v[84:87]
	v_cvt_pk_bf16_f32 v91, v70, v71
	ds_read_b128 v[232:235], v126 offset:59392
	ds_read_b128 v[236:239], v126 offset:60416
	s_waitcnt lgkmcnt(6)
	v_mfma_f32_16x16x32_bf16 v[80:83], v[240:243], v[16:19], v[80:83]
	v_cvt_pk_bf16_f32 v92, v56, v57
	v_mfma_f32_16x16x32_bf16 v[76:79], v[244:247], v[16:19], v[76:79]
	v_cvt_pk_bf16_f32 v93, v58, v59
	v_mfma_f32_16x16x32_bf16 v[72:75], v[244:247], v[20:23], v[72:75]
	v_cvt_pk_bf16_f32 v94, v60, v61
	v_mfma_f32_16x16x32_bf16 v[84:87], v[240:243], v[20:23], v[84:87]
	v_cvt_pk_bf16_f32 v95, v62, v63
	ds_read_b128 v[240:243], v126 offset:61440
	ds_read_b128 v[244:247], v126 offset:62464
	s_waitcnt lgkmcnt(6)
	v_mfma_f32_16x16x32_bf16 v[80:83], v[248:251], v[24:27], v[80:83]
	v_pk_max_i16 v88, v88, 0
	v_mfma_f32_16x16x32_bf16 v[76:79], v[252:255], v[24:27], v[76:79]
	v_pk_max_i16 v89, v89, 0
	v_mfma_f32_16x16x32_bf16 v[72:75], v[252:255], v[28:31], v[72:75]
	v_pk_max_i16 v90, v90, 0
	v_mfma_f32_16x16x32_bf16 v[84:87], v[248:251], v[28:31], v[84:87]
	v_pk_max_i16 v91, v91, 0
	ds_read_b128 v[248:251], v126 offset:63488
	ds_read_b128 v[252:255], v126 offset:64512
	s_setprio 0
	s_waitcnt lgkmcnt(6)
	v_mfma_f32_16x16x32_bf16 v[80:83], v[224:227], v[32:35], v[80:83]
	v_pk_max_i16 v92, v92, 0
	v_mfma_f32_16x16x32_bf16 v[76:79], v[228:231], v[32:35], v[76:79]
	v_pk_max_i16 v93, v93, 0
	v_mfma_f32_16x16x32_bf16 v[72:75], v[228:231], v[36:39], v[72:75]
	v_pk_max_i16 v94, v94, 0
	v_mfma_f32_16x16x32_bf16 v[84:87], v[224:227], v[36:39], v[84:87]
	v_pk_max_i16 v95, v95, 0
	s_waitcnt lgkmcnt(4)
	v_mfma_f32_16x16x32_bf16 v[80:83], v[232:235], v[40:43], v[80:83]
	v_mfma_f32_16x16x32_bf16 v[76:79], v[236:239], v[40:43], v[76:79]
	v_mfma_f32_16x16x32_bf16 v[72:75], v[236:239], v[44:47], v[72:75]
	v_mfma_f32_16x16x32_bf16 v[84:87], v[232:235], v[44:47], v[84:87]
.Lnerf_hid_b1:
	s_waitcnt vmcnt(0) lgkmcnt(0)
	s_barrier
	ds_read_b128 v[224:227], v121 offset:8192
	ds_read_b128 v[228:231], v121 offset:9216
	v_mfma_f32_16x16x32_bf16 v[80:83], v[240:243], v[48:51], v[80:83]
	ds_read_b128 v[232:235], v121 offset:10240
	v_mfma_f32_16x16x32_bf16 v[76:79], v[244:247], v[48:51], v[76:79]
	ds_read_b128 v[236:239], v121 offset:11264
	v_mfma_f32_16x16x32_bf16 v[72:75], v[244:247], v[52:55], v[72:75]
	v_mfma_f32_16x16x32_bf16 v[84:87], v[240:243], v[52:55], v[84:87]
	ds_read_b128 v[240:243], v121 offset:12288
	ds_read_b128 v[244:247], v121 offset:13312
	v_mfma_f32_16x16x32_bf16 v[80:83], v[248:251], v[112:115], v[80:83]
	v_mfma_f32_16x16x32_bf16 v[76:79], v[252:255], v[112:115], v[76:79]
	v_mfma_f32_16x16x32_bf16 v[72:75], v[252:255], v[116:119], v[72:75]
	v_mfma_f32_16x16x32_bf16 v[84:87], v[248:251], v[116:119], v[84:87]
	ds_read_b128 v[248:251], v121 offset:14336
	ds_read_b128 v[252:255], v121 offset:15360
	s_setprio 3
	s_waitcnt lgkmcnt(6)
	v_mfma_f32_16x16x32_bf16 v[64:67], v[224:227], v[0:3], v[152:155]
	v_mfma_f32_16x16x32_bf16 v[68:71], v[228:231], v[0:3], v[156:159]
	v_mfma_f32_16x16x32_bf16 v[60:63], v[228:231], v[4:7], v[156:159]
	v_mfma_f32_16x16x32_bf16 v[56:59], v[224:227], v[4:7], v[152:155]
	ds_read_b128 v[224:227], v121 offset:16384
	ds_read_b128 v[228:231], v121 offset:17408
	s_waitcnt lgkmcnt(6)
	ds_read_b128 v[160:163], v183 offset:384
	ds_read_b128 v[164:167], v183 offset:448
	v_mfma_f32_16x16x32_bf16 v[64:67], v[232:235], v[12:15], v[64:67]
	v_cvt_pk_bf16_f32 v96, v80, v81
	v_mfma_f32_16x16x32_bf16 v[68:71], v[236:239], v[12:15], v[68:71]
	v_cvt_pk_bf16_f32 v97, v82, v83
	v_mfma_f32_16x16x32_bf16 v[60:63], v[236:239], v[8:11], v[60:63]
	v_cvt_pk_bf16_f32 v98, v76, v77
	v_mfma_f32_16x16x32_bf16 v[56:59], v[232:235], v[8:11], v[56:59]
	v_cvt_pk_bf16_f32 v99, v78, v79
	ds_read_b128 v[232:235], v121 offset:18432
	ds_read_b128 v[236:239], v121 offset:19456
	s_waitcnt lgkmcnt(8)
	v_mfma_f32_16x16x32_bf16 v[64:67], v[240:243], v[16:19], v[64:67]
	v_cvt_pk_bf16_f32 v100, v84, v85
	v_mfma_f32_16x16x32_bf16 v[68:71], v[244:247], v[16:19], v[68:71]
	v_cvt_pk_bf16_f32 v101, v86, v87
	v_mfma_f32_16x16x32_bf16 v[60:63], v[244:247], v[20:23], v[60:63]
	v_cvt_pk_bf16_f32 v102, v72, v73
	v_mfma_f32_16x16x32_bf16 v[56:59], v[240:243], v[20:23], v[56:59]
	v_cvt_pk_bf16_f32 v103, v74, v75
	ds_read_b128 v[240:243], v121 offset:20480
	ds_read_b128 v[244:247], v121 offset:21504
	s_waitcnt lgkmcnt(8)
	v_mfma_f32_16x16x32_bf16 v[64:67], v[248:251], v[24:27], v[64:67]
	v_pk_max_i16 v96, v96, 0
	v_mfma_f32_16x16x32_bf16 v[68:71], v[252:255], v[24:27], v[68:71]
	v_pk_max_i16 v97, v97, 0
	v_mfma_f32_16x16x32_bf16 v[60:63], v[252:255], v[28:31], v[60:63]
	v_pk_max_i16 v98, v98, 0
	v_mfma_f32_16x16x32_bf16 v[56:59], v[248:251], v[28:31], v[56:59]
	v_pk_max_i16 v99, v99, 0
	ds_read_b128 v[248:251], v121 offset:22528
	ds_read_b128 v[252:255], v121 offset:23552
	s_setprio 2
	s_waitcnt lgkmcnt(8)
	v_mfma_f32_16x16x32_bf16 v[64:67], v[224:227], v[32:35], v[64:67]
	v_pk_max_i16 v100, v100, 0
	v_mfma_f32_16x16x32_bf16 v[68:71], v[228:231], v[32:35], v[68:71]
	v_pk_max_i16 v101, v101, 0
	v_mfma_f32_16x16x32_bf16 v[60:63], v[228:231], v[36:39], v[60:63]
	v_pk_max_i16 v102, v102, 0
	v_mfma_f32_16x16x32_bf16 v[56:59], v[224:227], v[36:39], v[56:59]
	v_pk_max_i16 v103, v103, 0
	ds_read_b128 v[224:227], v121 offset:24576
	ds_read_b128 v[228:231], v121 offset:25600
	s_waitcnt lgkmcnt(6)
	v_mfma_f32_16x16x32_bf16 v[64:67], v[232:235], v[40:43], v[64:67]
	v_mfma_f32_16x16x32_bf16 v[68:71], v[236:239], v[40:43], v[68:71]
	s_mov_b32 m0, s28
	s_add_i32 s51, s50, 0x8000
	v_mfma_f32_16x16x32_bf16 v[60:63], v[236:239], v[44:47], v[60:63]
	buffer_load_dwordx4 v125, s[36:39], s51 offen lds
	v_mfma_f32_16x16x32_bf16 v[56:59], v[232:235], v[44:47], v[56:59]
	ds_read_b128 v[232:235], v121 offset:26624
	ds_read_b128 v[236:239], v121 offset:27648
	s_waitcnt lgkmcnt(6)
	ds_read_b128 v[152:155], v183 offset:512
	ds_read_b128 v[156:159], v183 offset:576
	v_mfma_f32_16x16x32_bf16 v[64:67], v[240:243], v[48:51], v[64:67]
	v_mfma_f32_16x16x32_bf16 v[68:71], v[244:247], v[48:51], v[68:71]
	s_mov_b32 m0, s29
	s_add_i32 s51, s50, 0xa000
	v_mfma_f32_16x16x32_bf16 v[60:63], v[244:247], v[52:55], v[60:63]
	buffer_load_dwordx4 v125, s[36:39], s51 offen lds
	v_mfma_f32_16x16x32_bf16 v[56:59], v[240:243], v[52:55], v[56:59]
	ds_read_b128 v[240:243], v121 offset:28672
	ds_read_b128 v[244:247], v121 offset:29696
	s_waitcnt lgkmcnt(8)
	v_mfma_f32_16x16x32_bf16 v[64:67], v[248:251], v[112:115], v[64:67]
	v_mfma_f32_16x16x32_bf16 v[68:71], v[252:255], v[112:115], v[68:71]
	s_mov_b32 m0, s33
	s_add_i32 s51, s50, 0xc000
	v_mfma_f32_16x16x32_bf16 v[60:63], v[252:255], v[116:119], v[60:63]
	buffer_load_dwordx4 v125, s[36:39], s51 offen lds
	v_mfma_f32_16x16x32_bf16 v[56:59], v[248:251], v[116:119], v[56:59]
	ds_read_b128 v[248:251], v121 offset:30720
	ds_read_b128 v[252:255], v121 offset:31744
	s_setprio 1
	s_waitcnt lgkmcnt(8)
	v_mfma_f32_16x16x32_bf16 v[80:83], v[224:227], v[0:3], v[160:163]
	v_mfma_f32_16x16x32_bf16 v[76:79], v[228:231], v[0:3], v[164:167]
	s_mov_b32 m0, s34
	s_add_i32 s51, s50, 0xe000
	v_mfma_f32_16x16x32_bf16 v[72:75], v[228:231], v[4:7], v[164:167]
	buffer_load_dwordx4 v125, s[36:39], s51 offen lds
	v_mfma_f32_16x16x32_bf16 v[84:87], v[224:227], v[4:7], v[160:163]
	ds_read_b128 v[224:227], v121 offset:32768
	ds_read_b128 v[228:231], v121 offset:33792
	s_waitcnt lgkmcnt(8)
	v_mfma_f32_16x16x32_bf16 v[80:83], v[232:235], v[12:15], v[80:83]
	v_cvt_pk_bf16_f32 v104, v64, v65
	v_mfma_f32_16x16x32_bf16 v[76:79], v[236:239], v[12:15], v[76:79]
	v_cvt_pk_bf16_f32 v105, v66, v67
	v_mfma_f32_16x16x32_bf16 v[72:75], v[236:239], v[8:11], v[72:75]
	v_cvt_pk_bf16_f32 v106, v68, v69
	v_mfma_f32_16x16x32_bf16 v[84:87], v[232:235], v[8:11], v[84:87]
	v_cvt_pk_bf16_f32 v107, v70, v71
	ds_read_b128 v[232:235], v121 offset:34816
	ds_read_b128 v[236:239], v121 offset:35840
	s_waitcnt lgkmcnt(6)
	v_mfma_f32_16x16x32_bf16 v[80:83], v[240:243], v[16:19], v[80:83]
	v_cvt_pk_bf16_f32 v108, v56, v57
	v_mfma_f32_16x16x32_bf16 v[76:79], v[244:247], v[16:19], v[76:79]
	v_cvt_pk_bf16_f32 v109, v58, v59
	v_mfma_f32_16x16x32_bf16 v[72:75], v[244:247], v[20:23], v[72:75]
	v_cvt_pk_bf16_f32 v110, v60, v61
	v_mfma_f32_16x16x32_bf16 v[84:87], v[240:243], v[20:23], v[84:87]
	v_cvt_pk_bf16_f32 v111, v62, v63
	ds_read_b128 v[240:243], v121 offset:36864
	ds_read_b128 v[244:247], v121 offset:37888
	s_waitcnt lgkmcnt(6)
	v_mfma_f32_16x16x32_bf16 v[80:83], v[248:251], v[24:27], v[80:83]
	v_pk_max_i16 v104, v104, 0
	v_mfma_f32_16x16x32_bf16 v[76:79], v[252:255], v[24:27], v[76:79]
	v_pk_max_i16 v105, v105, 0
	v_mfma_f32_16x16x32_bf16 v[72:75], v[252:255], v[28:31], v[72:75]
	v_pk_max_i16 v106, v106, 0
	v_mfma_f32_16x16x32_bf16 v[84:87], v[248:251], v[28:31], v[84:87]
	v_pk_max_i16 v107, v107, 0
	ds_read_b128 v[248:251], v121 offset:38912
	ds_read_b128 v[252:255], v121 offset:39936
	s_setprio 0
	s_waitcnt lgkmcnt(6)
	v_mfma_f32_16x16x32_bf16 v[80:83], v[224:227], v[32:35], v[80:83]
	v_pk_max_i16 v108, v108, 0
	v_mfma_f32_16x16x32_bf16 v[76:79], v[228:231], v[32:35], v[76:79]
	v_pk_max_i16 v109, v109, 0
	v_mfma_f32_16x16x32_bf16 v[72:75], v[228:231], v[36:39], v[72:75]
	v_pk_max_i16 v110, v110, 0
	v_mfma_f32_16x16x32_bf16 v[84:87], v[224:227], v[36:39], v[84:87]
	v_pk_max_i16 v111, v111, 0
	s_waitcnt lgkmcnt(4)
	v_mfma_f32_16x16x32_bf16 v[80:83], v[232:235], v[40:43], v[80:83]
	v_mfma_f32_16x16x32_bf16 v[76:79], v[236:239], v[40:43], v[76:79]
	v_mfma_f32_16x16x32_bf16 v[72:75], v[236:239], v[44:47], v[72:75]
	v_mfma_f32_16x16x32_bf16 v[84:87], v[232:235], v[44:47], v[84:87]
.Lnerf_hid_b2:
	s_waitcnt vmcnt(0) lgkmcnt(0)
	s_barrier
	ds_read_b128 v[224:227], v121 offset:40960
	ds_read_b128 v[228:231], v121 offset:41984
	v_mfma_f32_16x16x32_bf16 v[80:83], v[240:243], v[48:51], v[80:83]
	ds_read_b128 v[232:235], v121 offset:43008
	v_mfma_f32_16x16x32_bf16 v[76:79], v[244:247], v[48:51], v[76:79]
	ds_read_b128 v[236:239], v121 offset:44032
	v_mfma_f32_16x16x32_bf16 v[72:75], v[244:247], v[52:55], v[72:75]
	v_mfma_f32_16x16x32_bf16 v[84:87], v[240:243], v[52:55], v[84:87]
	ds_read_b128 v[240:243], v121 offset:45056
	ds_read_b128 v[244:247], v121 offset:46080
	v_mfma_f32_16x16x32_bf16 v[80:83], v[248:251], v[112:115], v[80:83]
	v_mfma_f32_16x16x32_bf16 v[76:79], v[252:255], v[112:115], v[76:79]
	v_mfma_f32_16x16x32_bf16 v[72:75], v[252:255], v[116:119], v[72:75]
	v_mfma_f32_16x16x32_bf16 v[84:87], v[248:251], v[116:119], v[84:87]
	ds_read_b128 v[248:251], v121 offset:47104
	ds_read_b128 v[252:255], v121 offset:48128
	s_setprio 3
	s_waitcnt lgkmcnt(6)
	v_mfma_f32_16x16x32_bf16 v[64:67], v[224:227], v[0:3], v[152:155]
	v_mfma_f32_16x16x32_bf16 v[68:71], v[228:231], v[0:3], v[156:159]
	v_mfma_f32_16x16x32_bf16 v[60:63], v[228:231], v[4:7], v[156:159]
	v_mfma_f32_16x16x32_bf16 v[56:59], v[224:227], v[4:7], v[152:155]
	ds_read_b128 v[224:227], v121 offset:49152
	ds_read_b128 v[228:231], v121 offset:50176
	s_waitcnt lgkmcnt(6)
	ds_read_b128 v[160:163], v183 offset:640
	ds_read_b128 v[164:167], v183 offset:704
	v_mfma_f32_16x16x32_bf16 v[64:67], v[232:235], v[12:15], v[64:67]
	v_cvt_pk_bf16_f32 v184, v80, v81
	v_mfma_f32_16x16x32_bf16 v[68:71], v[236:239], v[12:15], v[68:71]
	v_cvt_pk_bf16_f32 v185, v82, v83
	v_mfma_f32_16x16x32_bf16 v[60:63], v[236:239], v[8:11], v[60:63]
	v_cvt_pk_bf16_f32 v186, v76, v77
	v_mfma_f32_16x16x32_bf16 v[56:59], v[232:235], v[8:11], v[56:59]
	v_cvt_pk_bf16_f32 v187, v78, v79
	ds_read_b128 v[232:235], v121 offset:51200
	ds_read_b128 v[236:239], v121 offset:52224
	s_waitcnt lgkmcnt(8)
	v_mfma_f32_16x16x32_bf16 v[64:67], v[240:243], v[16:19], v[64:67]
	v_cvt_pk_bf16_f32 v188, v84, v85
	v_mfma_f32_16x16x32_bf16 v[68:71], v[244:247], v[16:19], v[68:71]
	v_cvt_pk_bf16_f32 v189, v86, v87
	v_mfma_f32_16x16x32_bf16 v[60:63], v[244:247], v[20:23], v[60:63]
	v_cvt_pk_bf16_f32 v190, v72, v73
	v_mfma_f32_16x16x32_bf16 v[56:59], v[240:243], v[20:23], v[56:59]
	v_cvt_pk_bf16_f32 v191, v74, v75
	ds_read_b128 v[240:243], v121 offset:53248
	ds_read_b128 v[244:247], v121 offset:54272
	s_waitcnt lgkmcnt(8)
	v_mfma_f32_16x16x32_bf16 v[64:67], v[248:251], v[24:27], v[64:67]
	v_pk_max_i16 v184, v184, 0
	v_mfma_f32_16x16x32_bf16 v[68:71], v[252:255], v[24:27], v[68:71]
	v_pk_max_i16 v185, v185, 0
	v_mfma_f32_16x16x32_bf16 v[60:63], v[252:255], v[28:31], v[60:63]
	v_pk_max_i16 v186, v186, 0
	v_mfma_f32_16x16x32_bf16 v[56:59], v[248:251], v[28:31], v[56:59]
	v_pk_max_i16 v187, v187, 0
	ds_read_b128 v[248:251], v121 offset:55296
	ds_read_b128 v[252:255], v121 offset:56320
	s_setprio 2
	s_waitcnt lgkmcnt(8)
	v_mfma_f32_16x16x32_bf16 v[64:67], v[224:227], v[32:35], v[64:67]
	v_pk_max_i16 v188, v188, 0
	v_mfma_f32_16x16x32_bf16 v[68:71], v[228:231], v[32:35], v[68:71]
	v_pk_max_i16 v189, v189, 0
	v_mfma_f32_16x16x32_bf16 v[60:63], v[228:231], v[36:39], v[60:63]
	v_pk_max_i16 v190, v190, 0
	v_mfma_f32_16x16x32_bf16 v[56:59], v[224:227], v[36:39], v[56:59]
	v_pk_max_i16 v191, v191, 0
	ds_read_b128 v[224:227], v121 offset:57344
	ds_read_b128 v[228:231], v121 offset:58368
	s_waitcnt lgkmcnt(6)
	v_mfma_f32_16x16x32_bf16 v[64:67], v[232:235], v[40:43], v[64:67]
	v_mfma_f32_16x16x32_bf16 v[68:71], v[236:239], v[40:43], v[68:71]
	s_mov_b32 m0, s35
	s_add_i32 s51, s50, 0x10000
	v_mfma_f32_16x16x32_bf16 v[60:63], v[236:239], v[44:47], v[60:63]
	buffer_load_dwordx4 v125, s[36:39], s51 offen lds
	v_mfma_f32_16x16x32_bf16 v[56:59], v[232:235], v[44:47], v[56:59]
	ds_read_b128 v[232:235], v121 offset:59392
	ds_read_b128 v[236:239], v121 offset:60416
	s_waitcnt lgkmcnt(6)
	ds_read_b128 v[152:155], v183 offset:768
	ds_read_b128 v[156:159], v183 offset:832
	v_mfma_f32_16x16x32_bf16 v[64:67], v[240:243], v[48:51], v[64:67]
	v_mfma_f32_16x16x32_bf16 v[68:71], v[244:247], v[48:51], v[68:71]
	s_mov_b32 m0, s42
	s_add_i32 s51, s50, 0x12000
	v_mfma_f32_16x16x32_bf16 v[60:63], v[244:247], v[52:55], v[60:63]
	buffer_load_dwordx4 v125, s[36:39], s51 offen lds
	v_mfma_f32_16x16x32_bf16 v[56:59], v[240:243], v[52:55], v[56:59]
	ds_read_b128 v[240:243], v121 offset:61440
	ds_read_b128 v[244:247], v121 offset:62464
	s_waitcnt lgkmcnt(8)
	v_mfma_f32_16x16x32_bf16 v[64:67], v[248:251], v[112:115], v[64:67]
	v_mfma_f32_16x16x32_bf16 v[68:71], v[252:255], v[112:115], v[68:71]
	s_mov_b32 m0, s41
	s_add_i32 s51, s50, 0x14000
	v_mfma_f32_16x16x32_bf16 v[60:63], v[252:255], v[116:119], v[60:63]
	buffer_load_dwordx4 v125, s[36:39], s51 offen lds
	v_mfma_f32_16x16x32_bf16 v[56:59], v[248:251], v[116:119], v[56:59]
	ds_read_b128 v[248:251], v121 offset:63488
	ds_read_b128 v[252:255], v121 offset:64512
	s_setprio 1
	s_waitcnt lgkmcnt(8)
	v_mfma_f32_16x16x32_bf16 v[80:83], v[224:227], v[0:3], v[160:163]
	v_mfma_f32_16x16x32_bf16 v[76:79], v[228:231], v[0:3], v[164:167]
	s_mov_b32 m0, s40
	s_add_i32 s51, s50, 0x16000
	v_mfma_f32_16x16x32_bf16 v[72:75], v[228:231], v[4:7], v[164:167]
	buffer_load_dwordx4 v125, s[36:39], s51 offen lds
	v_mfma_f32_16x16x32_bf16 v[84:87], v[224:227], v[4:7], v[160:163]
	ds_read_b128 v[224:227], v126 offset:57344
	ds_read_b128 v[228:231], v126 offset:58368
	s_waitcnt lgkmcnt(8)
	v_mfma_f32_16x16x32_bf16 v[80:83], v[232:235], v[12:15], v[80:83]
	v_cvt_pk_bf16_f32 v192, v64, v65
	v_mfma_f32_16x16x32_bf16 v[76:79], v[236:239], v[12:15], v[76:79]
	v_cvt_pk_bf16_f32 v193, v66, v67
	v_mfma_f32_16x16x32_bf16 v[72:75], v[236:239], v[8:11], v[72:75]
	v_cvt_pk_bf16_f32 v194, v68, v69
	v_mfma_f32_16x16x32_bf16 v[84:87], v[232:235], v[8:11], v[84:87]
	v_cvt_pk_bf16_f32 v195, v70, v71
	ds_read_b128 v[232:235], v126 offset:59392
	ds_read_b128 v[236:239], v126 offset:60416
	s_waitcnt lgkmcnt(6)
	v_mfma_f32_16x16x32_bf16 v[80:83], v[240:243], v[16:19], v[80:83]
	v_cvt_pk_bf16_f32 v196, v56, v57
	v_mfma_f32_16x16x32_bf16 v[76:79], v[244:247], v[16:19], v[76:79]
	v_cvt_pk_bf16_f32 v197, v58, v59
	v_mfma_f32_16x16x32_bf16 v[72:75], v[244:247], v[20:23], v[72:75]
	v_cvt_pk_bf16_f32 v198, v60, v61
	v_mfma_f32_16x16x32_bf16 v[84:87], v[240:243], v[20:23], v[84:87]
	v_cvt_pk_bf16_f32 v199, v62, v63
	ds_read_b128 v[240:243], v126 offset:61440
	ds_read_b128 v[244:247], v126 offset:62464
	s_waitcnt lgkmcnt(6)
	v_mfma_f32_16x16x32_bf16 v[80:83], v[248:251], v[24:27], v[80:83]
	v_pk_max_i16 v192, v192, 0
	v_mfma_f32_16x16x32_bf16 v[76:79], v[252:255], v[24:27], v[76:79]
	v_pk_max_i16 v193, v193, 0
	v_mfma_f32_16x16x32_bf16 v[72:75], v[252:255], v[28:31], v[72:75]
	v_pk_max_i16 v194, v194, 0
	v_mfma_f32_16x16x32_bf16 v[84:87], v[248:251], v[28:31], v[84:87]
	v_pk_max_i16 v195, v195, 0
	ds_read_b128 v[248:251], v126 offset:63488
	ds_read_b128 v[252:255], v126 offset:64512
	s_setprio 0
	s_waitcnt lgkmcnt(6)
	v_mfma_f32_16x16x32_bf16 v[80:83], v[224:227], v[32:35], v[80:83]
	v_pk_max_i16 v196, v196, 0
	v_mfma_f32_16x16x32_bf16 v[76:79], v[228:231], v[32:35], v[76:79]
	v_pk_max_i16 v197, v197, 0
	v_mfma_f32_16x16x32_bf16 v[72:75], v[228:231], v[36:39], v[72:75]
	v_pk_max_i16 v198, v198, 0
	v_mfma_f32_16x16x32_bf16 v[84:87], v[224:227], v[36:39], v[84:87]
	v_pk_max_i16 v199, v199, 0
	s_waitcnt lgkmcnt(4)
	v_mfma_f32_16x16x32_bf16 v[80:83], v[232:235], v[40:43], v[80:83]
	v_mfma_f32_16x16x32_bf16 v[76:79], v[236:239], v[40:43], v[76:79]
	v_mfma_f32_16x16x32_bf16 v[72:75], v[236:239], v[44:47], v[72:75]
	v_mfma_f32_16x16x32_bf16 v[84:87], v[232:235], v[44:47], v[84:87]
.Lnerf_hid_b3:
	s_waitcnt vmcnt(0) lgkmcnt(0)
	s_barrier
	ds_read_b128 v[224:227], v121 offset:8192
	ds_read_b128 v[228:231], v121 offset:9216
	v_mfma_f32_16x16x32_bf16 v[80:83], v[240:243], v[48:51], v[80:83]
	ds_read_b128 v[232:235], v121 offset:10240
	v_mfma_f32_16x16x32_bf16 v[76:79], v[244:247], v[48:51], v[76:79]
	ds_read_b128 v[236:239], v121 offset:11264
	v_mfma_f32_16x16x32_bf16 v[72:75], v[244:247], v[52:55], v[72:75]
	v_mfma_f32_16x16x32_bf16 v[84:87], v[240:243], v[52:55], v[84:87]
	ds_read_b128 v[240:243], v121 offset:12288
	ds_read_b128 v[244:247], v121 offset:13312
	v_mfma_f32_16x16x32_bf16 v[80:83], v[248:251], v[112:115], v[80:83]
	v_mfma_f32_16x16x32_bf16 v[76:79], v[252:255], v[112:115], v[76:79]
	v_mfma_f32_16x16x32_bf16 v[72:75], v[252:255], v[116:119], v[72:75]
	v_mfma_f32_16x16x32_bf16 v[84:87], v[248:251], v[116:119], v[84:87]
	ds_read_b128 v[248:251], v121 offset:14336
	ds_read_b128 v[252:255], v121 offset:15360
	s_setprio 3
	s_waitcnt lgkmcnt(6)
	v_mfma_f32_16x16x32_bf16 v[64:67], v[224:227], v[0:3], v[152:155]
	v_mfma_f32_16x16x32_bf16 v[68:71], v[228:231], v[0:3], v[156:159]
	v_mfma_f32_16x16x32_bf16 v[60:63], v[228:231], v[4:7], v[156:159]
	v_mfma_f32_16x16x32_bf16 v[56:59], v[224:227], v[4:7], v[152:155]
	ds_read_b128 v[224:227], v121 offset:16384
	ds_read_b128 v[228:231], v121 offset:17408
	s_waitcnt lgkmcnt(6)
	ds_read_b128 v[160:163], v183 offset:896
	ds_read_b128 v[164:167], v183 offset:960
	v_mfma_f32_16x16x32_bf16 v[64:67], v[232:235], v[12:15], v[64:67]
	v_cvt_pk_bf16_f32 v200, v80, v81
	v_mfma_f32_16x16x32_bf16 v[68:71], v[236:239], v[12:15], v[68:71]
	v_cvt_pk_bf16_f32 v201, v82, v83
	v_mfma_f32_16x16x32_bf16 v[60:63], v[236:239], v[8:11], v[60:63]
	v_cvt_pk_bf16_f32 v202, v76, v77
	v_mfma_f32_16x16x32_bf16 v[56:59], v[232:235], v[8:11], v[56:59]
	v_cvt_pk_bf16_f32 v203, v78, v79
	ds_read_b128 v[232:235], v121 offset:18432
	ds_read_b128 v[236:239], v121 offset:19456
	s_waitcnt lgkmcnt(8)
	v_mfma_f32_16x16x32_bf16 v[64:67], v[240:243], v[16:19], v[64:67]
	v_cvt_pk_bf16_f32 v204, v84, v85
	v_mfma_f32_16x16x32_bf16 v[68:71], v[244:247], v[16:19], v[68:71]
	v_cvt_pk_bf16_f32 v205, v86, v87
	v_mfma_f32_16x16x32_bf16 v[60:63], v[244:247], v[20:23], v[60:63]
	v_cvt_pk_bf16_f32 v206, v72, v73
	v_mfma_f32_16x16x32_bf16 v[56:59], v[240:243], v[20:23], v[56:59]
	v_cvt_pk_bf16_f32 v207, v74, v75
	ds_read_b128 v[240:243], v121 offset:20480
	ds_read_b128 v[244:247], v121 offset:21504
	s_waitcnt lgkmcnt(8)
	v_mfma_f32_16x16x32_bf16 v[64:67], v[248:251], v[24:27], v[64:67]
	v_pk_max_i16 v200, v200, 0
	v_mfma_f32_16x16x32_bf16 v[68:71], v[252:255], v[24:27], v[68:71]
	v_pk_max_i16 v201, v201, 0
	v_mfma_f32_16x16x32_bf16 v[60:63], v[252:255], v[28:31], v[60:63]
	v_pk_max_i16 v202, v202, 0
	v_mfma_f32_16x16x32_bf16 v[56:59], v[248:251], v[28:31], v[56:59]
	v_pk_max_i16 v203, v203, 0
	ds_read_b128 v[248:251], v121 offset:22528
	ds_read_b128 v[252:255], v121 offset:23552
	s_setprio 2
	s_waitcnt lgkmcnt(8)
	v_mfma_f32_16x16x32_bf16 v[64:67], v[224:227], v[32:35], v[64:67]
	v_pk_max_i16 v204, v204, 0
	v_mfma_f32_16x16x32_bf16 v[68:71], v[228:231], v[32:35], v[68:71]
	v_pk_max_i16 v205, v205, 0
	v_mfma_f32_16x16x32_bf16 v[60:63], v[228:231], v[36:39], v[60:63]
	v_pk_max_i16 v206, v206, 0
	v_mfma_f32_16x16x32_bf16 v[56:59], v[224:227], v[36:39], v[56:59]
	v_pk_max_i16 v207, v207, 0
	ds_read_b128 v[224:227], v121 offset:24576
	ds_read_b128 v[228:231], v121 offset:25600
	s_waitcnt lgkmcnt(6)
	v_mfma_f32_16x16x32_bf16 v[64:67], v[232:235], v[40:43], v[64:67]
	v_mfma_f32_16x16x32_bf16 v[68:71], v[236:239], v[40:43], v[68:71]
	s_mov_b32 m0, s28
	s_add_i32 s51, s50, 0x18000
	v_mfma_f32_16x16x32_bf16 v[60:63], v[236:239], v[44:47], v[60:63]
	buffer_load_dwordx4 v125, s[36:39], s51 offen lds
	v_mfma_f32_16x16x32_bf16 v[56:59], v[232:235], v[44:47], v[56:59]
	ds_read_b128 v[232:235], v121 offset:26624
	ds_read_b128 v[236:239], v121 offset:27648
	s_waitcnt lgkmcnt(6)
	ds_read_b128 v[152:155], v183 offset:1024
	ds_read_b128 v[156:159], v183 offset:1088
	v_mfma_f32_16x16x32_bf16 v[64:67], v[240:243], v[48:51], v[64:67]
	v_mfma_f32_16x16x32_bf16 v[68:71], v[244:247], v[48:51], v[68:71]
	s_mov_b32 m0, s29
	s_add_i32 s51, s50, 0x1a000
	v_mfma_f32_16x16x32_bf16 v[60:63], v[244:247], v[52:55], v[60:63]
	buffer_load_dwordx4 v125, s[36:39], s51 offen lds
	v_mfma_f32_16x16x32_bf16 v[56:59], v[240:243], v[52:55], v[56:59]
	ds_read_b128 v[240:243], v121 offset:28672
	ds_read_b128 v[244:247], v121 offset:29696
	s_waitcnt lgkmcnt(8)
	v_mfma_f32_16x16x32_bf16 v[64:67], v[248:251], v[112:115], v[64:67]
	v_mfma_f32_16x16x32_bf16 v[68:71], v[252:255], v[112:115], v[68:71]
	s_mov_b32 m0, s33
	s_add_i32 s51, s50, 0x1c000
	v_mfma_f32_16x16x32_bf16 v[60:63], v[252:255], v[116:119], v[60:63]
	buffer_load_dwordx4 v125, s[36:39], s51 offen lds
	v_mfma_f32_16x16x32_bf16 v[56:59], v[248:251], v[116:119], v[56:59]
	ds_read_b128 v[248:251], v121 offset:30720
	ds_read_b128 v[252:255], v121 offset:31744
	s_setprio 1
	s_waitcnt lgkmcnt(8)
	v_mfma_f32_16x16x32_bf16 v[80:83], v[224:227], v[0:3], v[160:163]
	v_mfma_f32_16x16x32_bf16 v[76:79], v[228:231], v[0:3], v[164:167]
	s_mov_b32 m0, s34
	s_add_i32 s51, s50, 0x1e000
	v_mfma_f32_16x16x32_bf16 v[72:75], v[228:231], v[4:7], v[164:167]
	buffer_load_dwordx4 v125, s[36:39], s51 offen lds
	v_mfma_f32_16x16x32_bf16 v[84:87], v[224:227], v[4:7], v[160:163]
	ds_read_b128 v[224:227], v121 offset:32768
	ds_read_b128 v[228:231], v121 offset:33792
	s_waitcnt lgkmcnt(8)
	v_mfma_f32_16x16x32_bf16 v[80:83], v[232:235], v[12:15], v[80:83]
	v_cvt_pk_bf16_f32 v208, v64, v65
	v_mfma_f32_16x16x32_bf16 v[76:79], v[236:239], v[12:15], v[76:79]
	v_cvt_pk_bf16_f32 v209, v66, v67
	v_mfma_f32_16x16x32_bf16 v[72:75], v[236:239], v[8:11], v[72:75]
	v_cvt_pk_bf16_f32 v210, v68, v69
	v_mfma_f32_16x16x32_bf16 v[84:87], v[232:235], v[8:11], v[84:87]
	v_cvt_pk_bf16_f32 v211, v70, v71
	ds_read_b128 v[232:235], v121 offset:34816
	ds_read_b128 v[236:239], v121 offset:35840
	s_waitcnt lgkmcnt(6)
	v_mfma_f32_16x16x32_bf16 v[80:83], v[240:243], v[16:19], v[80:83]
	v_cvt_pk_bf16_f32 v212, v56, v57
	v_mfma_f32_16x16x32_bf16 v[76:79], v[244:247], v[16:19], v[76:79]
	v_cvt_pk_bf16_f32 v213, v58, v59
	v_mfma_f32_16x16x32_bf16 v[72:75], v[244:247], v[20:23], v[72:75]
	v_cvt_pk_bf16_f32 v214, v60, v61
	v_mfma_f32_16x16x32_bf16 v[84:87], v[240:243], v[20:23], v[84:87]
	v_cvt_pk_bf16_f32 v215, v62, v63
	ds_read_b128 v[240:243], v121 offset:36864
	ds_read_b128 v[244:247], v121 offset:37888
	s_waitcnt lgkmcnt(6)
	v_mfma_f32_16x16x32_bf16 v[80:83], v[248:251], v[24:27], v[80:83]
	v_pk_max_i16 v208, v208, 0
	v_mfma_f32_16x16x32_bf16 v[76:79], v[252:255], v[24:27], v[76:79]
	v_pk_max_i16 v209, v209, 0
	v_mfma_f32_16x16x32_bf16 v[72:75], v[252:255], v[28:31], v[72:75]
	v_pk_max_i16 v210, v210, 0
	v_mfma_f32_16x16x32_bf16 v[84:87], v[248:251], v[28:31], v[84:87]
	v_pk_max_i16 v211, v211, 0
	ds_read_b128 v[248:251], v121 offset:38912
	ds_read_b128 v[252:255], v121 offset:39936
	s_setprio 0
	s_waitcnt lgkmcnt(6)
	v_mfma_f32_16x16x32_bf16 v[80:83], v[224:227], v[32:35], v[80:83]
	v_pk_max_i16 v212, v212, 0
	v_mfma_f32_16x16x32_bf16 v[76:79], v[228:231], v[32:35], v[76:79]
	v_pk_max_i16 v213, v213, 0
	v_mfma_f32_16x16x32_bf16 v[72:75], v[228:231], v[36:39], v[72:75]
	v_pk_max_i16 v214, v214, 0
	v_mfma_f32_16x16x32_bf16 v[84:87], v[224:227], v[36:39], v[84:87]
	v_pk_max_i16 v215, v215, 0
	s_waitcnt lgkmcnt(4)
	v_mfma_f32_16x16x32_bf16 v[80:83], v[232:235], v[40:43], v[80:83]
	v_mfma_f32_16x16x32_bf16 v[76:79], v[236:239], v[40:43], v[76:79]
	v_mfma_f32_16x16x32_bf16 v[72:75], v[236:239], v[44:47], v[72:75]
	v_mfma_f32_16x16x32_bf16 v[84:87], v[232:235], v[44:47], v[84:87]
	s_cmp_eq_u32 s52, 3
	s_cbranch_scc1 .Lnerf_head
.Lnerf_hid_b4:
	s_waitcnt vmcnt(0) lgkmcnt(0)
	s_barrier
	ds_read_b128 v[224:227], v121 offset:40960
	ds_read_b128 v[228:231], v121 offset:41984
	v_mfma_f32_16x16x32_bf16 v[80:83], v[240:243], v[48:51], v[80:83]
	ds_read_b128 v[232:235], v121 offset:43008
	v_mfma_f32_16x16x32_bf16 v[76:79], v[244:247], v[48:51], v[76:79]
	ds_read_b128 v[236:239], v121 offset:44032
	v_mfma_f32_16x16x32_bf16 v[72:75], v[244:247], v[52:55], v[72:75]
	v_mfma_f32_16x16x32_bf16 v[84:87], v[240:243], v[52:55], v[84:87]
	ds_read_b128 v[240:243], v121 offset:45056
	ds_read_b128 v[244:247], v121 offset:46080
	v_mfma_f32_16x16x32_bf16 v[80:83], v[248:251], v[112:115], v[80:83]
	v_mfma_f32_16x16x32_bf16 v[76:79], v[252:255], v[112:115], v[76:79]
	v_mfma_f32_16x16x32_bf16 v[72:75], v[252:255], v[116:119], v[72:75]
	v_mfma_f32_16x16x32_bf16 v[84:87], v[248:251], v[116:119], v[84:87]
	ds_read_b128 v[248:251], v121 offset:47104
	ds_read_b128 v[252:255], v121 offset:48128
	s_setprio 3
	s_waitcnt lgkmcnt(6)
	v_mfma_f32_16x16x32_bf16 v[64:67], v[224:227], v[88:91], v[152:155]
	v_mfma_f32_16x16x32_bf16 v[68:71], v[228:231], v[88:91], v[156:159]
	v_mfma_f32_16x16x32_bf16 v[60:63], v[228:231], v[92:95], v[156:159]
	v_mfma_f32_16x16x32_bf16 v[56:59], v[224:227], v[92:95], v[152:155]
	ds_read_b128 v[224:227], v121 offset:49152
	ds_read_b128 v[228:231], v121 offset:50176
	s_waitcnt lgkmcnt(6)
	ds_read_b128 v[160:163], v183 offset:1152
	ds_read_b128 v[164:167], v183 offset:1216
	v_mfma_f32_16x16x32_bf16 v[64:67], v[232:235], v[96:99], v[64:67]
	v_cvt_pk_bf16_f32 v216, v80, v81
	v_mfma_f32_16x16x32_bf16 v[68:71], v[236:239], v[96:99], v[68:71]
	v_cvt_pk_bf16_f32 v217, v82, v83
	v_mfma_f32_16x16x32_bf16 v[60:63], v[236:239], v[100:103], v[60:63]
	v_cvt_pk_bf16_f32 v218, v76, v77
	v_mfma_f32_16x16x32_bf16 v[56:59], v[232:235], v[100:103], v[56:59]
	v_cvt_pk_bf16_f32 v219, v78, v79
	ds_read_b128 v[232:235], v121 offset:51200
	ds_read_b128 v[236:239], v121 offset:52224
	s_waitcnt lgkmcnt(8)
	v_mfma_f32_16x16x32_bf16 v[64:67], v[240:243], v[104:107], v[64:67]
	v_cvt_pk_bf16_f32 v220, v84, v85
	v_mfma_f32_16x16x32_bf16 v[68:71], v[244:247], v[104:107], v[68:71]
	v_cvt_pk_bf16_f32 v221, v86, v87
	v_mfma_f32_16x16x32_bf16 v[60:63], v[244:247], v[108:111], v[60:63]
	v_cvt_pk_bf16_f32 v222, v72, v73
	v_mfma_f32_16x16x32_bf16 v[56:59], v[240:243], v[108:111], v[56:59]
	v_cvt_pk_bf16_f32 v223, v74, v75
	ds_read_b128 v[240:243], v121 offset:53248
	ds_read_b128 v[244:247], v121 offset:54272
	s_waitcnt lgkmcnt(8)
	v_mfma_f32_16x16x32_bf16 v[64:67], v[248:251], v[184:187], v[64:67]
	v_pk_max_i16 v216, v216, 0
	v_mfma_f32_16x16x32_bf16 v[68:71], v[252:255], v[184:187], v[68:71]
	v_pk_max_i16 v217, v217, 0
	v_mfma_f32_16x16x32_bf16 v[60:63], v[252:255], v[188:191], v[60:63]
	v_pk_max_i16 v218, v218, 0
	v_mfma_f32_16x16x32_bf16 v[56:59], v[248:251], v[188:191], v[56:59]
	v_pk_max_i16 v219, v219, 0
	ds_read_b128 v[248:251], v121 offset:55296
	ds_read_b128 v[252:255], v121 offset:56320
	s_setprio 2
	s_waitcnt lgkmcnt(8)
	v_mfma_f32_16x16x32_bf16 v[64:67], v[224:227], v[192:195], v[64:67]
	v_pk_max_i16 v220, v220, 0
	v_mfma_f32_16x16x32_bf16 v[68:71], v[228:231], v[192:195], v[68:71]
	v_pk_max_i16 v221, v221, 0
	v_mfma_f32_16x16x32_bf16 v[60:63], v[228:231], v[196:199], v[60:63]
	v_pk_max_i16 v222, v222, 0
	v_mfma_f32_16x16x32_bf16 v[56:59], v[224:227], v[196:199], v[56:59]
	v_pk_max_i16 v223, v223, 0
	ds_read_b128 v[224:227], v121 offset:57344
	ds_read_b128 v[228:231], v121 offset:58368
	s_waitcnt lgkmcnt(6)
	v_mfma_f32_16x16x32_bf16 v[64:67], v[232:235], v[200:203], v[64:67]
	v_mfma_f32_16x16x32_bf16 v[68:71], v[236:239], v[200:203], v[68:71]
	s_mov_b32 m0, s35
	s_add_i32 s51, s50, 0x20000
	v_mfma_f32_16x16x32_bf16 v[60:63], v[236:239], v[204:207], v[60:63]
	buffer_load_dwordx4 v125, s[36:39], s51 offen lds
	v_mfma_f32_16x16x32_bf16 v[56:59], v[232:235], v[204:207], v[56:59]
	ds_read_b128 v[232:235], v121 offset:59392
	ds_read_b128 v[236:239], v121 offset:60416
	s_waitcnt lgkmcnt(6)
	ds_read_b128 v[152:155], v183 offset:1280
	ds_read_b128 v[156:159], v183 offset:1344
	v_mfma_f32_16x16x32_bf16 v[64:67], v[240:243], v[208:211], v[64:67]
	v_mfma_f32_16x16x32_bf16 v[68:71], v[244:247], v[208:211], v[68:71]
	s_mov_b32 m0, s42
	s_add_i32 s51, s50, 0x22000
	v_mfma_f32_16x16x32_bf16 v[60:63], v[244:247], v[212:215], v[60:63]
	buffer_load_dwordx4 v125, s[36:39], s51 offen lds
	v_mfma_f32_16x16x32_bf16 v[56:59], v[240:243], v[212:215], v[56:59]
	ds_read_b128 v[240:243], v121 offset:61440
	ds_read_b128 v[244:247], v121 offset:62464
	s_waitcnt lgkmcnt(8)
	v_mfma_f32_16x16x32_bf16 v[64:67], v[248:251], v[216:219], v[64:67]
	v_mfma_f32_16x16x32_bf16 v[68:71], v[252:255], v[216:219], v[68:71]
	s_mov_b32 m0, s41
	s_add_i32 s51, s50, 0x24000
	v_mfma_f32_16x16x32_bf16 v[60:63], v[252:255], v[220:223], v[60:63]
	buffer_load_dwordx4 v125, s[36:39], s51 offen lds
	v_mfma_f32_16x16x32_bf16 v[56:59], v[248:251], v[220:223], v[56:59]
	ds_read_b128 v[248:251], v121 offset:63488
	ds_read_b128 v[252:255], v121 offset:64512
	s_setprio 1
	s_waitcnt lgkmcnt(8)
	v_mfma_f32_16x16x32_bf16 v[80:83], v[224:227], v[88:91], v[160:163]
	v_mfma_f32_16x16x32_bf16 v[76:79], v[228:231], v[88:91], v[164:167]
	s_mov_b32 m0, s40
	s_add_i32 s51, s50, 0x26000
	v_mfma_f32_16x16x32_bf16 v[72:75], v[228:231], v[92:95], v[164:167]
	buffer_load_dwordx4 v125, s[36:39], s51 offen lds
	v_mfma_f32_16x16x32_bf16 v[84:87], v[224:227], v[92:95], v[160:163]
	ds_read_b128 v[224:227], v126 offset:57344
	ds_read_b128 v[228:231], v126 offset:58368
	s_waitcnt lgkmcnt(8)
	v_mfma_f32_16x16x32_bf16 v[80:83], v[232:235], v[96:99], v[80:83]
	v_cvt_pk_bf16_f32 v0, v64, v65
	v_mfma_f32_16x16x32_bf16 v[76:79], v[236:239], v[96:99], v[76:79]
	v_cvt_pk_bf16_f32 v1, v66, v67
	v_mfma_f32_16x16x32_bf16 v[72:75], v[236:239], v[100:103], v[72:75]
	v_cvt_pk_bf16_f32 v2, v68, v69
	v_mfma_f32_16x16x32_bf16 v[84:87], v[232:235], v[100:103], v[84:87]
	v_cvt_pk_bf16_f32 v3, v70, v71
	ds_read_b128 v[232:235], v126 offset:59392
	ds_read_b128 v[236:239], v126 offset:60416
	s_waitcnt lgkmcnt(6)
	v_mfma_f32_16x16x32_bf16 v[80:83], v[240:243], v[104:107], v[80:83]
	v_cvt_pk_bf16_f32 v4, v56, v57
	v_mfma_f32_16x16x32_bf16 v[76:79], v[244:247], v[104:107], v[76:79]
	v_cvt_pk_bf16_f32 v5, v58, v59
	v_mfma_f32_16x16x32_bf16 v[72:75], v[244:247], v[108:111], v[72:75]
	v_cvt_pk_bf16_f32 v6, v60, v61
	v_mfma_f32_16x16x32_bf16 v[84:87], v[240:243], v[108:111], v[84:87]
	v_cvt_pk_bf16_f32 v7, v62, v63
	ds_read_b128 v[240:243], v126 offset:61440
	ds_read_b128 v[244:247], v126 offset:62464
	s_waitcnt lgkmcnt(6)
	v_mfma_f32_16x16x32_bf16 v[80:83], v[248:251], v[184:187], v[80:83]
	v_pk_max_i16 v0, v0, 0
	v_mfma_f32_16x16x32_bf16 v[76:79], v[252:255], v[184:187], v[76:79]
	v_pk_max_i16 v1, v1, 0
	v_mfma_f32_16x16x32_bf16 v[72:75], v[252:255], v[188:191], v[72:75]
	v_pk_max_i16 v2, v2, 0
	v_mfma_f32_16x16x32_bf16 v[84:87], v[248:251], v[188:191], v[84:87]
	v_pk_max_i16 v3, v3, 0
	ds_read_b128 v[248:251], v126 offset:63488
	ds_read_b128 v[252:255], v126 offset:64512
	s_setprio 0
	s_waitcnt lgkmcnt(6)
	v_mfma_f32_16x16x32_bf16 v[80:83], v[224:227], v[192:195], v[80:83]
	v_pk_max_i16 v4, v4, 0
	v_mfma_f32_16x16x32_bf16 v[76:79], v[228:231], v[192:195], v[76:79]
	v_pk_max_i16 v5, v5, 0
	v_mfma_f32_16x16x32_bf16 v[72:75], v[228:231], v[196:199], v[72:75]
	v_pk_max_i16 v6, v6, 0
	v_mfma_f32_16x16x32_bf16 v[84:87], v[224:227], v[196:199], v[84:87]
	v_pk_max_i16 v7, v7, 0
	s_waitcnt lgkmcnt(4)
	v_mfma_f32_16x16x32_bf16 v[80:83], v[232:235], v[200:203], v[80:83]
	v_mfma_f32_16x16x32_bf16 v[76:79], v[236:239], v[200:203], v[76:79]
	v_mfma_f32_16x16x32_bf16 v[72:75], v[236:239], v[204:207], v[72:75]
	v_mfma_f32_16x16x32_bf16 v[84:87], v[232:235], v[204:207], v[84:87]
.Lnerf_hid_b5:
	s_waitcnt vmcnt(0) lgkmcnt(0)
	s_barrier
	ds_read_b128 v[224:227], v121 offset:8192
	ds_read_b128 v[228:231], v121 offset:9216
	v_mfma_f32_16x16x32_bf16 v[80:83], v[240:243], v[208:211], v[80:83]
	ds_read_b128 v[232:235], v121 offset:10240
	v_mfma_f32_16x16x32_bf16 v[76:79], v[244:247], v[208:211], v[76:79]
	ds_read_b128 v[236:239], v121 offset:11264
	v_mfma_f32_16x16x32_bf16 v[72:75], v[244:247], v[212:215], v[72:75]
	v_mfma_f32_16x16x32_bf16 v[84:87], v[240:243], v[212:215], v[84:87]
	ds_read_b128 v[240:243], v121 offset:12288
	ds_read_b128 v[244:247], v121 offset:13312
	v_mfma_f32_16x16x32_bf16 v[80:83], v[248:251], v[216:219], v[80:83]
	v_mfma_f32_16x16x32_bf16 v[76:79], v[252:255], v[216:219], v[76:79]
	v_mfma_f32_16x16x32_bf16 v[72:75], v[252:255], v[220:223], v[72:75]
	v_mfma_f32_16x16x32_bf16 v[84:87], v[248:251], v[220:223], v[84:87]
	ds_read_b128 v[248:251], v121 offset:14336
	ds_read_b128 v[252:255], v121 offset:15360
	s_setprio 3
	s_waitcnt lgkmcnt(6)
	v_mfma_f32_16x16x32_bf16 v[64:67], v[224:227], v[88:91], v[152:155]
	v_mfma_f32_16x16x32_bf16 v[68:71], v[228:231], v[88:91], v[156:159]
	v_mfma_f32_16x16x32_bf16 v[60:63], v[228:231], v[92:95], v[156:159]
	v_mfma_f32_16x16x32_bf16 v[56:59], v[224:227], v[92:95], v[152:155]
	ds_read_b128 v[224:227], v121 offset:16384
	ds_read_b128 v[228:231], v121 offset:17408
	s_waitcnt lgkmcnt(6)
	ds_read_b128 v[160:163], v183 offset:1408
	ds_read_b128 v[164:167], v183 offset:1472
	v_mfma_f32_16x16x32_bf16 v[64:67], v[232:235], v[96:99], v[64:67]
	v_cvt_pk_bf16_f32 v12, v80, v81
	v_mfma_f32_16x16x32_bf16 v[68:71], v[236:239], v[96:99], v[68:71]
	v_cvt_pk_bf16_f32 v13, v82, v83
	v_mfma_f32_16x16x32_bf16 v[60:63], v[236:239], v[100:103], v[60:63]
	v_cvt_pk_bf16_f32 v14, v76, v77
	v_mfma_f32_16x16x32_bf16 v[56:59], v[232:235], v[100:103], v[56:59]
	v_cvt_pk_bf16_f32 v15, v78, v79
	ds_read_b128 v[232:235], v121 offset:18432
	ds_read_b128 v[236:239], v121 offset:19456
	s_waitcnt lgkmcnt(8)
	v_mfma_f32_16x16x32_bf16 v[64:67], v[240:243], v[104:107], v[64:67]
	v_cvt_pk_bf16_f32 v8, v84, v85
	v_mfma_f32_16x16x32_bf16 v[68:71], v[244:247], v[104:107], v[68:71]
	v_cvt_pk_bf16_f32 v9, v86, v87
	v_mfma_f32_16x16x32_bf16 v[60:63], v[244:247], v[108:111], v[60:63]
	v_cvt_pk_bf16_f32 v10, v72, v73
	v_mfma_f32_16x16x32_bf16 v[56:59], v[240:243], v[108:111], v[56:59]
	v_cvt_pk_bf16_f32 v11, v74, v75
	ds_read_b128 v[240:243], v121 offset:20480
	ds_read_b128 v[244:247], v121 offset:21504
	s_waitcnt lgkmcnt(8)
	v_mfma_f32_16x16x32_bf16 v[64:67], v[248:251], v[184:187], v[64:67]
	v_pk_max_i16 v12, v12, 0
	v_mfma_f32_16x16x32_bf16 v[68:71], v[252:255], v[184:187], v[68:71]
	v_pk_max_i16 v13, v13, 0
	v_mfma_f32_16x16x32_bf16 v[60:63], v[252:255], v[188:191], v[60:63]
	v_pk_max_i16 v14, v14, 0
	v_mfma_f32_16x16x32_bf16 v[56:59], v[248:251], v[188:191], v[56:59]
	v_pk_max_i16 v15, v15, 0
	ds_read_b128 v[248:251], v121 offset:22528
	ds_read_b128 v[252:255], v121 offset:23552
	s_setprio 2
	s_waitcnt lgkmcnt(8)
	v_mfma_f32_16x16x32_bf16 v[64:67], v[224:227], v[192:195], v[64:67]
	v_pk_max_i16 v8, v8, 0
	v_mfma_f32_16x16x32_bf16 v[68:71], v[228:231], v[192:195], v[68:71]
	v_pk_max_i16 v9, v9, 0
	v_mfma_f32_16x16x32_bf16 v[60:63], v[228:231], v[196:199], v[60:63]
	v_pk_max_i16 v10, v10, 0
	v_mfma_f32_16x16x32_bf16 v[56:59], v[224:227], v[196:199], v[56:59]
	v_pk_max_i16 v11, v11, 0
	ds_read_b128 v[224:227], v121 offset:24576
	ds_read_b128 v[228:231], v121 offset:25600
	s_waitcnt lgkmcnt(6)
	v_mfma_f32_16x16x32_bf16 v[64:67], v[232:235], v[200:203], v[64:67]
	v_mfma_f32_16x16x32_bf16 v[68:71], v[236:239], v[200:203], v[68:71]
	s_mov_b32 m0, s28
	s_add_i32 s51, s50, 0x28000
	v_mfma_f32_16x16x32_bf16 v[60:63], v[236:239], v[204:207], v[60:63]
	buffer_load_dwordx4 v125, s[36:39], s51 offen lds
	v_mfma_f32_16x16x32_bf16 v[56:59], v[232:235], v[204:207], v[56:59]
	ds_read_b128 v[232:235], v121 offset:26624
	ds_read_b128 v[236:239], v121 offset:27648
	s_waitcnt lgkmcnt(6)
	ds_read_b128 v[152:155], v183 offset:1536
	ds_read_b128 v[156:159], v183 offset:1600
	v_mfma_f32_16x16x32_bf16 v[64:67], v[240:243], v[208:211], v[64:67]
	v_mfma_f32_16x16x32_bf16 v[68:71], v[244:247], v[208:211], v[68:71]
	s_mov_b32 m0, s29
	s_add_i32 s51, s50, 0x2a000
	v_mfma_f32_16x16x32_bf16 v[60:63], v[244:247], v[212:215], v[60:63]
	buffer_load_dwordx4 v125, s[36:39], s51 offen lds
	v_mfma_f32_16x16x32_bf16 v[56:59], v[240:243], v[212:215], v[56:59]
	ds_read_b128 v[240:243], v121 offset:28672
	ds_read_b128 v[244:247], v121 offset:29696
	s_waitcnt lgkmcnt(8)
	v_mfma_f32_16x16x32_bf16 v[64:67], v[248:251], v[216:219], v[64:67]
	v_mfma_f32_16x16x32_bf16 v[68:71], v[252:255], v[216:219], v[68:71]
	s_mov_b32 m0, s33
	s_add_i32 s51, s50, 0x2c000
	v_mfma_f32_16x16x32_bf16 v[60:63], v[252:255], v[220:223], v[60:63]
	buffer_load_dwordx4 v125, s[36:39], s51 offen lds
	v_mfma_f32_16x16x32_bf16 v[56:59], v[248:251], v[220:223], v[56:59]
	ds_read_b128 v[248:251], v121 offset:30720
	ds_read_b128 v[252:255], v121 offset:31744
	s_setprio 1
	s_waitcnt lgkmcnt(8)
	v_mfma_f32_16x16x32_bf16 v[80:83], v[224:227], v[88:91], v[160:163]
	v_mfma_f32_16x16x32_bf16 v[76:79], v[228:231], v[88:91], v[164:167]
	s_mov_b32 m0, s34
	s_add_i32 s51, s50, 0x2e000
	v_mfma_f32_16x16x32_bf16 v[72:75], v[228:231], v[92:95], v[164:167]
	buffer_load_dwordx4 v125, s[36:39], s51 offen lds
	v_mfma_f32_16x16x32_bf16 v[84:87], v[224:227], v[92:95], v[160:163]
	ds_read_b128 v[224:227], v121 offset:32768
	ds_read_b128 v[228:231], v121 offset:33792
	s_waitcnt lgkmcnt(8)
	v_mfma_f32_16x16x32_bf16 v[80:83], v[232:235], v[96:99], v[80:83]
	v_cvt_pk_bf16_f32 v16, v64, v65
	v_mfma_f32_16x16x32_bf16 v[76:79], v[236:239], v[96:99], v[76:79]
	v_cvt_pk_bf16_f32 v17, v66, v67
	v_mfma_f32_16x16x32_bf16 v[72:75], v[236:239], v[100:103], v[72:75]
	v_cvt_pk_bf16_f32 v18, v68, v69
	v_mfma_f32_16x16x32_bf16 v[84:87], v[232:235], v[100:103], v[84:87]
	v_cvt_pk_bf16_f32 v19, v70, v71
	ds_read_b128 v[232:235], v121 offset:34816
	ds_read_b128 v[236:239], v121 offset:35840
	s_waitcnt lgkmcnt(6)
	v_mfma_f32_16x16x32_bf16 v[80:83], v[240:243], v[104:107], v[80:83]
	v_cvt_pk_bf16_f32 v20, v56, v57
	v_mfma_f32_16x16x32_bf16 v[76:79], v[244:247], v[104:107], v[76:79]
	v_cvt_pk_bf16_f32 v21, v58, v59
	v_mfma_f32_16x16x32_bf16 v[72:75], v[244:247], v[108:111], v[72:75]
	v_cvt_pk_bf16_f32 v22, v60, v61
	v_mfma_f32_16x16x32_bf16 v[84:87], v[240:243], v[108:111], v[84:87]
	v_cvt_pk_bf16_f32 v23, v62, v63
	ds_read_b128 v[240:243], v121 offset:36864
	ds_read_b128 v[244:247], v121 offset:37888
	s_waitcnt lgkmcnt(6)
	v_mfma_f32_16x16x32_bf16 v[80:83], v[248:251], v[184:187], v[80:83]
	v_pk_max_i16 v16, v16, 0
	v_mfma_f32_16x16x32_bf16 v[76:79], v[252:255], v[184:187], v[76:79]
	v_pk_max_i16 v17, v17, 0
	v_mfma_f32_16x16x32_bf16 v[72:75], v[252:255], v[188:191], v[72:75]
	v_pk_max_i16 v18, v18, 0
	v_mfma_f32_16x16x32_bf16 v[84:87], v[248:251], v[188:191], v[84:87]
	v_pk_max_i16 v19, v19, 0
	ds_read_b128 v[248:251], v121 offset:38912
	ds_read_b128 v[252:255], v121 offset:39936
	s_setprio 0
	s_waitcnt lgkmcnt(6)
	v_mfma_f32_16x16x32_bf16 v[80:83], v[224:227], v[192:195], v[80:83]
	v_pk_max_i16 v20, v20, 0
	v_mfma_f32_16x16x32_bf16 v[76:79], v[228:231], v[192:195], v[76:79]
	v_pk_max_i16 v21, v21, 0
	v_mfma_f32_16x16x32_bf16 v[72:75], v[228:231], v[196:199], v[72:75]
	v_pk_max_i16 v22, v22, 0
	v_mfma_f32_16x16x32_bf16 v[84:87], v[224:227], v[196:199], v[84:87]
	v_pk_max_i16 v23, v23, 0
	s_waitcnt lgkmcnt(4)
	v_mfma_f32_16x16x32_bf16 v[80:83], v[232:235], v[200:203], v[80:83]
	v_mfma_f32_16x16x32_bf16 v[76:79], v[236:239], v[200:203], v[76:79]
	v_mfma_f32_16x16x32_bf16 v[72:75], v[236:239], v[204:207], v[72:75]
	v_mfma_f32_16x16x32_bf16 v[84:87], v[232:235], v[204:207], v[84:87]
.Lnerf_hid_b6:
	s_waitcnt vmcnt(0) lgkmcnt(0)
	s_barrier
	ds_read_b128 v[224:227], v121 offset:40960
	ds_read_b128 v[228:231], v121 offset:41984
	v_mfma_f32_16x16x32_bf16 v[80:83], v[240:243], v[208:211], v[80:83]
	ds_read_b128 v[232:235], v121 offset:43008
	v_mfma_f32_16x16x32_bf16 v[76:79], v[244:247], v[208:211], v[76:79]
	ds_read_b128 v[236:239], v121 offset:44032
	v_mfma_f32_16x16x32_bf16 v[72:75], v[244:247], v[212:215], v[72:75]
	v_mfma_f32_16x16x32_bf16 v[84:87], v[240:243], v[212:215], v[84:87]
	ds_read_b128 v[240:243], v121 offset:45056
	ds_read_b128 v[244:247], v121 offset:46080
	v_mfma_f32_16x16x32_bf16 v[80:83], v[248:251], v[216:219], v[80:83]
	v_mfma_f32_16x16x32_bf16 v[76:79], v[252:255], v[216:219], v[76:79]
	v_mfma_f32_16x16x32_bf16 v[72:75], v[252:255], v[220:223], v[72:75]
	v_mfma_f32_16x16x32_bf16 v[84:87], v[248:251], v[220:223], v[84:87]
	ds_read_b128 v[248:251], v121 offset:47104
	ds_read_b128 v[252:255], v121 offset:48128
	s_setprio 3
	s_waitcnt lgkmcnt(6)
	v_mfma_f32_16x16x32_bf16 v[64:67], v[224:227], v[88:91], v[152:155]
	v_mfma_f32_16x16x32_bf16 v[68:71], v[228:231], v[88:91], v[156:159]
	v_mfma_f32_16x16x32_bf16 v[60:63], v[228:231], v[92:95], v[156:159]
	v_mfma_f32_16x16x32_bf16 v[56:59], v[224:227], v[92:95], v[152:155]
	ds_read_b128 v[224:227], v121 offset:49152
	ds_read_b128 v[228:231], v121 offset:50176
	s_waitcnt lgkmcnt(6)
	ds_read_b128 v[160:163], v183 offset:1664
	ds_read_b128 v[164:167], v183 offset:1728
	v_mfma_f32_16x16x32_bf16 v[64:67], v[232:235], v[96:99], v[64:67]
	v_cvt_pk_bf16_f32 v24, v80, v81
	v_mfma_f32_16x16x32_bf16 v[68:71], v[236:239], v[96:99], v[68:71]
	v_cvt_pk_bf16_f32 v25, v82, v83
	v_mfma_f32_16x16x32_bf16 v[60:63], v[236:239], v[100:103], v[60:63]
	v_cvt_pk_bf16_f32 v26, v76, v77
	v_mfma_f32_16x16x32_bf16 v[56:59], v[232:235], v[100:103], v[56:59]
	v_cvt_pk_bf16_f32 v27, v78, v79
	ds_read_b128 v[232:235], v121 offset:51200
	ds_read_b128 v[236:239], v121 offset:52224
	s_waitcnt lgkmcnt(8)
	v_mfma_f32_16x16x32_bf16 v[64:67], v[240:243], v[104:107], v[64:67]
	v_cvt_pk_bf16_f32 v28, v84, v85
	v_mfma_f32_16x16x32_bf16 v[68:71], v[244:247], v[104:107], v[68:71]
	v_cvt_pk_bf16_f32 v29, v86, v87
	v_mfma_f32_16x16x32_bf16 v[60:63], v[244:247], v[108:111], v[60:63]
	v_cvt_pk_bf16_f32 v30, v72, v73
	v_mfma_f32_16x16x32_bf16 v[56:59], v[240:243], v[108:111], v[56:59]
	v_cvt_pk_bf16_f32 v31, v74, v75
	ds_read_b128 v[240:243], v121 offset:53248
	ds_read_b128 v[244:247], v121 offset:54272
	s_waitcnt lgkmcnt(8)
	v_mfma_f32_16x16x32_bf16 v[64:67], v[248:251], v[184:187], v[64:67]
	v_pk_max_i16 v24, v24, 0
	v_mfma_f32_16x16x32_bf16 v[68:71], v[252:255], v[184:187], v[68:71]
	v_pk_max_i16 v25, v25, 0
	v_mfma_f32_16x16x32_bf16 v[60:63], v[252:255], v[188:191], v[60:63]
	v_pk_max_i16 v26, v26, 0
	v_mfma_f32_16x16x32_bf16 v[56:59], v[248:251], v[188:191], v[56:59]
	v_pk_max_i16 v27, v27, 0
	ds_read_b128 v[248:251], v121 offset:55296
	ds_read_b128 v[252:255], v121 offset:56320
	s_setprio 2
	s_waitcnt lgkmcnt(8)
	v_mfma_f32_16x16x32_bf16 v[64:67], v[224:227], v[192:195], v[64:67]
	v_pk_max_i16 v28, v28, 0
	v_mfma_f32_16x16x32_bf16 v[68:71], v[228:231], v[192:195], v[68:71]
	v_pk_max_i16 v29, v29, 0
	v_mfma_f32_16x16x32_bf16 v[60:63], v[228:231], v[196:199], v[60:63]
	v_pk_max_i16 v30, v30, 0
	v_mfma_f32_16x16x32_bf16 v[56:59], v[224:227], v[196:199], v[56:59]
	v_pk_max_i16 v31, v31, 0
	ds_read_b128 v[224:227], v121 offset:57344
	ds_read_b128 v[228:231], v121 offset:58368
	s_waitcnt lgkmcnt(6)
	v_mfma_f32_16x16x32_bf16 v[64:67], v[232:235], v[200:203], v[64:67]
	v_mfma_f32_16x16x32_bf16 v[68:71], v[236:239], v[200:203], v[68:71]
	s_mov_b32 m0, s35
	s_add_i32 s51, s50, 0x30000
	v_mfma_f32_16x16x32_bf16 v[60:63], v[236:239], v[204:207], v[60:63]
	buffer_load_dwordx4 v125, s[36:39], s51 offen lds
	v_mfma_f32_16x16x32_bf16 v[56:59], v[232:235], v[204:207], v[56:59]
	ds_read_b128 v[232:235], v121 offset:59392
	ds_read_b128 v[236:239], v121 offset:60416
	s_waitcnt lgkmcnt(6)
	ds_read_b128 v[152:155], v183 offset:1792
	ds_read_b128 v[156:159], v183 offset:1856
	v_mfma_f32_16x16x32_bf16 v[64:67], v[240:243], v[208:211], v[64:67]
	v_mfma_f32_16x16x32_bf16 v[68:71], v[244:247], v[208:211], v[68:71]
	s_mov_b32 m0, s42
	s_add_i32 s51, s50, 0x32000
	v_mfma_f32_16x16x32_bf16 v[60:63], v[244:247], v[212:215], v[60:63]
	buffer_load_dwordx4 v125, s[36:39], s51 offen lds
	v_mfma_f32_16x16x32_bf16 v[56:59], v[240:243], v[212:215], v[56:59]
	ds_read_b128 v[240:243], v121 offset:61440
	ds_read_b128 v[244:247], v121 offset:62464
	s_waitcnt lgkmcnt(8)
	v_mfma_f32_16x16x32_bf16 v[64:67], v[248:251], v[216:219], v[64:67]
	v_mfma_f32_16x16x32_bf16 v[68:71], v[252:255], v[216:219], v[68:71]
	s_mov_b32 m0, s41
	s_add_i32 s51, s50, 0x34000
	v_mfma_f32_16x16x32_bf16 v[60:63], v[252:255], v[220:223], v[60:63]
	buffer_load_dwordx4 v125, s[36:39], s51 offen lds
	v_mfma_f32_16x16x32_bf16 v[56:59], v[248:251], v[220:223], v[56:59]
	ds_read_b128 v[248:251], v121 offset:63488
	ds_read_b128 v[252:255], v121 offset:64512
	s_setprio 1
	s_waitcnt lgkmcnt(8)
	v_mfma_f32_16x16x32_bf16 v[80:83], v[224:227], v[88:91], v[160:163]
	v_mfma_f32_16x16x32_bf16 v[76:79], v[228:231], v[88:91], v[164:167]
	s_mov_b32 m0, s40
	s_add_i32 s51, s50, 0x36000
	v_mfma_f32_16x16x32_bf16 v[72:75], v[228:231], v[92:95], v[164:167]
	buffer_load_dwordx4 v125, s[36:39], s51 offen lds
	v_mfma_f32_16x16x32_bf16 v[84:87], v[224:227], v[92:95], v[160:163]
	ds_read_b128 v[224:227], v126 offset:57344
	ds_read_b128 v[228:231], v126 offset:58368
	s_waitcnt lgkmcnt(8)
	v_mfma_f32_16x16x32_bf16 v[80:83], v[232:235], v[96:99], v[80:83]
	v_cvt_pk_bf16_f32 v32, v64, v65
	v_mfma_f32_16x16x32_bf16 v[76:79], v[236:239], v[96:99], v[76:79]
	v_cvt_pk_bf16_f32 v33, v66, v67
	v_mfma_f32_16x16x32_bf16 v[72:75], v[236:239], v[100:103], v[72:75]
	v_cvt_pk_bf16_f32 v34, v68, v69
	v_mfma_f32_16x16x32_bf16 v[84:87], v[232:235], v[100:103], v[84:87]
	v_cvt_pk_bf16_f32 v35, v70, v71
	ds_read_b128 v[232:235], v126 offset:59392
	ds_read_b128 v[236:239], v126 offset:60416
	s_waitcnt lgkmcnt(6)
	v_mfma_f32_16x16x32_bf16 v[80:83], v[240:243], v[104:107], v[80:83]
	v_cvt_pk_bf16_f32 v36, v56, v57
	v_mfma_f32_16x16x32_bf16 v[76:79], v[244:247], v[104:107], v[76:79]
	v_cvt_pk_bf16_f32 v37, v58, v59
	v_mfma_f32_16x16x32_bf16 v[72:75], v[244:247], v[108:111], v[72:75]
	v_cvt_pk_bf16_f32 v38, v60, v61
	v_mfma_f32_16x16x32_bf16 v[84:87], v[240:243], v[108:111], v[84:87]
	v_cvt_pk_bf16_f32 v39, v62, v63
	ds_read_b128 v[240:243], v126 offset:61440
	ds_read_b128 v[244:247], v126 offset:62464
	s_waitcnt lgkmcnt(6)
	v_mfma_f32_16x16x32_bf16 v[80:83], v[248:251], v[184:187], v[80:83]
	v_pk_max_i16 v32, v32, 0
	v_mfma_f32_16x16x32_bf16 v[76:79], v[252:255], v[184:187], v[76:79]
	v_pk_max_i16 v33, v33, 0
	v_mfma_f32_16x16x32_bf16 v[72:75], v[252:255], v[188:191], v[72:75]
	v_pk_max_i16 v34, v34, 0
	v_mfma_f32_16x16x32_bf16 v[84:87], v[248:251], v[188:191], v[84:87]
	v_pk_max_i16 v35, v35, 0
	ds_read_b128 v[248:251], v126 offset:63488
	ds_read_b128 v[252:255], v126 offset:64512
	s_setprio 0
	s_waitcnt lgkmcnt(6)
	v_mfma_f32_16x16x32_bf16 v[80:83], v[224:227], v[192:195], v[80:83]
	v_pk_max_i16 v36, v36, 0
	v_mfma_f32_16x16x32_bf16 v[76:79], v[228:231], v[192:195], v[76:79]
	v_pk_max_i16 v37, v37, 0
	v_mfma_f32_16x16x32_bf16 v[72:75], v[228:231], v[196:199], v[72:75]
	v_pk_max_i16 v38, v38, 0
	v_mfma_f32_16x16x32_bf16 v[84:87], v[224:227], v[196:199], v[84:87]
	v_pk_max_i16 v39, v39, 0
	s_waitcnt lgkmcnt(4)
	v_mfma_f32_16x16x32_bf16 v[80:83], v[232:235], v[200:203], v[80:83]
	v_mfma_f32_16x16x32_bf16 v[76:79], v[236:239], v[200:203], v[76:79]
	v_mfma_f32_16x16x32_bf16 v[72:75], v[236:239], v[204:207], v[72:75]
	v_mfma_f32_16x16x32_bf16 v[84:87], v[232:235], v[204:207], v[84:87]
.Lnerf_hid_b7:
	s_waitcnt vmcnt(0) lgkmcnt(0)
	s_barrier
	ds_read_b128 v[224:227], v121 offset:8192
	ds_read_b128 v[228:231], v121 offset:9216
	v_mfma_f32_16x16x32_bf16 v[80:83], v[240:243], v[208:211], v[80:83]
	ds_read_b128 v[232:235], v121 offset:10240
	v_mfma_f32_16x16x32_bf16 v[76:79], v[244:247], v[208:211], v[76:79]
	ds_read_b128 v[236:239], v121 offset:11264
	v_mfma_f32_16x16x32_bf16 v[72:75], v[244:247], v[212:215], v[72:75]
	v_mfma_f32_16x16x32_bf16 v[84:87], v[240:243], v[212:215], v[84:87]
	ds_read_b128 v[240:243], v121 offset:12288
	ds_read_b128 v[244:247], v121 offset:13312
	v_mfma_f32_16x16x32_bf16 v[80:83], v[248:251], v[216:219], v[80:83]
	v_mfma_f32_16x16x32_bf16 v[76:79], v[252:255], v[216:219], v[76:79]
	v_mfma_f32_16x16x32_bf16 v[72:75], v[252:255], v[220:223], v[72:75]
	v_mfma_f32_16x16x32_bf16 v[84:87], v[248:251], v[220:223], v[84:87]
	ds_read_b128 v[248:251], v121 offset:14336
	ds_read_b128 v[252:255], v121 offset:15360
	s_setprio 3
	s_waitcnt lgkmcnt(6)
	v_mfma_f32_16x16x32_bf16 v[64:67], v[224:227], v[88:91], v[152:155]
	v_mfma_f32_16x16x32_bf16 v[68:71], v[228:231], v[88:91], v[156:159]
	v_mfma_f32_16x16x32_bf16 v[60:63], v[228:231], v[92:95], v[156:159]
	v_mfma_f32_16x16x32_bf16 v[56:59], v[224:227], v[92:95], v[152:155]
	ds_read_b128 v[224:227], v121 offset:16384
	ds_read_b128 v[228:231], v121 offset:17408
	s_waitcnt lgkmcnt(6)
	ds_read_b128 v[160:163], v183 offset:1920
	ds_read_b128 v[164:167], v183 offset:1984
	v_mfma_f32_16x16x32_bf16 v[64:67], v[232:235], v[96:99], v[64:67]
	v_cvt_pk_bf16_f32 v40, v80, v81
	v_mfma_f32_16x16x32_bf16 v[68:71], v[236:239], v[96:99], v[68:71]
	v_cvt_pk_bf16_f32 v41, v82, v83
	v_mfma_f32_16x16x32_bf16 v[60:63], v[236:239], v[100:103], v[60:63]
	v_cvt_pk_bf16_f32 v42, v76, v77
	v_mfma_f32_16x16x32_bf16 v[56:59], v[232:235], v[100:103], v[56:59]
	v_cvt_pk_bf16_f32 v43, v78, v79
	ds_read_b128 v[232:235], v121 offset:18432
	ds_read_b128 v[236:239], v121 offset:19456
	s_waitcnt lgkmcnt(8)
	v_mfma_f32_16x16x32_bf16 v[64:67], v[240:243], v[104:107], v[64:67]
	v_cvt_pk_bf16_f32 v44, v84, v85
	v_mfma_f32_16x16x32_bf16 v[68:71], v[244:247], v[104:107], v[68:71]
	v_cvt_pk_bf16_f32 v45, v86, v87
	v_mfma_f32_16x16x32_bf16 v[60:63], v[244:247], v[108:111], v[60:63]
	v_cvt_pk_bf16_f32 v46, v72, v73
	v_mfma_f32_16x16x32_bf16 v[56:59], v[240:243], v[108:111], v[56:59]
	v_cvt_pk_bf16_f32 v47, v74, v75
	ds_read_b128 v[240:243], v121 offset:20480
	ds_read_b128 v[244:247], v121 offset:21504
	s_waitcnt lgkmcnt(8)
	v_mfma_f32_16x16x32_bf16 v[64:67], v[248:251], v[184:187], v[64:67]
	v_pk_max_i16 v40, v40, 0
	v_mfma_f32_16x16x32_bf16 v[68:71], v[252:255], v[184:187], v[68:71]
	v_pk_max_i16 v41, v41, 0
	v_mfma_f32_16x16x32_bf16 v[60:63], v[252:255], v[188:191], v[60:63]
	v_pk_max_i16 v42, v42, 0
	v_mfma_f32_16x16x32_bf16 v[56:59], v[248:251], v[188:191], v[56:59]
	v_pk_max_i16 v43, v43, 0
	ds_read_b128 v[248:251], v121 offset:22528
	ds_read_b128 v[252:255], v121 offset:23552
	s_setprio 2
	s_waitcnt lgkmcnt(8)
	v_mfma_f32_16x16x32_bf16 v[64:67], v[224:227], v[192:195], v[64:67]
	v_pk_max_i16 v44, v44, 0
	v_mfma_f32_16x16x32_bf16 v[68:71], v[228:231], v[192:195], v[68:71]
	v_pk_max_i16 v45, v45, 0
	v_mfma_f32_16x16x32_bf16 v[60:63], v[228:231], v[196:199], v[60:63]
	v_pk_max_i16 v46, v46, 0
	v_mfma_f32_16x16x32_bf16 v[56:59], v[224:227], v[196:199], v[56:59]
	v_pk_max_i16 v47, v47, 0
	ds_read_b128 v[224:227], v121 offset:24576
	ds_read_b128 v[228:231], v121 offset:25600
	s_waitcnt lgkmcnt(6)
	v_mfma_f32_16x16x32_bf16 v[64:67], v[232:235], v[200:203], v[64:67]
	v_mfma_f32_16x16x32_bf16 v[68:71], v[236:239], v[200:203], v[68:71]
	s_mov_b32 m0, s28
	s_add_i32 s51, s50, 0x38000
	v_mfma_f32_16x16x32_bf16 v[60:63], v[236:239], v[204:207], v[60:63]
	buffer_load_dwordx4 v125, s[36:39], s51 offen lds
	v_mfma_f32_16x16x32_bf16 v[56:59], v[232:235], v[204:207], v[56:59]
	ds_read_b128 v[232:235], v121 offset:26624
	ds_read_b128 v[236:239], v121 offset:27648
	s_waitcnt lgkmcnt(6)
	ds_read_b128 v[152:155], v183 offset:2048
	ds_read_b128 v[156:159], v183 offset:2112
	v_mfma_f32_16x16x32_bf16 v[64:67], v[240:243], v[208:211], v[64:67]
	v_mfma_f32_16x16x32_bf16 v[68:71], v[244:247], v[208:211], v[68:71]
	s_mov_b32 m0, s29
	s_add_i32 s51, s50, 0x3a000
	v_mfma_f32_16x16x32_bf16 v[60:63], v[244:247], v[212:215], v[60:63]
	buffer_load_dwordx4 v125, s[36:39], s51 offen lds
	v_mfma_f32_16x16x32_bf16 v[56:59], v[240:243], v[212:215], v[56:59]
	ds_read_b128 v[240:243], v121 offset:28672
	ds_read_b128 v[244:247], v121 offset:29696
	s_waitcnt lgkmcnt(8)
	v_mfma_f32_16x16x32_bf16 v[64:67], v[248:251], v[216:219], v[64:67]
	v_mfma_f32_16x16x32_bf16 v[68:71], v[252:255], v[216:219], v[68:71]
	s_mov_b32 m0, s33
	s_add_i32 s51, s50, 0x3c000
	v_mfma_f32_16x16x32_bf16 v[60:63], v[252:255], v[220:223], v[60:63]
	buffer_load_dwordx4 v125, s[36:39], s51 offen lds
	v_mfma_f32_16x16x32_bf16 v[56:59], v[248:251], v[220:223], v[56:59]
	ds_read_b128 v[248:251], v121 offset:30720
	ds_read_b128 v[252:255], v121 offset:31744
	s_setprio 1
	s_waitcnt lgkmcnt(8)
	v_mfma_f32_16x16x32_bf16 v[80:83], v[224:227], v[88:91], v[160:163]
	v_mfma_f32_16x16x32_bf16 v[76:79], v[228:231], v[88:91], v[164:167]
	s_mov_b32 m0, s34
	s_add_i32 s51, s50, 0x3e000
	v_mfma_f32_16x16x32_bf16 v[72:75], v[228:231], v[92:95], v[164:167]
	buffer_load_dwordx4 v125, s[36:39], s51 offen lds
	v_mfma_f32_16x16x32_bf16 v[84:87], v[224:227], v[92:95], v[160:163]
	ds_read_b128 v[224:227], v121 offset:32768
	ds_read_b128 v[228:231], v121 offset:33792
	s_waitcnt lgkmcnt(8)
	v_mfma_f32_16x16x32_bf16 v[80:83], v[232:235], v[96:99], v[80:83]
	v_cvt_pk_bf16_f32 v48, v64, v65
	v_mfma_f32_16x16x32_bf16 v[76:79], v[236:239], v[96:99], v[76:79]
	v_cvt_pk_bf16_f32 v49, v66, v67
	v_mfma_f32_16x16x32_bf16 v[72:75], v[236:239], v[100:103], v[72:75]
	v_cvt_pk_bf16_f32 v50, v68, v69
	v_mfma_f32_16x16x32_bf16 v[84:87], v[232:235], v[100:103], v[84:87]
	v_cvt_pk_bf16_f32 v51, v70, v71
	ds_read_b128 v[232:235], v121 offset:34816
	ds_read_b128 v[236:239], v121 offset:35840
	s_waitcnt lgkmcnt(6)
	v_mfma_f32_16x16x32_bf16 v[80:83], v[240:243], v[104:107], v[80:83]
	v_cvt_pk_bf16_f32 v52, v56, v57
	v_mfma_f32_16x16x32_bf16 v[76:79], v[244:247], v[104:107], v[76:79]
	v_cvt_pk_bf16_f32 v53, v58, v59
	v_mfma_f32_16x16x32_bf16 v[72:75], v[244:247], v[108:111], v[72:75]
	v_cvt_pk_bf16_f32 v54, v60, v61
	v_mfma_f32_16x16x32_bf16 v[84:87], v[240:243], v[108:111], v[84:87]
	v_cvt_pk_bf16_f32 v55, v62, v63
	ds_read_b128 v[240:243], v121 offset:36864
	ds_read_b128 v[244:247], v121 offset:37888
	s_waitcnt lgkmcnt(6)
	v_mfma_f32_16x16x32_bf16 v[80:83], v[248:251], v[184:187], v[80:83]
	v_pk_max_i16 v48, v48, 0
	v_mfma_f32_16x16x32_bf16 v[76:79], v[252:255], v[184:187], v[76:79]
	v_pk_max_i16 v49, v49, 0
	v_mfma_f32_16x16x32_bf16 v[72:75], v[252:255], v[188:191], v[72:75]
	v_pk_max_i16 v50, v50, 0
	v_mfma_f32_16x16x32_bf16 v[84:87], v[248:251], v[188:191], v[84:87]
	v_pk_max_i16 v51, v51, 0
	ds_read_b128 v[248:251], v121 offset:38912
	ds_read_b128 v[252:255], v121 offset:39936
	s_setprio 0
	s_waitcnt lgkmcnt(6)
	v_mfma_f32_16x16x32_bf16 v[80:83], v[224:227], v[192:195], v[80:83]
	v_pk_max_i16 v52, v52, 0
	v_mfma_f32_16x16x32_bf16 v[76:79], v[228:231], v[192:195], v[76:79]
	v_pk_max_i16 v53, v53, 0
	v_mfma_f32_16x16x32_bf16 v[72:75], v[228:231], v[196:199], v[72:75]
	v_pk_max_i16 v54, v54, 0
	v_mfma_f32_16x16x32_bf16 v[84:87], v[224:227], v[196:199], v[84:87]
	v_pk_max_i16 v55, v55, 0
	s_waitcnt lgkmcnt(4)
	v_mfma_f32_16x16x32_bf16 v[80:83], v[232:235], v[200:203], v[80:83]
	v_mfma_f32_16x16x32_bf16 v[76:79], v[236:239], v[200:203], v[76:79]
	v_mfma_f32_16x16x32_bf16 v[72:75], v[236:239], v[204:207], v[72:75]
	v_mfma_f32_16x16x32_bf16 v[84:87], v[232:235], v[204:207], v[84:87]
	s_add_i32 s50, s50, 0x40000
	v_add_u32_e32 v183, 0x800, v183
	s_add_i32 s52, s52, 1
	s_branch .Lnerf_hid_b0
